# speedup vs baseline: 1.0115x; 1.0045x over previous
.LBB6_9:
	s_mov_b32 s60, s14
	s_mov_b32 s61, s15
	s_mov_b32 s24, s60
	s_mov_b32 s25, s61
	s_load_dwordx2 s[28:29], s[0:1], 0x58
	s_load_dwordx2 s[30:31], s[0:1], 0x68
	s_load_dwordx2 s[32:33], s[0:1], 0x78
	v_and_b32_e32 v66, 63, v0
	v_lshrrev_b32_e32 v67, 6, v0
	v_and_b32_e32 v68, 15, v0
	v_bfe_u32 v69, v0, 4, 2
	v_mul_u32_u24_e32 v70, 0x2000, v67
	s_movk_i32 s2, 0x440
	v_mad_u32_u24 v71, v69, s2, v70
	v_lshl_add_u32 v71, v68, 2, v71
	v_lshrrev_b32_e32 v72, 4, v66
	s_movk_i32 s3, 0x110
	v_mad_u32_u24 v78, v72, s3, v70
	v_lshl_add_u32 v78, v68, 4, v78
	v_lshrrev_b32_e32 v73, 1, v67
	v_lshl_add_u32 v79, v73, 6, v72
	v_and_b32_e32 v73, 1, v67
	v_lshlrev_b32_e32 v73, 8, v73
	v_lshl_add_u32 v73, v79, 11, v73
	v_lshl_add_u32 v73, v68, 4, v73
	v_and_b32_e32 v72, 0x4f, v0
	v_lshlrev_b32_e32 v72, 2, v72
	s_waitcnt lgkmcnt(0)
	s_lshl_b32 s2, s25, 2
	s_add_u32 s28, s28, s2
	s_addc_u32 s29, s29, 0
	global_load_dword v74, v72, s[28:29]
	global_load_dword v75, v72, s[28:29] offset:64
	global_load_dword v76, v72, s[28:29] offset:128
	global_load_dword v77, v72, s[28:29] offset:192
	s_lshl_b32 s2, s24, 11
	s_lshl_b32 s3, s25, 2
	s_add_u32 s2, s2, s3
	s_add_u32 s34, s30, s2
	s_addc_u32 s35, s31, 0
	s_add_u32 s36, s32, s2
	s_addc_u32 s37, s33, 0
	s_mov_b32 s38, s34
	s_addc_u32 s39, s35, 0
	global_load_dwordx4 v[100:103], v73, s[38:39]
	s_add_u32 s38, s34, 0x2000
	s_addc_u32 s39, s35, 0
	global_load_dwordx4 v[104:107], v73, s[38:39]
	s_add_u32 s38, s34, 0x4000
	s_addc_u32 s39, s35, 0
	global_load_dwordx4 v[108:111], v73, s[38:39]
	s_add_u32 s38, s34, 0x6000
	s_addc_u32 s39, s35, 0
	global_load_dwordx4 v[112:115], v73, s[38:39]
	s_add_u32 s38, s34, 0x8000
	s_addc_u32 s39, s35, 0
	global_load_dwordx4 v[116:119], v73, s[38:39]
	s_add_u32 s38, s34, 0xa000
	s_addc_u32 s39, s35, 0
	global_load_dwordx4 v[120:123], v73, s[38:39]
	s_add_u32 s38, s34, 0xc000
	s_addc_u32 s39, s35, 0
	global_load_dwordx4 v[124:127], v73, s[38:39]
	s_add_u32 s38, s34, 0xe000
	s_addc_u32 s39, s35, 0
	global_load_dwordx4 v[128:131], v73, s[38:39]
	s_add_u32 s38, s34, 0x10000
	s_addc_u32 s39, s35, 0
	global_load_dwordx4 v[132:135], v73, s[38:39]
	s_add_u32 s38, s34, 0x12000
	s_addc_u32 s39, s35, 0
	global_load_dwordx4 v[136:139], v73, s[38:39]
	s_add_u32 s38, s34, 0x14000
	s_addc_u32 s39, s35, 0
	global_load_dwordx4 v[140:143], v73, s[38:39]
	s_add_u32 s38, s34, 0x16000
	s_addc_u32 s39, s35, 0
	global_load_dwordx4 v[144:147], v73, s[38:39]
	s_add_u32 s38, s34, 0x18000
	s_addc_u32 s39, s35, 0
	global_load_dwordx4 v[148:151], v73, s[38:39]
	s_add_u32 s38, s34, 0x1a000
	s_addc_u32 s39, s35, 0
	global_load_dwordx4 v[152:155], v73, s[38:39]
	s_add_u32 s38, s34, 0x1c000
	s_addc_u32 s39, s35, 0
	global_load_dwordx4 v[156:159], v73, s[38:39]
	s_add_u32 s38, s34, 0x1e000
	s_addc_u32 s39, s35, 0
	global_load_dwordx4 v[160:163], v73, s[38:39]
	s_waitcnt vmcnt(16)
	v_fmamk_f32 v62, v62, 0x35800000, v74
	v_fmamk_f32 v63, v63, 0x35800000, v74
	v_fmamk_f32 v64, v64, 0x35800000, v74
	v_fmamk_f32 v65, v65, 0x35800000, v74
	v_fmamk_f32 v58, v58, 0x35800000, v75
	v_fmamk_f32 v59, v59, 0x35800000, v75
	v_fmamk_f32 v60, v60, 0x35800000, v75
	v_fmamk_f32 v61, v61, 0x35800000, v75
	v_fmamk_f32 v54, v54, 0x35800000, v76
	v_fmamk_f32 v55, v55, 0x35800000, v76
	v_fmamk_f32 v56, v56, 0x35800000, v76
	v_fmamk_f32 v57, v57, 0x35800000, v76
	v_fmamk_f32 v50, v50, 0x35800000, v77
	v_fmamk_f32 v51, v51, 0x35800000, v77
	v_fmamk_f32 v52, v52, 0x35800000, v77
	v_fmamk_f32 v53, v53, 0x35800000, v77
	ds_write_b32 v71, v62
	ds_write_b32 v71, v63 offset:272
	ds_write_b32 v71, v64 offset:544
	ds_write_b32 v71, v65 offset:816
	ds_write_b32 v71, v58 offset:64
	ds_write_b32 v71, v59 offset:336
	ds_write_b32 v71, v60 offset:608
	ds_write_b32 v71, v61 offset:880
	ds_write_b32 v71, v54 offset:128
	ds_write_b32 v71, v55 offset:400
	ds_write_b32 v71, v56 offset:672
	ds_write_b32 v71, v57 offset:944
	ds_write_b32 v71, v50 offset:192
	ds_write_b32 v71, v51 offset:464
	ds_write_b32 v71, v52 offset:736
	ds_write_b32 v71, v53 offset:1008
	ds_read_b128 v[164:167], v78
	ds_read_b128 v[168:171], v78 offset:1088
	ds_read_b128 v[172:175], v78 offset:2176
	ds_read_b128 v[176:179], v78 offset:3264
	s_waitcnt lgkmcnt(0)
	s_waitcnt vmcnt(15)
	v_add_f32_e32 v164, v100, v164
	v_add_f32_e32 v165, v101, v165
	v_add_f32_e32 v166, v102, v166
	v_add_f32_e32 v167, v103, v167
	s_mov_b32 s38, s36
	s_addc_u32 s39, s37, 0
	global_store_dwordx4 v73, v[164:167], s[38:39]
	s_waitcnt vmcnt(15)
	v_add_f32_e32 v168, v104, v168
	v_add_f32_e32 v169, v105, v169
	v_add_f32_e32 v170, v106, v170
	v_add_f32_e32 v171, v107, v171
	s_add_u32 s38, s36, 0x2000
	s_addc_u32 s39, s37, 0
	global_store_dwordx4 v73, v[168:171], s[38:39]
	s_waitcnt vmcnt(15)
	v_add_f32_e32 v172, v108, v172
	v_add_f32_e32 v173, v109, v173
	v_add_f32_e32 v174, v110, v174
	v_add_f32_e32 v175, v111, v175
	s_add_u32 s38, s36, 0x4000
	s_addc_u32 s39, s37, 0
	global_store_dwordx4 v73, v[172:175], s[38:39]
	s_waitcnt vmcnt(15)
	v_add_f32_e32 v176, v112, v176
	v_add_f32_e32 v177, v113, v177
	v_add_f32_e32 v178, v114, v178
	v_add_f32_e32 v179, v115, v179
	s_add_u32 s38, s36, 0x6000
	s_addc_u32 s39, s37, 0
	global_store_dwordx4 v73, v[176:179], s[38:39]
	v_fmamk_f32 v46, v46, 0x35800000, v74
	v_fmamk_f32 v47, v47, 0x35800000, v74
	v_fmamk_f32 v48, v48, 0x35800000, v74
	v_fmamk_f32 v49, v49, 0x35800000, v74
	v_fmamk_f32 v42, v42, 0x35800000, v75
	v_fmamk_f32 v43, v43, 0x35800000, v75
	v_fmamk_f32 v44, v44, 0x35800000, v75
	v_fmamk_f32 v45, v45, 0x35800000, v75
	v_fmamk_f32 v38, v38, 0x35800000, v76
	v_fmamk_f32 v39, v39, 0x35800000, v76
	v_fmamk_f32 v40, v40, 0x35800000, v76
	v_fmamk_f32 v41, v41, 0x35800000, v76
	v_fmamk_f32 v34, v34, 0x35800000, v77
	v_fmamk_f32 v35, v35, 0x35800000, v77
	v_fmamk_f32 v36, v36, 0x35800000, v77
	v_fmamk_f32 v37, v37, 0x35800000, v77
	ds_write_b32 v71, v46
	ds_write_b32 v71, v47 offset:272
	ds_write_b32 v71, v48 offset:544
	ds_write_b32 v71, v49 offset:816
	ds_write_b32 v71, v42 offset:64
	ds_write_b32 v71, v43 offset:336
	ds_write_b32 v71, v44 offset:608
	ds_write_b32 v71, v45 offset:880
	ds_write_b32 v71, v38 offset:128
	ds_write_b32 v71, v39 offset:400
	ds_write_b32 v71, v40 offset:672
	ds_write_b32 v71, v41 offset:944
	ds_write_b32 v71, v34 offset:192
	ds_write_b32 v71, v35 offset:464
	ds_write_b32 v71, v36 offset:736
	ds_write_b32 v71, v37 offset:1008
	ds_read_b128 v[180:183], v78
	ds_read_b128 v[184:187], v78 offset:1088
	ds_read_b128 v[188:191], v78 offset:2176
	ds_read_b128 v[192:195], v78 offset:3264
	s_waitcnt lgkmcnt(0)
	s_waitcnt vmcnt(15)
	v_add_f32_e32 v180, v116, v180
	v_add_f32_e32 v181, v117, v181
	v_add_f32_e32 v182, v118, v182
	v_add_f32_e32 v183, v119, v183
	s_add_u32 s38, s36, 0x8000
	s_addc_u32 s39, s37, 0
	global_store_dwordx4 v73, v[180:183], s[38:39]
	s_waitcnt vmcnt(15)
	v_add_f32_e32 v184, v120, v184
	v_add_f32_e32 v185, v121, v185
	v_add_f32_e32 v186, v122, v186
	v_add_f32_e32 v187, v123, v187
	s_add_u32 s38, s36, 0xa000
	s_addc_u32 s39, s37, 0
	global_store_dwordx4 v73, v[184:187], s[38:39]
	s_waitcnt vmcnt(15)
	v_add_f32_e32 v188, v124, v188
	v_add_f32_e32 v189, v125, v189
	v_add_f32_e32 v190, v126, v190
	v_add_f32_e32 v191, v127, v191
	s_add_u32 s38, s36, 0xc000
	s_addc_u32 s39, s37, 0
	global_store_dwordx4 v73, v[188:191], s[38:39]
	s_waitcnt vmcnt(15)
	v_add_f32_e32 v192, v128, v192
	v_add_f32_e32 v193, v129, v193
	v_add_f32_e32 v194, v130, v194
	v_add_f32_e32 v195, v131, v195
	s_add_u32 s38, s36, 0xe000
	s_addc_u32 s39, s37, 0
	global_store_dwordx4 v73, v[192:195], s[38:39]
	v_fmamk_f32 v30, v30, 0x35800000, v74
	v_fmamk_f32 v31, v31, 0x35800000, v74
	v_fmamk_f32 v32, v32, 0x35800000, v74
	v_fmamk_f32 v33, v33, 0x35800000, v74
	v_fmamk_f32 v26, v26, 0x35800000, v75
	v_fmamk_f32 v27, v27, 0x35800000, v75
	v_fmamk_f32 v28, v28, 0x35800000, v75
	v_fmamk_f32 v29, v29, 0x35800000, v75
	v_fmamk_f32 v22, v22, 0x35800000, v76
	v_fmamk_f32 v23, v23, 0x35800000, v76
	v_fmamk_f32 v24, v24, 0x35800000, v76
	v_fmamk_f32 v25, v25, 0x35800000, v76
	v_fmamk_f32 v18, v18, 0x35800000, v77
	v_fmamk_f32 v19, v19, 0x35800000, v77
	v_fmamk_f32 v20, v20, 0x35800000, v77
	v_fmamk_f32 v21, v21, 0x35800000, v77
	ds_write_b32 v71, v30
	ds_write_b32 v71, v31 offset:272
	ds_write_b32 v71, v32 offset:544
	ds_write_b32 v71, v33 offset:816
	ds_write_b32 v71, v26 offset:64
	ds_write_b32 v71, v27 offset:336
	ds_write_b32 v71, v28 offset:608
	ds_write_b32 v71, v29 offset:880
	ds_write_b32 v71, v22 offset:128
	ds_write_b32 v71, v23 offset:400
	ds_write_b32 v71, v24 offset:672
	ds_write_b32 v71, v25 offset:944
	ds_write_b32 v71, v18 offset:192
	ds_write_b32 v71, v19 offset:464
	ds_write_b32 v71, v20 offset:736
	ds_write_b32 v71, v21 offset:1008
	ds_read_b128 v[164:167], v78
	ds_read_b128 v[168:171], v78 offset:1088
	ds_read_b128 v[172:175], v78 offset:2176
	ds_read_b128 v[176:179], v78 offset:3264
	s_waitcnt lgkmcnt(0)
	s_waitcnt vmcnt(15)
	v_add_f32_e32 v164, v132, v164
	v_add_f32_e32 v165, v133, v165
	v_add_f32_e32 v166, v134, v166
	v_add_f32_e32 v167, v135, v167
	s_add_u32 s38, s36, 0x10000
	s_addc_u32 s39, s37, 0
	global_store_dwordx4 v73, v[164:167], s[38:39]
	s_waitcnt vmcnt(15)
	v_add_f32_e32 v168, v136, v168
	v_add_f32_e32 v169, v137, v169
	v_add_f32_e32 v170, v138, v170
	v_add_f32_e32 v171, v139, v171
	s_add_u32 s38, s36, 0x12000
	s_addc_u32 s39, s37, 0
	global_store_dwordx4 v73, v[168:171], s[38:39]
	s_waitcnt vmcnt(15)
	v_add_f32_e32 v172, v140, v172
	v_add_f32_e32 v173, v141, v173
	v_add_f32_e32 v174, v142, v174
	v_add_f32_e32 v175, v143, v175
	s_add_u32 s38, s36, 0x14000
	s_addc_u32 s39, s37, 0
	global_store_dwordx4 v73, v[172:175], s[38:39]
	s_waitcnt vmcnt(15)
	v_add_f32_e32 v176, v144, v176
	v_add_f32_e32 v177, v145, v177
	v_add_f32_e32 v178, v146, v178
	v_add_f32_e32 v179, v147, v179
	s_add_u32 s38, s36, 0x16000
	s_addc_u32 s39, s37, 0
	global_store_dwordx4 v73, v[176:179], s[38:39]
	v_fmamk_f32 v14, v14, 0x35800000, v74
	v_fmamk_f32 v15, v15, 0x35800000, v74
	v_fmamk_f32 v16, v16, 0x35800000, v74
	v_fmamk_f32 v17, v17, 0x35800000, v74
	v_fmamk_f32 v10, v10, 0x35800000, v75
	v_fmamk_f32 v11, v11, 0x35800000, v75
	v_fmamk_f32 v12, v12, 0x35800000, v75
	v_fmamk_f32 v13, v13, 0x35800000, v75
	v_fmamk_f32 v6, v6, 0x35800000, v76
	v_fmamk_f32 v7, v7, 0x35800000, v76
	v_fmamk_f32 v8, v8, 0x35800000, v76
	v_fmamk_f32 v9, v9, 0x35800000, v76
	v_fmamk_f32 v2, v2, 0x35800000, v77
	v_fmamk_f32 v3, v3, 0x35800000, v77
	v_fmamk_f32 v4, v4, 0x35800000, v77
	v_fmamk_f32 v5, v5, 0x35800000, v77
	ds_write_b32 v71, v14
	ds_write_b32 v71, v15 offset:272
	ds_write_b32 v71, v16 offset:544
	ds_write_b32 v71, v17 offset:816
	ds_write_b32 v71, v10 offset:64
	ds_write_b32 v71, v11 offset:336
	ds_write_b32 v71, v12 offset:608
	ds_write_b32 v71, v13 offset:880
	ds_write_b32 v71, v6 offset:128
	ds_write_b32 v71, v7 offset:400
	ds_write_b32 v71, v8 offset:672
	ds_write_b32 v71, v9 offset:944
	ds_write_b32 v71, v2 offset:192
	ds_write_b32 v71, v3 offset:464
	ds_write_b32 v71, v4 offset:736
	ds_write_b32 v71, v5 offset:1008
	ds_read_b128 v[180:183], v78
	ds_read_b128 v[184:187], v78 offset:1088
	ds_read_b128 v[188:191], v78 offset:2176
	ds_read_b128 v[192:195], v78 offset:3264
	s_waitcnt lgkmcnt(0)
	s_waitcnt vmcnt(15)
	v_add_f32_e32 v180, v148, v180
	v_add_f32_e32 v181, v149, v181
	v_add_f32_e32 v182, v150, v182
	v_add_f32_e32 v183, v151, v183
	s_add_u32 s38, s36, 0x18000
	s_addc_u32 s39, s37, 0
	global_store_dwordx4 v73, v[180:183], s[38:39]
	s_waitcnt vmcnt(15)
	v_add_f32_e32 v184, v152, v184
	v_add_f32_e32 v185, v153, v185
	v_add_f32_e32 v186, v154, v186
	v_add_f32_e32 v187, v155, v187
	s_add_u32 s38, s36, 0x1a000
	s_addc_u32 s39, s37, 0
	global_store_dwordx4 v73, v[184:187], s[38:39]
	s_waitcnt vmcnt(15)
	v_add_f32_e32 v188, v156, v188
	v_add_f32_e32 v189, v157, v189
	v_add_f32_e32 v190, v158, v190
	v_add_f32_e32 v191, v159, v191
	s_add_u32 s38, s36, 0x1c000
	s_addc_u32 s39, s37, 0
	global_store_dwordx4 v73, v[188:191], s[38:39]
	s_waitcnt vmcnt(15)
	v_add_f32_e32 v192, v160, v192
	v_add_f32_e32 v193, v161, v193
	v_add_f32_e32 v194, v162, v194
	v_add_f32_e32 v195, v163, v195
	s_add_u32 s38, s36, 0x1e000
	s_addc_u32 s39, s37, 0
	global_store_dwordx4 v73, v[192:195], s[38:39]
	s_endpgm
	.p2alignl 8, 3212836864

.LBB9_47:
.Lepi_again_g3:
	s_mov_b32 s24, s21
	s_mov_b32 s25, s18
	s_mov_b32 s26, s20
	s_mov_b32 s27, s22
	s_load_dwordx2 s[28:29], s[0:1], 0x58
	s_load_dwordx2 s[30:31], s[0:1], 0x60
	s_load_dwordx4 s[32:35], s[0:1], 0x88
	v_and_b32_e32 v66, 63, v0
	v_lshrrev_b32_e32 v67, 6, v0
	v_and_b32_e32 v68, 15, v0
	v_bfe_u32 v69, v0, 4, 2
	v_mul_u32_u24_e32 v70, 0x4000, v67
	s_movk_i32 s2, 0x240
	v_mad_u32_u24 v71, v69, s2, v70
	v_lshl_add_u32 v71, v68, 1, v71
	v_lshrrev_b32_e32 v72, 3, v66
	v_and_b32_e32 v73, 7, v66
	s_movk_i32 s3, 0x90
	v_mad_u32_u24 v74, v72, s3, v70
	v_lshl_add_u32 v74, v73, 4, v74
	v_lshrrev_b32_e32 v75, 1, v67
	v_lshl_add_u32 v75, v75, 6, v72
	v_and_b32_e32 v76, 1, v67
	v_lshlrev_b32_e32 v76, 7, v76
	v_lshl_add_u32 v76, v75, 12, v76
	v_lshl_add_u32 v76, v73, 4, v76
	v_and_b32_e32 v77, 0x4f, v0
	v_lshlrev_b32_e32 v77, 2, v77
	s_waitcnt lgkmcnt(0)
	s_mul_i32 s2, s24, s30
	s_add_i32 s2, s2, s27
	s_lshl_b32 s2, s2, 2
	s_add_u32 s36, s28, s2
	s_addc_u32 s37, s29, 0
	global_load_dword v78, v77, s[36:37]
	global_load_dword v79, v77, s[36:37] offset:64
	global_load_dword v80, v77, s[36:37] offset:128
	global_load_dword v81, v77, s[36:37] offset:192
	s_lshl_b32 s2, s25, 12
	s_lshl_b32 s3, s27, 1
	s_add_u32 s2, s2, s3
	s_add_u32 s38, s32, s2
	s_addc_u32 s39, s33, 0
	s_add_u32 s40, s34, s2
	s_addc_u32 s41, s35, 0
	s_sub_i32 s42, s26, s25
	s_mov_b32 s50, 0xb9c68948
	s_mov_b32 s51, 0x3b7cd369
	s_mov_b32 s52, 0xbcc618b2
	s_mov_b32 s53, 0x3dda74e4
	s_mov_b32 s54, 0x3f228afd
	s_mov_b32 s55, 0x3e03c728
	s_mov_b32 s56, 0x3ba10414
	s_mov_b32 s57, 0xbcdac9b8
	s_mov_b32 s58, 0x3de703be
	s_mov_b32 s59, 0xbec09330
	s_mov_b32 s60, 0x3e0375d0
	s_mov_b32 s61, 0x353504f3
	s_mov_b32 s62, 0x39000000
	v_mov_b32_e32 v102, 0x378e98ab
	v_mov_b32_e32 v103, 0xba1345e1
	s_waitcnt vmcnt(0)
	v_mul_f32_e32 v140, 0x3f3504f3, v78
	v_mul_f32_e32 v144, 0x43000000, v78
	v_mul_f32_e32 v141, 0x3f3504f3, v79
	v_mul_f32_e32 v145, 0x43000000, v79
	v_mul_f32_e32 v142, 0x3f3504f3, v80
	v_mul_f32_e32 v146, 0x43000000, v80
	v_mul_f32_e32 v143, 0x3f3504f3, v81
	v_mul_f32_e32 v147, 0x43000000, v81
	v_fma_f32 v82, v62, s61, v140
	v_fma_f32 v87, v63, s61, v140
	v_fma_f32 v92, v64, s61, v140
	v_fma_f32 v97, v65, s61, v140
	v_fma_f32 v83, v62, s62, v144
	v_fma_f32 v88, v63, s62, v144
	v_fma_f32 v93, v64, s62, v144
	v_fma_f32 v98, v65, s62, v144
	v_mul_f32_e32 v84, v82, v82
	v_mul_f32_e32 v89, v87, v87
	v_mul_f32_e32 v94, v92, v92
	v_mul_f32_e32 v99, v97, v97
	v_cmp_lt_f32_e64 s[64:65], |v82|, 1.0
	v_cmp_lt_f32_e64 s[66:67], |v87|, 1.0
	v_cmp_lt_f32_e64 s[68:69], |v92|, 1.0
	v_cmp_lt_f32_e64 s[70:71], |v97|, 1.0
	v_fma_f32 v86, v84, v103, s56
	v_fma_f32 v91, v89, v103, s56
	v_fma_f32 v96, v94, v103, s56
	v_fma_f32 v101, v99, v103, s56
	s_and_b64 s[72:73], s[64:65], s[66:67]
	s_and_b64 s[74:75], s[68:69], s[70:71]
	s_and_b64 s[72:73], s[72:73], s[74:75]
	v_fma_f32 v86, v84, v86, s57
	v_fma_f32 v91, v89, v91, s57
	v_fma_f32 v96, v94, v96, s57
	v_fma_f32 v101, v99, v101, s57
	v_fma_f32 v86, v84, v86, s58
	v_fma_f32 v91, v89, v91, s58
	v_fma_f32 v96, v94, v96, s58
	v_fma_f32 v101, v99, v101, s58
	v_fma_f32 v86, v84, v86, s59
	v_fma_f32 v91, v89, v91, s59
	v_fma_f32 v96, v94, v96, s59
	v_fma_f32 v101, v99, v101, s59
	v_fma_f32 v86, v84, v86, s60
	v_fma_f32 v91, v89, v91, s60
	v_fma_f32 v96, v94, v96, s60
	v_fma_f32 v101, v99, v101, s60
	v_fma_f32 v86, |v82|, v86, |v82|
	v_fma_f32 v91, |v87|, v91, |v87|
	v_fma_f32 v96, |v92|, v96, |v92|
	v_fma_f32 v101, |v97|, v101, |v97|
	s_cmp_eq_u64 s[72:73], exec
	s_cbranch_scc1 .Lgsk_g3_0
	v_fma_f32 v85, |v82|, v102, s50
	v_fma_f32 v90, |v87|, v102, s50
	v_fma_f32 v95, |v92|, v102, s50
	v_fma_f32 v100, |v97|, v102, s50
	v_fma_f32 v85, |v82|, v85, s51
	v_fma_f32 v90, |v87|, v90, s51
	v_fma_f32 v95, |v92|, v95, s51
	v_fma_f32 v100, |v97|, v100, s51
	v_fma_f32 v85, |v82|, v85, s52
	v_fma_f32 v90, |v87|, v90, s52
	v_fma_f32 v95, |v92|, v95, s52
	v_fma_f32 v100, |v97|, v100, s52
	v_fma_f32 v85, |v82|, v85, s53
	v_fma_f32 v90, |v87|, v90, s53
	v_fma_f32 v95, |v92|, v95, s53
	v_fma_f32 v100, |v97|, v100, s53
	v_fma_f32 v85, |v82|, v85, s54
	v_fma_f32 v90, |v87|, v90, s54
	v_fma_f32 v95, |v92|, v95, s54
	v_fma_f32 v100, |v97|, v100, s54
	v_fma_f32 v85, |v82|, v85, s55
	v_fma_f32 v90, |v87|, v90, s55
	v_fma_f32 v95, |v92|, v95, s55
	v_fma_f32 v100, |v97|, v100, s55
	v_fma_f32 v85, |v82|, v85, |v82|
	v_fma_f32 v90, |v87|, v90, |v87|
	v_fma_f32 v95, |v92|, v95, |v92|
	v_fma_f32 v100, |v97|, v100, |v97|
	v_mul_f32_e32 v85, 0xbfb8aa3b, v85
	v_mul_f32_e32 v90, 0xbfb8aa3b, v90
	v_mul_f32_e32 v95, 0xbfb8aa3b, v95
	v_mul_f32_e32 v100, 0xbfb8aa3b, v100
	v_exp_f32_e32 v85, v85
	v_exp_f32_e32 v90, v90
	v_exp_f32_e32 v95, v95
	v_exp_f32_e32 v100, v100
	s_nop 0
	v_sub_f32_e32 v85, 1.0, v85
	v_sub_f32_e32 v90, 1.0, v90
	v_sub_f32_e32 v95, 1.0, v95
	v_sub_f32_e32 v100, 1.0, v100
	v_cndmask_b32_e64 v86, v85, v86, s[64:65]
	v_cndmask_b32_e64 v91, v90, v91, s[66:67]
	v_cndmask_b32_e64 v96, v95, v96, s[68:69]
	v_cndmask_b32_e64 v101, v100, v101, s[70:71]
.Lgsk_g3_0:
	v_fma_f32 v83, |v83|, v86, v83
	v_fma_f32 v88, |v88|, v91, v88
	v_fma_f32 v93, |v93|, v96, v93
	v_fma_f32 v98, |v98|, v101, v98
	v_cvt_f16_f32_e32 v82, v83
	v_cvt_f16_f32_e32 v87, v88
	v_cvt_f16_f32_e32 v92, v93
	v_cvt_f16_f32_e32 v97, v98
	v_fma_mixlo_f16 v84, v83, 1.0, -v82 op_sel_hi:[0,0,1]
	v_fma_mixlo_f16 v89, v88, 1.0, -v87 op_sel_hi:[0,0,1]
	v_fma_mixlo_f16 v94, v93, 1.0, -v92 op_sel_hi:[0,0,1]
	v_fma_mixlo_f16 v99, v98, 1.0, -v97 op_sel_hi:[0,0,1]
	ds_write_b16 v71, v82
	ds_write_b16 v71, v87 offset:144
	ds_write_b16 v71, v92 offset:288
	ds_write_b16 v71, v97 offset:432
	ds_write_b16 v71, v84 offset:4608
	ds_write_b16 v71, v89 offset:4752
	ds_write_b16 v71, v94 offset:4896
	ds_write_b16 v71, v99 offset:5040
	v_fma_f32 v82, v58, s61, v141
	v_fma_f32 v87, v59, s61, v141
	v_fma_f32 v92, v60, s61, v141
	v_fma_f32 v97, v61, s61, v141
	v_fma_f32 v83, v58, s62, v145
	v_fma_f32 v88, v59, s62, v145
	v_fma_f32 v93, v60, s62, v145
	v_fma_f32 v98, v61, s62, v145
	v_mul_f32_e32 v84, v82, v82
	v_mul_f32_e32 v89, v87, v87
	v_mul_f32_e32 v94, v92, v92
	v_mul_f32_e32 v99, v97, v97
	v_cmp_lt_f32_e64 s[64:65], |v82|, 1.0
	v_cmp_lt_f32_e64 s[66:67], |v87|, 1.0
	v_cmp_lt_f32_e64 s[68:69], |v92|, 1.0
	v_cmp_lt_f32_e64 s[70:71], |v97|, 1.0
	v_fma_f32 v86, v84, v103, s56
	v_fma_f32 v91, v89, v103, s56
	v_fma_f32 v96, v94, v103, s56
	v_fma_f32 v101, v99, v103, s56
	s_and_b64 s[72:73], s[64:65], s[66:67]
	s_and_b64 s[74:75], s[68:69], s[70:71]
	s_and_b64 s[72:73], s[72:73], s[74:75]
	v_fma_f32 v86, v84, v86, s57
	v_fma_f32 v91, v89, v91, s57
	v_fma_f32 v96, v94, v96, s57
	v_fma_f32 v101, v99, v101, s57
	v_fma_f32 v86, v84, v86, s58
	v_fma_f32 v91, v89, v91, s58
	v_fma_f32 v96, v94, v96, s58
	v_fma_f32 v101, v99, v101, s58
	v_fma_f32 v86, v84, v86, s59
	v_fma_f32 v91, v89, v91, s59
	v_fma_f32 v96, v94, v96, s59
	v_fma_f32 v101, v99, v101, s59
	v_fma_f32 v86, v84, v86, s60
	v_fma_f32 v91, v89, v91, s60
	v_fma_f32 v96, v94, v96, s60
	v_fma_f32 v101, v99, v101, s60
	v_fma_f32 v86, |v82|, v86, |v82|
	v_fma_f32 v91, |v87|, v91, |v87|
	v_fma_f32 v96, |v92|, v96, |v92|
	v_fma_f32 v101, |v97|, v101, |v97|
	s_cmp_eq_u64 s[72:73], exec
	s_cbranch_scc1 .Lgsk_g3_1
	v_fma_f32 v85, |v82|, v102, s50
	v_fma_f32 v90, |v87|, v102, s50
	v_fma_f32 v95, |v92|, v102, s50
	v_fma_f32 v100, |v97|, v102, s50
	v_fma_f32 v85, |v82|, v85, s51
	v_fma_f32 v90, |v87|, v90, s51
	v_fma_f32 v95, |v92|, v95, s51
	v_fma_f32 v100, |v97|, v100, s51
	v_fma_f32 v85, |v82|, v85, s52
	v_fma_f32 v90, |v87|, v90, s52
	v_fma_f32 v95, |v92|, v95, s52
	v_fma_f32 v100, |v97|, v100, s52
	v_fma_f32 v85, |v82|, v85, s53
	v_fma_f32 v90, |v87|, v90, s53
	v_fma_f32 v95, |v92|, v95, s53
	v_fma_f32 v100, |v97|, v100, s53
	v_fma_f32 v85, |v82|, v85, s54
	v_fma_f32 v90, |v87|, v90, s54
	v_fma_f32 v95, |v92|, v95, s54
	v_fma_f32 v100, |v97|, v100, s54
	v_fma_f32 v85, |v82|, v85, s55
	v_fma_f32 v90, |v87|, v90, s55
	v_fma_f32 v95, |v92|, v95, s55
	v_fma_f32 v100, |v97|, v100, s55
	v_fma_f32 v85, |v82|, v85, |v82|
	v_fma_f32 v90, |v87|, v90, |v87|
	v_fma_f32 v95, |v92|, v95, |v92|
	v_fma_f32 v100, |v97|, v100, |v97|
	v_mul_f32_e32 v85, 0xbfb8aa3b, v85
	v_mul_f32_e32 v90, 0xbfb8aa3b, v90
	v_mul_f32_e32 v95, 0xbfb8aa3b, v95
	v_mul_f32_e32 v100, 0xbfb8aa3b, v100
	v_exp_f32_e32 v85, v85
	v_exp_f32_e32 v90, v90
	v_exp_f32_e32 v95, v95
	v_exp_f32_e32 v100, v100
	s_nop 0
	v_sub_f32_e32 v85, 1.0, v85
	v_sub_f32_e32 v90, 1.0, v90
	v_sub_f32_e32 v95, 1.0, v95
	v_sub_f32_e32 v100, 1.0, v100
	v_cndmask_b32_e64 v86, v85, v86, s[64:65]
	v_cndmask_b32_e64 v91, v90, v91, s[66:67]
	v_cndmask_b32_e64 v96, v95, v96, s[68:69]
	v_cndmask_b32_e64 v101, v100, v101, s[70:71]
.Lgsk_g3_1:
	v_fma_f32 v83, |v83|, v86, v83
	v_fma_f32 v88, |v88|, v91, v88
	v_fma_f32 v93, |v93|, v96, v93
	v_fma_f32 v98, |v98|, v101, v98
	v_cvt_f16_f32_e32 v82, v83
	v_cvt_f16_f32_e32 v87, v88
	v_cvt_f16_f32_e32 v92, v93
	v_cvt_f16_f32_e32 v97, v98
	v_fma_mixlo_f16 v84, v83, 1.0, -v82 op_sel_hi:[0,0,1]
	v_fma_mixlo_f16 v89, v88, 1.0, -v87 op_sel_hi:[0,0,1]
	v_fma_mixlo_f16 v94, v93, 1.0, -v92 op_sel_hi:[0,0,1]
	v_fma_mixlo_f16 v99, v98, 1.0, -v97 op_sel_hi:[0,0,1]
	ds_write_b16 v71, v82 offset:32
	ds_write_b16 v71, v87 offset:176
	ds_write_b16 v71, v92 offset:320
	ds_write_b16 v71, v97 offset:464
	ds_write_b16 v71, v84 offset:4640
	ds_write_b16 v71, v89 offset:4784
	ds_write_b16 v71, v94 offset:4928
	ds_write_b16 v71, v99 offset:5072
	v_fma_f32 v82, v54, s61, v142
	v_fma_f32 v87, v55, s61, v142
	v_fma_f32 v92, v56, s61, v142
	v_fma_f32 v97, v57, s61, v142
	v_fma_f32 v83, v54, s62, v146
	v_fma_f32 v88, v55, s62, v146
	v_fma_f32 v93, v56, s62, v146
	v_fma_f32 v98, v57, s62, v146
	v_mul_f32_e32 v84, v82, v82
	v_mul_f32_e32 v89, v87, v87
	v_mul_f32_e32 v94, v92, v92
	v_mul_f32_e32 v99, v97, v97
	v_cmp_lt_f32_e64 s[64:65], |v82|, 1.0
	v_cmp_lt_f32_e64 s[66:67], |v87|, 1.0
	v_cmp_lt_f32_e64 s[68:69], |v92|, 1.0
	v_cmp_lt_f32_e64 s[70:71], |v97|, 1.0
	v_fma_f32 v86, v84, v103, s56
	v_fma_f32 v91, v89, v103, s56
	v_fma_f32 v96, v94, v103, s56
	v_fma_f32 v101, v99, v103, s56
	s_and_b64 s[72:73], s[64:65], s[66:67]
	s_and_b64 s[74:75], s[68:69], s[70:71]
	s_and_b64 s[72:73], s[72:73], s[74:75]
	v_fma_f32 v86, v84, v86, s57
	v_fma_f32 v91, v89, v91, s57
	v_fma_f32 v96, v94, v96, s57
	v_fma_f32 v101, v99, v101, s57
	v_fma_f32 v86, v84, v86, s58
	v_fma_f32 v91, v89, v91, s58
	v_fma_f32 v96, v94, v96, s58
	v_fma_f32 v101, v99, v101, s58
	v_fma_f32 v86, v84, v86, s59
	v_fma_f32 v91, v89, v91, s59
	v_fma_f32 v96, v94, v96, s59
	v_fma_f32 v101, v99, v101, s59
	v_fma_f32 v86, v84, v86, s60
	v_fma_f32 v91, v89, v91, s60
	v_fma_f32 v96, v94, v96, s60
	v_fma_f32 v101, v99, v101, s60
	v_fma_f32 v86, |v82|, v86, |v82|
	v_fma_f32 v91, |v87|, v91, |v87|
	v_fma_f32 v96, |v92|, v96, |v92|
	v_fma_f32 v101, |v97|, v101, |v97|
	s_cmp_eq_u64 s[72:73], exec
	s_cbranch_scc1 .Lgsk_g3_2
	v_fma_f32 v85, |v82|, v102, s50
	v_fma_f32 v90, |v87|, v102, s50
	v_fma_f32 v95, |v92|, v102, s50
	v_fma_f32 v100, |v97|, v102, s50
	v_fma_f32 v85, |v82|, v85, s51
	v_fma_f32 v90, |v87|, v90, s51
	v_fma_f32 v95, |v92|, v95, s51
	v_fma_f32 v100, |v97|, v100, s51
	v_fma_f32 v85, |v82|, v85, s52
	v_fma_f32 v90, |v87|, v90, s52
	v_fma_f32 v95, |v92|, v95, s52
	v_fma_f32 v100, |v97|, v100, s52
	v_fma_f32 v85, |v82|, v85, s53
	v_fma_f32 v90, |v87|, v90, s53
	v_fma_f32 v95, |v92|, v95, s53
	v_fma_f32 v100, |v97|, v100, s53
	v_fma_f32 v85, |v82|, v85, s54
	v_fma_f32 v90, |v87|, v90, s54
	v_fma_f32 v95, |v92|, v95, s54
	v_fma_f32 v100, |v97|, v100, s54
	v_fma_f32 v85, |v82|, v85, s55
	v_fma_f32 v90, |v87|, v90, s55
	v_fma_f32 v95, |v92|, v95, s55
	v_fma_f32 v100, |v97|, v100, s55
	v_fma_f32 v85, |v82|, v85, |v82|
	v_fma_f32 v90, |v87|, v90, |v87|
	v_fma_f32 v95, |v92|, v95, |v92|
	v_fma_f32 v100, |v97|, v100, |v97|
	v_mul_f32_e32 v85, 0xbfb8aa3b, v85
	v_mul_f32_e32 v90, 0xbfb8aa3b, v90
	v_mul_f32_e32 v95, 0xbfb8aa3b, v95
	v_mul_f32_e32 v100, 0xbfb8aa3b, v100
	v_exp_f32_e32 v85, v85
	v_exp_f32_e32 v90, v90
	v_exp_f32_e32 v95, v95
	v_exp_f32_e32 v100, v100
	s_nop 0
	v_sub_f32_e32 v85, 1.0, v85
	v_sub_f32_e32 v90, 1.0, v90
	v_sub_f32_e32 v95, 1.0, v95
	v_sub_f32_e32 v100, 1.0, v100
	v_cndmask_b32_e64 v86, v85, v86, s[64:65]
	v_cndmask_b32_e64 v91, v90, v91, s[66:67]
	v_cndmask_b32_e64 v96, v95, v96, s[68:69]
	v_cndmask_b32_e64 v101, v100, v101, s[70:71]
.Lgsk_g3_2:
	v_fma_f32 v83, |v83|, v86, v83
	v_fma_f32 v88, |v88|, v91, v88
	v_fma_f32 v93, |v93|, v96, v93
	v_fma_f32 v98, |v98|, v101, v98
	v_cvt_f16_f32_e32 v82, v83
	v_cvt_f16_f32_e32 v87, v88
	v_cvt_f16_f32_e32 v92, v93
	v_cvt_f16_f32_e32 v97, v98
	v_fma_mixlo_f16 v84, v83, 1.0, -v82 op_sel_hi:[0,0,1]
	v_fma_mixlo_f16 v89, v88, 1.0, -v87 op_sel_hi:[0,0,1]
	v_fma_mixlo_f16 v94, v93, 1.0, -v92 op_sel_hi:[0,0,1]
	v_fma_mixlo_f16 v99, v98, 1.0, -v97 op_sel_hi:[0,0,1]
	ds_write_b16 v71, v82 offset:64
	ds_write_b16 v71, v87 offset:208
	ds_write_b16 v71, v92 offset:352
	ds_write_b16 v71, v97 offset:496
	ds_write_b16 v71, v84 offset:4672
	ds_write_b16 v71, v89 offset:4816
	ds_write_b16 v71, v94 offset:4960
	ds_write_b16 v71, v99 offset:5104
	v_fma_f32 v82, v50, s61, v143
	v_fma_f32 v87, v51, s61, v143
	v_fma_f32 v92, v52, s61, v143
	v_fma_f32 v97, v53, s61, v143
	v_fma_f32 v83, v50, s62, v147
	v_fma_f32 v88, v51, s62, v147
	v_fma_f32 v93, v52, s62, v147
	v_fma_f32 v98, v53, s62, v147
	v_mul_f32_e32 v84, v82, v82
	v_mul_f32_e32 v89, v87, v87
	v_mul_f32_e32 v94, v92, v92
	v_mul_f32_e32 v99, v97, v97
	v_cmp_lt_f32_e64 s[64:65], |v82|, 1.0
	v_cmp_lt_f32_e64 s[66:67], |v87|, 1.0
	v_cmp_lt_f32_e64 s[68:69], |v92|, 1.0
	v_cmp_lt_f32_e64 s[70:71], |v97|, 1.0
	v_fma_f32 v86, v84, v103, s56
	v_fma_f32 v91, v89, v103, s56
	v_fma_f32 v96, v94, v103, s56
	v_fma_f32 v101, v99, v103, s56
	s_and_b64 s[72:73], s[64:65], s[66:67]
	s_and_b64 s[74:75], s[68:69], s[70:71]
	s_and_b64 s[72:73], s[72:73], s[74:75]
	v_fma_f32 v86, v84, v86, s57
	v_fma_f32 v91, v89, v91, s57
	v_fma_f32 v96, v94, v96, s57
	v_fma_f32 v101, v99, v101, s57
	v_fma_f32 v86, v84, v86, s58
	v_fma_f32 v91, v89, v91, s58
	v_fma_f32 v96, v94, v96, s58
	v_fma_f32 v101, v99, v101, s58
	v_fma_f32 v86, v84, v86, s59
	v_fma_f32 v91, v89, v91, s59
	v_fma_f32 v96, v94, v96, s59
	v_fma_f32 v101, v99, v101, s59
	v_fma_f32 v86, v84, v86, s60
	v_fma_f32 v91, v89, v91, s60
	v_fma_f32 v96, v94, v96, s60
	v_fma_f32 v101, v99, v101, s60
	v_fma_f32 v86, |v82|, v86, |v82|
	v_fma_f32 v91, |v87|, v91, |v87|
	v_fma_f32 v96, |v92|, v96, |v92|
	v_fma_f32 v101, |v97|, v101, |v97|
	s_cmp_eq_u64 s[72:73], exec
	s_cbranch_scc1 .Lgsk_g3_3
	v_fma_f32 v85, |v82|, v102, s50
	v_fma_f32 v90, |v87|, v102, s50
	v_fma_f32 v95, |v92|, v102, s50
	v_fma_f32 v100, |v97|, v102, s50
	v_fma_f32 v85, |v82|, v85, s51
	v_fma_f32 v90, |v87|, v90, s51
	v_fma_f32 v95, |v92|, v95, s51
	v_fma_f32 v100, |v97|, v100, s51
	v_fma_f32 v85, |v82|, v85, s52
	v_fma_f32 v90, |v87|, v90, s52
	v_fma_f32 v95, |v92|, v95, s52
	v_fma_f32 v100, |v97|, v100, s52
	v_fma_f32 v85, |v82|, v85, s53
	v_fma_f32 v90, |v87|, v90, s53
	v_fma_f32 v95, |v92|, v95, s53
	v_fma_f32 v100, |v97|, v100, s53
	v_fma_f32 v85, |v82|, v85, s54
	v_fma_f32 v90, |v87|, v90, s54
	v_fma_f32 v95, |v92|, v95, s54
	v_fma_f32 v100, |v97|, v100, s54
	v_fma_f32 v85, |v82|, v85, s55
	v_fma_f32 v90, |v87|, v90, s55
	v_fma_f32 v95, |v92|, v95, s55
	v_fma_f32 v100, |v97|, v100, s55
	v_fma_f32 v85, |v82|, v85, |v82|
	v_fma_f32 v90, |v87|, v90, |v87|
	v_fma_f32 v95, |v92|, v95, |v92|
	v_fma_f32 v100, |v97|, v100, |v97|
	v_mul_f32_e32 v85, 0xbfb8aa3b, v85
	v_mul_f32_e32 v90, 0xbfb8aa3b, v90
	v_mul_f32_e32 v95, 0xbfb8aa3b, v95
	v_mul_f32_e32 v100, 0xbfb8aa3b, v100
	v_exp_f32_e32 v85, v85
	v_exp_f32_e32 v90, v90
	v_exp_f32_e32 v95, v95
	v_exp_f32_e32 v100, v100
	s_nop 0
	v_sub_f32_e32 v85, 1.0, v85
	v_sub_f32_e32 v90, 1.0, v90
	v_sub_f32_e32 v95, 1.0, v95
	v_sub_f32_e32 v100, 1.0, v100
	v_cndmask_b32_e64 v86, v85, v86, s[64:65]
	v_cndmask_b32_e64 v91, v90, v91, s[66:67]
	v_cndmask_b32_e64 v96, v95, v96, s[68:69]
	v_cndmask_b32_e64 v101, v100, v101, s[70:71]
.Lgsk_g3_3:
	v_fma_f32 v83, |v83|, v86, v83
	v_fma_f32 v88, |v88|, v91, v88
	v_fma_f32 v93, |v93|, v96, v93
	v_fma_f32 v98, |v98|, v101, v98
	v_cvt_f16_f32_e32 v82, v83
	v_cvt_f16_f32_e32 v87, v88
	v_cvt_f16_f32_e32 v92, v93
	v_cvt_f16_f32_e32 v97, v98
	v_fma_mixlo_f16 v84, v83, 1.0, -v82 op_sel_hi:[0,0,1]
	v_fma_mixlo_f16 v89, v88, 1.0, -v87 op_sel_hi:[0,0,1]
	v_fma_mixlo_f16 v94, v93, 1.0, -v92 op_sel_hi:[0,0,1]
	v_fma_mixlo_f16 v99, v98, 1.0, -v97 op_sel_hi:[0,0,1]
	ds_write_b16 v71, v82 offset:96
	ds_write_b16 v71, v87 offset:240
	ds_write_b16 v71, v92 offset:384
	ds_write_b16 v71, v97 offset:528
	ds_write_b16 v71, v84 offset:4704
	ds_write_b16 v71, v89 offset:4848
	ds_write_b16 v71, v94 offset:4992
	ds_write_b16 v71, v99 offset:5136
	v_fma_f32 v82, v46, s61, v140
	v_fma_f32 v87, v47, s61, v140
	v_fma_f32 v92, v48, s61, v140
	v_fma_f32 v97, v49, s61, v140
	v_fma_f32 v83, v46, s62, v144
	v_fma_f32 v88, v47, s62, v144
	v_fma_f32 v93, v48, s62, v144
	v_fma_f32 v98, v49, s62, v144
	v_mul_f32_e32 v84, v82, v82
	v_mul_f32_e32 v89, v87, v87
	v_mul_f32_e32 v94, v92, v92
	v_mul_f32_e32 v99, v97, v97
	v_cmp_lt_f32_e64 s[64:65], |v82|, 1.0
	v_cmp_lt_f32_e64 s[66:67], |v87|, 1.0
	v_cmp_lt_f32_e64 s[68:69], |v92|, 1.0
	v_cmp_lt_f32_e64 s[70:71], |v97|, 1.0
	v_fma_f32 v86, v84, v103, s56
	v_fma_f32 v91, v89, v103, s56
	v_fma_f32 v96, v94, v103, s56
	v_fma_f32 v101, v99, v103, s56
	s_and_b64 s[72:73], s[64:65], s[66:67]
	s_and_b64 s[74:75], s[68:69], s[70:71]
	s_and_b64 s[72:73], s[72:73], s[74:75]
	v_fma_f32 v86, v84, v86, s57
	v_fma_f32 v91, v89, v91, s57
	v_fma_f32 v96, v94, v96, s57
	v_fma_f32 v101, v99, v101, s57
	v_fma_f32 v86, v84, v86, s58
	v_fma_f32 v91, v89, v91, s58
	v_fma_f32 v96, v94, v96, s58
	v_fma_f32 v101, v99, v101, s58
	v_fma_f32 v86, v84, v86, s59
	v_fma_f32 v91, v89, v91, s59
	v_fma_f32 v96, v94, v96, s59
	v_fma_f32 v101, v99, v101, s59
	v_fma_f32 v86, v84, v86, s60
	v_fma_f32 v91, v89, v91, s60
	v_fma_f32 v96, v94, v96, s60
	v_fma_f32 v101, v99, v101, s60
	v_fma_f32 v86, |v82|, v86, |v82|
	v_fma_f32 v91, |v87|, v91, |v87|
	v_fma_f32 v96, |v92|, v96, |v92|
	v_fma_f32 v101, |v97|, v101, |v97|
	s_cmp_eq_u64 s[72:73], exec
	s_cbranch_scc1 .Lgsk_g3_4
	v_fma_f32 v85, |v82|, v102, s50
	v_fma_f32 v90, |v87|, v102, s50
	v_fma_f32 v95, |v92|, v102, s50
	v_fma_f32 v100, |v97|, v102, s50
	v_fma_f32 v85, |v82|, v85, s51
	v_fma_f32 v90, |v87|, v90, s51
	v_fma_f32 v95, |v92|, v95, s51
	v_fma_f32 v100, |v97|, v100, s51
	v_fma_f32 v85, |v82|, v85, s52
	v_fma_f32 v90, |v87|, v90, s52
	v_fma_f32 v95, |v92|, v95, s52
	v_fma_f32 v100, |v97|, v100, s52
	v_fma_f32 v85, |v82|, v85, s53
	v_fma_f32 v90, |v87|, v90, s53
	v_fma_f32 v95, |v92|, v95, s53
	v_fma_f32 v100, |v97|, v100, s53
	v_fma_f32 v85, |v82|, v85, s54
	v_fma_f32 v90, |v87|, v90, s54
	v_fma_f32 v95, |v92|, v95, s54
	v_fma_f32 v100, |v97|, v100, s54
	v_fma_f32 v85, |v82|, v85, s55
	v_fma_f32 v90, |v87|, v90, s55
	v_fma_f32 v95, |v92|, v95, s55
	v_fma_f32 v100, |v97|, v100, s55
	v_fma_f32 v85, |v82|, v85, |v82|
	v_fma_f32 v90, |v87|, v90, |v87|
	v_fma_f32 v95, |v92|, v95, |v92|
	v_fma_f32 v100, |v97|, v100, |v97|
	v_mul_f32_e32 v85, 0xbfb8aa3b, v85
	v_mul_f32_e32 v90, 0xbfb8aa3b, v90
	v_mul_f32_e32 v95, 0xbfb8aa3b, v95
	v_mul_f32_e32 v100, 0xbfb8aa3b, v100
	v_exp_f32_e32 v85, v85
	v_exp_f32_e32 v90, v90
	v_exp_f32_e32 v95, v95
	v_exp_f32_e32 v100, v100
	s_nop 0
	v_sub_f32_e32 v85, 1.0, v85
	v_sub_f32_e32 v90, 1.0, v90
	v_sub_f32_e32 v95, 1.0, v95
	v_sub_f32_e32 v100, 1.0, v100
	v_cndmask_b32_e64 v86, v85, v86, s[64:65]
	v_cndmask_b32_e64 v91, v90, v91, s[66:67]
	v_cndmask_b32_e64 v96, v95, v96, s[68:69]
	v_cndmask_b32_e64 v101, v100, v101, s[70:71]
.Lgsk_g3_4:
	v_fma_f32 v83, |v83|, v86, v83
	v_fma_f32 v88, |v88|, v91, v88
	v_fma_f32 v93, |v93|, v96, v93
	v_fma_f32 v98, |v98|, v101, v98
	v_cvt_f16_f32_e32 v82, v83
	v_cvt_f16_f32_e32 v87, v88
	v_cvt_f16_f32_e32 v92, v93
	v_cvt_f16_f32_e32 v97, v98
	v_fma_mixlo_f16 v84, v83, 1.0, -v82 op_sel_hi:[0,0,1]
	v_fma_mixlo_f16 v89, v88, 1.0, -v87 op_sel_hi:[0,0,1]
	v_fma_mixlo_f16 v94, v93, 1.0, -v92 op_sel_hi:[0,0,1]
	v_fma_mixlo_f16 v99, v98, 1.0, -v97 op_sel_hi:[0,0,1]
	ds_write_b16 v71, v82 offset:2304
	ds_write_b16 v71, v87 offset:2448
	ds_write_b16 v71, v92 offset:2592
	ds_write_b16 v71, v97 offset:2736
	ds_write_b16 v71, v84 offset:6912
	ds_write_b16 v71, v89 offset:7056
	ds_write_b16 v71, v94 offset:7200
	ds_write_b16 v71, v99 offset:7344
	v_fma_f32 v82, v42, s61, v141
	v_fma_f32 v87, v43, s61, v141
	v_fma_f32 v92, v44, s61, v141
	v_fma_f32 v97, v45, s61, v141
	v_fma_f32 v83, v42, s62, v145
	v_fma_f32 v88, v43, s62, v145
	v_fma_f32 v93, v44, s62, v145
	v_fma_f32 v98, v45, s62, v145
	v_mul_f32_e32 v84, v82, v82
	v_mul_f32_e32 v89, v87, v87
	v_mul_f32_e32 v94, v92, v92
	v_mul_f32_e32 v99, v97, v97
	v_cmp_lt_f32_e64 s[64:65], |v82|, 1.0
	v_cmp_lt_f32_e64 s[66:67], |v87|, 1.0
	v_cmp_lt_f32_e64 s[68:69], |v92|, 1.0
	v_cmp_lt_f32_e64 s[70:71], |v97|, 1.0
	v_fma_f32 v86, v84, v103, s56
	v_fma_f32 v91, v89, v103, s56
	v_fma_f32 v96, v94, v103, s56
	v_fma_f32 v101, v99, v103, s56
	s_and_b64 s[72:73], s[64:65], s[66:67]
	s_and_b64 s[74:75], s[68:69], s[70:71]
	s_and_b64 s[72:73], s[72:73], s[74:75]
	v_fma_f32 v86, v84, v86, s57
	v_fma_f32 v91, v89, v91, s57
	v_fma_f32 v96, v94, v96, s57
	v_fma_f32 v101, v99, v101, s57
	v_fma_f32 v86, v84, v86, s58
	v_fma_f32 v91, v89, v91, s58
	v_fma_f32 v96, v94, v96, s58
	v_fma_f32 v101, v99, v101, s58
	v_fma_f32 v86, v84, v86, s59
	v_fma_f32 v91, v89, v91, s59
	v_fma_f32 v96, v94, v96, s59
	v_fma_f32 v101, v99, v101, s59
	v_fma_f32 v86, v84, v86, s60
	v_fma_f32 v91, v89, v91, s60
	v_fma_f32 v96, v94, v96, s60
	v_fma_f32 v101, v99, v101, s60
	v_fma_f32 v86, |v82|, v86, |v82|
	v_fma_f32 v91, |v87|, v91, |v87|
	v_fma_f32 v96, |v92|, v96, |v92|
	v_fma_f32 v101, |v97|, v101, |v97|
	s_cmp_eq_u64 s[72:73], exec
	s_cbranch_scc1 .Lgsk_g3_5
	v_fma_f32 v85, |v82|, v102, s50
	v_fma_f32 v90, |v87|, v102, s50
	v_fma_f32 v95, |v92|, v102, s50
	v_fma_f32 v100, |v97|, v102, s50
	v_fma_f32 v85, |v82|, v85, s51
	v_fma_f32 v90, |v87|, v90, s51
	v_fma_f32 v95, |v92|, v95, s51
	v_fma_f32 v100, |v97|, v100, s51
	v_fma_f32 v85, |v82|, v85, s52
	v_fma_f32 v90, |v87|, v90, s52
	v_fma_f32 v95, |v92|, v95, s52
	v_fma_f32 v100, |v97|, v100, s52
	v_fma_f32 v85, |v82|, v85, s53
	v_fma_f32 v90, |v87|, v90, s53
	v_fma_f32 v95, |v92|, v95, s53
	v_fma_f32 v100, |v97|, v100, s53
	v_fma_f32 v85, |v82|, v85, s54
	v_fma_f32 v90, |v87|, v90, s54
	v_fma_f32 v95, |v92|, v95, s54
	v_fma_f32 v100, |v97|, v100, s54
	v_fma_f32 v85, |v82|, v85, s55
	v_fma_f32 v90, |v87|, v90, s55
	v_fma_f32 v95, |v92|, v95, s55
	v_fma_f32 v100, |v97|, v100, s55
	v_fma_f32 v85, |v82|, v85, |v82|
	v_fma_f32 v90, |v87|, v90, |v87|
	v_fma_f32 v95, |v92|, v95, |v92|
	v_fma_f32 v100, |v97|, v100, |v97|
	v_mul_f32_e32 v85, 0xbfb8aa3b, v85
	v_mul_f32_e32 v90, 0xbfb8aa3b, v90
	v_mul_f32_e32 v95, 0xbfb8aa3b, v95
	v_mul_f32_e32 v100, 0xbfb8aa3b, v100
	v_exp_f32_e32 v85, v85
	v_exp_f32_e32 v90, v90
	v_exp_f32_e32 v95, v95
	v_exp_f32_e32 v100, v100
	s_nop 0
	v_sub_f32_e32 v85, 1.0, v85
	v_sub_f32_e32 v90, 1.0, v90
	v_sub_f32_e32 v95, 1.0, v95
	v_sub_f32_e32 v100, 1.0, v100
	v_cndmask_b32_e64 v86, v85, v86, s[64:65]
	v_cndmask_b32_e64 v91, v90, v91, s[66:67]
	v_cndmask_b32_e64 v96, v95, v96, s[68:69]
	v_cndmask_b32_e64 v101, v100, v101, s[70:71]
.Lgsk_g3_5:
	v_fma_f32 v83, |v83|, v86, v83
	v_fma_f32 v88, |v88|, v91, v88
	v_fma_f32 v93, |v93|, v96, v93
	v_fma_f32 v98, |v98|, v101, v98
	v_cvt_f16_f32_e32 v82, v83
	v_cvt_f16_f32_e32 v87, v88
	v_cvt_f16_f32_e32 v92, v93
	v_cvt_f16_f32_e32 v97, v98
	v_fma_mixlo_f16 v84, v83, 1.0, -v82 op_sel_hi:[0,0,1]
	v_fma_mixlo_f16 v89, v88, 1.0, -v87 op_sel_hi:[0,0,1]
	v_fma_mixlo_f16 v94, v93, 1.0, -v92 op_sel_hi:[0,0,1]
	v_fma_mixlo_f16 v99, v98, 1.0, -v97 op_sel_hi:[0,0,1]
	ds_write_b16 v71, v82 offset:2336
	ds_write_b16 v71, v87 offset:2480
	ds_write_b16 v71, v92 offset:2624
	ds_write_b16 v71, v97 offset:2768
	ds_write_b16 v71, v84 offset:6944
	ds_write_b16 v71, v89 offset:7088
	ds_write_b16 v71, v94 offset:7232
	ds_write_b16 v71, v99 offset:7376
	v_fma_f32 v82, v38, s61, v142
	v_fma_f32 v87, v39, s61, v142
	v_fma_f32 v92, v40, s61, v142
	v_fma_f32 v97, v41, s61, v142
	v_fma_f32 v83, v38, s62, v146
	v_fma_f32 v88, v39, s62, v146
	v_fma_f32 v93, v40, s62, v146
	v_fma_f32 v98, v41, s62, v146
	v_mul_f32_e32 v84, v82, v82
	v_mul_f32_e32 v89, v87, v87
	v_mul_f32_e32 v94, v92, v92
	v_mul_f32_e32 v99, v97, v97
	v_cmp_lt_f32_e64 s[64:65], |v82|, 1.0
	v_cmp_lt_f32_e64 s[66:67], |v87|, 1.0
	v_cmp_lt_f32_e64 s[68:69], |v92|, 1.0
	v_cmp_lt_f32_e64 s[70:71], |v97|, 1.0
	v_fma_f32 v86, v84, v103, s56
	v_fma_f32 v91, v89, v103, s56
	v_fma_f32 v96, v94, v103, s56
	v_fma_f32 v101, v99, v103, s56
	s_and_b64 s[72:73], s[64:65], s[66:67]
	s_and_b64 s[74:75], s[68:69], s[70:71]
	s_and_b64 s[72:73], s[72:73], s[74:75]
	v_fma_f32 v86, v84, v86, s57
	v_fma_f32 v91, v89, v91, s57
	v_fma_f32 v96, v94, v96, s57
	v_fma_f32 v101, v99, v101, s57
	v_fma_f32 v86, v84, v86, s58
	v_fma_f32 v91, v89, v91, s58
	v_fma_f32 v96, v94, v96, s58
	v_fma_f32 v101, v99, v101, s58
	v_fma_f32 v86, v84, v86, s59
	v_fma_f32 v91, v89, v91, s59
	v_fma_f32 v96, v94, v96, s59
	v_fma_f32 v101, v99, v101, s59
	v_fma_f32 v86, v84, v86, s60
	v_fma_f32 v91, v89, v91, s60
	v_fma_f32 v96, v94, v96, s60
	v_fma_f32 v101, v99, v101, s60
	v_fma_f32 v86, |v82|, v86, |v82|
	v_fma_f32 v91, |v87|, v91, |v87|
	v_fma_f32 v96, |v92|, v96, |v92|
	v_fma_f32 v101, |v97|, v101, |v97|
	s_cmp_eq_u64 s[72:73], exec
	s_cbranch_scc1 .Lgsk_g3_6
	v_fma_f32 v85, |v82|, v102, s50
	v_fma_f32 v90, |v87|, v102, s50
	v_fma_f32 v95, |v92|, v102, s50
	v_fma_f32 v100, |v97|, v102, s50
	v_fma_f32 v85, |v82|, v85, s51
	v_fma_f32 v90, |v87|, v90, s51
	v_fma_f32 v95, |v92|, v95, s51
	v_fma_f32 v100, |v97|, v100, s51
	v_fma_f32 v85, |v82|, v85, s52
	v_fma_f32 v90, |v87|, v90, s52
	v_fma_f32 v95, |v92|, v95, s52
	v_fma_f32 v100, |v97|, v100, s52
	v_fma_f32 v85, |v82|, v85, s53
	v_fma_f32 v90, |v87|, v90, s53
	v_fma_f32 v95, |v92|, v95, s53
	v_fma_f32 v100, |v97|, v100, s53
	v_fma_f32 v85, |v82|, v85, s54
	v_fma_f32 v90, |v87|, v90, s54
	v_fma_f32 v95, |v92|, v95, s54
	v_fma_f32 v100, |v97|, v100, s54
	v_fma_f32 v85, |v82|, v85, s55
	v_fma_f32 v90, |v87|, v90, s55
	v_fma_f32 v95, |v92|, v95, s55
	v_fma_f32 v100, |v97|, v100, s55
	v_fma_f32 v85, |v82|, v85, |v82|
	v_fma_f32 v90, |v87|, v90, |v87|
	v_fma_f32 v95, |v92|, v95, |v92|
	v_fma_f32 v100, |v97|, v100, |v97|
	v_mul_f32_e32 v85, 0xbfb8aa3b, v85
	v_mul_f32_e32 v90, 0xbfb8aa3b, v90
	v_mul_f32_e32 v95, 0xbfb8aa3b, v95
	v_mul_f32_e32 v100, 0xbfb8aa3b, v100
	v_exp_f32_e32 v85, v85
	v_exp_f32_e32 v90, v90
	v_exp_f32_e32 v95, v95
	v_exp_f32_e32 v100, v100
	s_nop 0
	v_sub_f32_e32 v85, 1.0, v85
	v_sub_f32_e32 v90, 1.0, v90
	v_sub_f32_e32 v95, 1.0, v95
	v_sub_f32_e32 v100, 1.0, v100
	v_cndmask_b32_e64 v86, v85, v86, s[64:65]
	v_cndmask_b32_e64 v91, v90, v91, s[66:67]
	v_cndmask_b32_e64 v96, v95, v96, s[68:69]
	v_cndmask_b32_e64 v101, v100, v101, s[70:71]
.Lgsk_g3_6:
	v_fma_f32 v83, |v83|, v86, v83
	v_fma_f32 v88, |v88|, v91, v88
	v_fma_f32 v93, |v93|, v96, v93
	v_fma_f32 v98, |v98|, v101, v98
	v_cvt_f16_f32_e32 v82, v83
	v_cvt_f16_f32_e32 v87, v88
	v_cvt_f16_f32_e32 v92, v93
	v_cvt_f16_f32_e32 v97, v98
	v_fma_mixlo_f16 v84, v83, 1.0, -v82 op_sel_hi:[0,0,1]
	v_fma_mixlo_f16 v89, v88, 1.0, -v87 op_sel_hi:[0,0,1]
	v_fma_mixlo_f16 v94, v93, 1.0, -v92 op_sel_hi:[0,0,1]
	v_fma_mixlo_f16 v99, v98, 1.0, -v97 op_sel_hi:[0,0,1]
	ds_write_b16 v71, v82 offset:2368
	ds_write_b16 v71, v87 offset:2512
	ds_write_b16 v71, v92 offset:2656
	ds_write_b16 v71, v97 offset:2800
	ds_write_b16 v71, v84 offset:6976
	ds_write_b16 v71, v89 offset:7120
	ds_write_b16 v71, v94 offset:7264
	ds_write_b16 v71, v99 offset:7408
	v_fma_f32 v82, v34, s61, v143
	v_fma_f32 v87, v35, s61, v143
	v_fma_f32 v92, v36, s61, v143
	v_fma_f32 v97, v37, s61, v143
	v_fma_f32 v83, v34, s62, v147
	v_fma_f32 v88, v35, s62, v147
	v_fma_f32 v93, v36, s62, v147
	v_fma_f32 v98, v37, s62, v147
	v_mul_f32_e32 v84, v82, v82
	v_mul_f32_e32 v89, v87, v87
	v_mul_f32_e32 v94, v92, v92
	v_mul_f32_e32 v99, v97, v97
	v_cmp_lt_f32_e64 s[64:65], |v82|, 1.0
	v_cmp_lt_f32_e64 s[66:67], |v87|, 1.0
	v_cmp_lt_f32_e64 s[68:69], |v92|, 1.0
	v_cmp_lt_f32_e64 s[70:71], |v97|, 1.0
	v_fma_f32 v86, v84, v103, s56
	v_fma_f32 v91, v89, v103, s56
	v_fma_f32 v96, v94, v103, s56
	v_fma_f32 v101, v99, v103, s56
	s_and_b64 s[72:73], s[64:65], s[66:67]
	s_and_b64 s[74:75], s[68:69], s[70:71]
	s_and_b64 s[72:73], s[72:73], s[74:75]
	v_fma_f32 v86, v84, v86, s57
	v_fma_f32 v91, v89, v91, s57
	v_fma_f32 v96, v94, v96, s57
	v_fma_f32 v101, v99, v101, s57
	v_fma_f32 v86, v84, v86, s58
	v_fma_f32 v91, v89, v91, s58
	v_fma_f32 v96, v94, v96, s58
	v_fma_f32 v101, v99, v101, s58
	v_fma_f32 v86, v84, v86, s59
	v_fma_f32 v91, v89, v91, s59
	v_fma_f32 v96, v94, v96, s59
	v_fma_f32 v101, v99, v101, s59
	v_fma_f32 v86, v84, v86, s60
	v_fma_f32 v91, v89, v91, s60
	v_fma_f32 v96, v94, v96, s60
	v_fma_f32 v101, v99, v101, s60
	v_fma_f32 v86, |v82|, v86, |v82|
	v_fma_f32 v91, |v87|, v91, |v87|
	v_fma_f32 v96, |v92|, v96, |v92|
	v_fma_f32 v101, |v97|, v101, |v97|
	s_cmp_eq_u64 s[72:73], exec
	s_cbranch_scc1 .Lgsk_g3_7
	v_fma_f32 v85, |v82|, v102, s50
	v_fma_f32 v90, |v87|, v102, s50
	v_fma_f32 v95, |v92|, v102, s50
	v_fma_f32 v100, |v97|, v102, s50
	v_fma_f32 v85, |v82|, v85, s51
	v_fma_f32 v90, |v87|, v90, s51
	v_fma_f32 v95, |v92|, v95, s51
	v_fma_f32 v100, |v97|, v100, s51
	v_fma_f32 v85, |v82|, v85, s52
	v_fma_f32 v90, |v87|, v90, s52
	v_fma_f32 v95, |v92|, v95, s52
	v_fma_f32 v100, |v97|, v100, s52
	v_fma_f32 v85, |v82|, v85, s53
	v_fma_f32 v90, |v87|, v90, s53
	v_fma_f32 v95, |v92|, v95, s53
	v_fma_f32 v100, |v97|, v100, s53
	v_fma_f32 v85, |v82|, v85, s54
	v_fma_f32 v90, |v87|, v90, s54
	v_fma_f32 v95, |v92|, v95, s54
	v_fma_f32 v100, |v97|, v100, s54
	v_fma_f32 v85, |v82|, v85, s55
	v_fma_f32 v90, |v87|, v90, s55
	v_fma_f32 v95, |v92|, v95, s55
	v_fma_f32 v100, |v97|, v100, s55
	v_fma_f32 v85, |v82|, v85, |v82|
	v_fma_f32 v90, |v87|, v90, |v87|
	v_fma_f32 v95, |v92|, v95, |v92|
	v_fma_f32 v100, |v97|, v100, |v97|
	v_mul_f32_e32 v85, 0xbfb8aa3b, v85
	v_mul_f32_e32 v90, 0xbfb8aa3b, v90
	v_mul_f32_e32 v95, 0xbfb8aa3b, v95
	v_mul_f32_e32 v100, 0xbfb8aa3b, v100
	v_exp_f32_e32 v85, v85
	v_exp_f32_e32 v90, v90
	v_exp_f32_e32 v95, v95
	v_exp_f32_e32 v100, v100
	s_nop 0
	v_sub_f32_e32 v85, 1.0, v85
	v_sub_f32_e32 v90, 1.0, v90
	v_sub_f32_e32 v95, 1.0, v95
	v_sub_f32_e32 v100, 1.0, v100
	v_cndmask_b32_e64 v86, v85, v86, s[64:65]
	v_cndmask_b32_e64 v91, v90, v91, s[66:67]
	v_cndmask_b32_e64 v96, v95, v96, s[68:69]
	v_cndmask_b32_e64 v101, v100, v101, s[70:71]
.Lgsk_g3_7:
	v_fma_f32 v83, |v83|, v86, v83
	v_fma_f32 v88, |v88|, v91, v88
	v_fma_f32 v93, |v93|, v96, v93
	v_fma_f32 v98, |v98|, v101, v98
	v_cvt_f16_f32_e32 v82, v83
	v_cvt_f16_f32_e32 v87, v88
	v_cvt_f16_f32_e32 v92, v93
	v_cvt_f16_f32_e32 v97, v98
	v_fma_mixlo_f16 v84, v83, 1.0, -v82 op_sel_hi:[0,0,1]
	v_fma_mixlo_f16 v89, v88, 1.0, -v87 op_sel_hi:[0,0,1]
	v_fma_mixlo_f16 v94, v93, 1.0, -v92 op_sel_hi:[0,0,1]
	v_fma_mixlo_f16 v99, v98, 1.0, -v97 op_sel_hi:[0,0,1]
	ds_write_b16 v71, v82 offset:2400
	ds_write_b16 v71, v87 offset:2544
	ds_write_b16 v71, v92 offset:2688
	ds_write_b16 v71, v97 offset:2832
	ds_write_b16 v71, v84 offset:7008
	ds_write_b16 v71, v89 offset:7152
	ds_write_b16 v71, v94 offset:7296
	ds_write_b16 v71, v99 offset:7440
	ds_read_b128 v[104:107], v74
	ds_read_b128 v[108:111], v74 offset:1152
	ds_read_b128 v[112:115], v74 offset:2304
	ds_read_b128 v[116:119], v74 offset:3456
	ds_read_b128 v[120:123], v74 offset:4608
	ds_read_b128 v[124:127], v74 offset:5760
	ds_read_b128 v[128:131], v74 offset:6912
	ds_read_b128 v[132:135], v74 offset:8064
	v_fma_f32 v82, v30, s61, v140
	v_fma_f32 v87, v31, s61, v140
	v_fma_f32 v92, v32, s61, v140
	v_fma_f32 v97, v33, s61, v140
	v_fma_f32 v83, v30, s62, v144
	v_fma_f32 v88, v31, s62, v144
	v_fma_f32 v93, v32, s62, v144
	v_fma_f32 v98, v33, s62, v144
	v_mul_f32_e32 v84, v82, v82
	v_mul_f32_e32 v89, v87, v87
	v_mul_f32_e32 v94, v92, v92
	v_mul_f32_e32 v99, v97, v97
	v_cmp_lt_f32_e64 s[64:65], |v82|, 1.0
	v_cmp_lt_f32_e64 s[66:67], |v87|, 1.0
	v_cmp_lt_f32_e64 s[68:69], |v92|, 1.0
	v_cmp_lt_f32_e64 s[70:71], |v97|, 1.0
	v_fma_f32 v86, v84, v103, s56
	v_fma_f32 v91, v89, v103, s56
	v_fma_f32 v96, v94, v103, s56
	v_fma_f32 v101, v99, v103, s56
	s_and_b64 s[72:73], s[64:65], s[66:67]
	s_and_b64 s[74:75], s[68:69], s[70:71]
	s_and_b64 s[72:73], s[72:73], s[74:75]
	v_fma_f32 v86, v84, v86, s57
	v_fma_f32 v91, v89, v91, s57
	v_fma_f32 v96, v94, v96, s57
	v_fma_f32 v101, v99, v101, s57
	v_fma_f32 v86, v84, v86, s58
	v_fma_f32 v91, v89, v91, s58
	v_fma_f32 v96, v94, v96, s58
	v_fma_f32 v101, v99, v101, s58
	v_fma_f32 v86, v84, v86, s59
	v_fma_f32 v91, v89, v91, s59
	v_fma_f32 v96, v94, v96, s59
	v_fma_f32 v101, v99, v101, s59
	v_fma_f32 v86, v84, v86, s60
	v_fma_f32 v91, v89, v91, s60
	v_fma_f32 v96, v94, v96, s60
	v_fma_f32 v101, v99, v101, s60
	v_fma_f32 v86, |v82|, v86, |v82|
	v_fma_f32 v91, |v87|, v91, |v87|
	v_fma_f32 v96, |v92|, v96, |v92|
	v_fma_f32 v101, |v97|, v101, |v97|
	s_cmp_eq_u64 s[72:73], exec
	s_cbranch_scc1 .Lgsk_g3_8
	v_fma_f32 v85, |v82|, v102, s50
	v_fma_f32 v90, |v87|, v102, s50
	v_fma_f32 v95, |v92|, v102, s50
	v_fma_f32 v100, |v97|, v102, s50
	v_fma_f32 v85, |v82|, v85, s51
	v_fma_f32 v90, |v87|, v90, s51
	v_fma_f32 v95, |v92|, v95, s51
	v_fma_f32 v100, |v97|, v100, s51
	v_fma_f32 v85, |v82|, v85, s52
	v_fma_f32 v90, |v87|, v90, s52
	v_fma_f32 v95, |v92|, v95, s52
	v_fma_f32 v100, |v97|, v100, s52
	v_fma_f32 v85, |v82|, v85, s53
	v_fma_f32 v90, |v87|, v90, s53
	v_fma_f32 v95, |v92|, v95, s53
	v_fma_f32 v100, |v97|, v100, s53
	v_fma_f32 v85, |v82|, v85, s54
	v_fma_f32 v90, |v87|, v90, s54
	v_fma_f32 v95, |v92|, v95, s54
	v_fma_f32 v100, |v97|, v100, s54
	v_fma_f32 v85, |v82|, v85, s55
	v_fma_f32 v90, |v87|, v90, s55
	v_fma_f32 v95, |v92|, v95, s55
	v_fma_f32 v100, |v97|, v100, s55
	v_fma_f32 v85, |v82|, v85, |v82|
	v_fma_f32 v90, |v87|, v90, |v87|
	v_fma_f32 v95, |v92|, v95, |v92|
	v_fma_f32 v100, |v97|, v100, |v97|
	v_mul_f32_e32 v85, 0xbfb8aa3b, v85
	v_mul_f32_e32 v90, 0xbfb8aa3b, v90
	v_mul_f32_e32 v95, 0xbfb8aa3b, v95
	v_mul_f32_e32 v100, 0xbfb8aa3b, v100
	v_exp_f32_e32 v85, v85
	v_exp_f32_e32 v90, v90
	v_exp_f32_e32 v95, v95
	v_exp_f32_e32 v100, v100
	s_nop 0
	v_sub_f32_e32 v85, 1.0, v85
	v_sub_f32_e32 v90, 1.0, v90
	v_sub_f32_e32 v95, 1.0, v95
	v_sub_f32_e32 v100, 1.0, v100
	v_cndmask_b32_e64 v86, v85, v86, s[64:65]
	v_cndmask_b32_e64 v91, v90, v91, s[66:67]
	v_cndmask_b32_e64 v96, v95, v96, s[68:69]
	v_cndmask_b32_e64 v101, v100, v101, s[70:71]
.Lgsk_g3_8:
	v_fma_f32 v83, |v83|, v86, v83
	v_fma_f32 v88, |v88|, v91, v88
	v_fma_f32 v93, |v93|, v96, v93
	v_fma_f32 v98, |v98|, v101, v98
	v_cvt_f16_f32_e32 v82, v83
	v_cvt_f16_f32_e32 v87, v88
	v_cvt_f16_f32_e32 v92, v93
	v_cvt_f16_f32_e32 v97, v98
	v_fma_mixlo_f16 v84, v83, 1.0, -v82 op_sel_hi:[0,0,1]
	v_fma_mixlo_f16 v89, v88, 1.0, -v87 op_sel_hi:[0,0,1]
	v_fma_mixlo_f16 v94, v93, 1.0, -v92 op_sel_hi:[0,0,1]
	v_fma_mixlo_f16 v99, v98, 1.0, -v97 op_sel_hi:[0,0,1]
	s_waitcnt lgkmcnt(0)
	s_sub_i32 s2, s42, 0
	v_cmp_gt_i32_e32 vcc, s2, v75
	s_and_saveexec_b64 s[44:45], vcc
	s_add_u32 s2, s38, 0x0
	s_addc_u32 s3, s39, 0
	global_store_dwordx4 v76, v[104:107], s[2:3]
	s_add_u32 s2, s40, 0x0
	s_addc_u32 s3, s41, 0
	global_store_dwordx4 v76, v[120:123], s[2:3]
	s_mov_b64 exec, s[44:45]
	s_sub_i32 s2, s42, 8
	v_cmp_gt_i32_e32 vcc, s2, v75
	s_and_saveexec_b64 s[44:45], vcc
	s_add_u32 s2, s38, 0x8000
	s_addc_u32 s3, s39, 0
	global_store_dwordx4 v76, v[108:111], s[2:3]
	s_add_u32 s2, s40, 0x8000
	s_addc_u32 s3, s41, 0
	global_store_dwordx4 v76, v[124:127], s[2:3]
	s_mov_b64 exec, s[44:45]
	s_sub_i32 s2, s42, 16
	v_cmp_gt_i32_e32 vcc, s2, v75
	s_and_saveexec_b64 s[44:45], vcc
	s_add_u32 s2, s38, 0x10000
	s_addc_u32 s3, s39, 0
	global_store_dwordx4 v76, v[112:115], s[2:3]
	s_add_u32 s2, s40, 0x10000
	s_addc_u32 s3, s41, 0
	global_store_dwordx4 v76, v[128:131], s[2:3]
	s_mov_b64 exec, s[44:45]
	s_sub_i32 s2, s42, 24
	v_cmp_gt_i32_e32 vcc, s2, v75
	s_and_saveexec_b64 s[44:45], vcc
	s_add_u32 s2, s38, 0x18000
	s_addc_u32 s3, s39, 0
	global_store_dwordx4 v76, v[116:119], s[2:3]
	s_add_u32 s2, s40, 0x18000
	s_addc_u32 s3, s41, 0
	global_store_dwordx4 v76, v[132:135], s[2:3]
	s_mov_b64 exec, s[44:45]
	ds_write_b16 v71, v82
	ds_write_b16 v71, v87 offset:144
	ds_write_b16 v71, v92 offset:288
	ds_write_b16 v71, v97 offset:432
	ds_write_b16 v71, v84 offset:4608
	ds_write_b16 v71, v89 offset:4752
	ds_write_b16 v71, v94 offset:4896
	ds_write_b16 v71, v99 offset:5040
	v_fma_f32 v82, v26, s61, v141
	v_fma_f32 v87, v27, s61, v141
	v_fma_f32 v92, v28, s61, v141
	v_fma_f32 v97, v29, s61, v141
	v_fma_f32 v83, v26, s62, v145
	v_fma_f32 v88, v27, s62, v145
	v_fma_f32 v93, v28, s62, v145
	v_fma_f32 v98, v29, s62, v145
	v_mul_f32_e32 v84, v82, v82
	v_mul_f32_e32 v89, v87, v87
	v_mul_f32_e32 v94, v92, v92
	v_mul_f32_e32 v99, v97, v97
	v_cmp_lt_f32_e64 s[64:65], |v82|, 1.0
	v_cmp_lt_f32_e64 s[66:67], |v87|, 1.0
	v_cmp_lt_f32_e64 s[68:69], |v92|, 1.0
	v_cmp_lt_f32_e64 s[70:71], |v97|, 1.0
	v_fma_f32 v86, v84, v103, s56
	v_fma_f32 v91, v89, v103, s56
	v_fma_f32 v96, v94, v103, s56
	v_fma_f32 v101, v99, v103, s56
	s_and_b64 s[72:73], s[64:65], s[66:67]
	s_and_b64 s[74:75], s[68:69], s[70:71]
	s_and_b64 s[72:73], s[72:73], s[74:75]
	v_fma_f32 v86, v84, v86, s57
	v_fma_f32 v91, v89, v91, s57
	v_fma_f32 v96, v94, v96, s57
	v_fma_f32 v101, v99, v101, s57
	v_fma_f32 v86, v84, v86, s58
	v_fma_f32 v91, v89, v91, s58
	v_fma_f32 v96, v94, v96, s58
	v_fma_f32 v101, v99, v101, s58
	v_fma_f32 v86, v84, v86, s59
	v_fma_f32 v91, v89, v91, s59
	v_fma_f32 v96, v94, v96, s59
	v_fma_f32 v101, v99, v101, s59
	v_fma_f32 v86, v84, v86, s60
	v_fma_f32 v91, v89, v91, s60
	v_fma_f32 v96, v94, v96, s60
	v_fma_f32 v101, v99, v101, s60
	v_fma_f32 v86, |v82|, v86, |v82|
	v_fma_f32 v91, |v87|, v91, |v87|
	v_fma_f32 v96, |v92|, v96, |v92|
	v_fma_f32 v101, |v97|, v101, |v97|
	s_cmp_eq_u64 s[72:73], exec
	s_cbranch_scc1 .Lgsk_g3_9
	v_fma_f32 v85, |v82|, v102, s50
	v_fma_f32 v90, |v87|, v102, s50
	v_fma_f32 v95, |v92|, v102, s50
	v_fma_f32 v100, |v97|, v102, s50
	v_fma_f32 v85, |v82|, v85, s51
	v_fma_f32 v90, |v87|, v90, s51
	v_fma_f32 v95, |v92|, v95, s51
	v_fma_f32 v100, |v97|, v100, s51
	v_fma_f32 v85, |v82|, v85, s52
	v_fma_f32 v90, |v87|, v90, s52
	v_fma_f32 v95, |v92|, v95, s52
	v_fma_f32 v100, |v97|, v100, s52
	v_fma_f32 v85, |v82|, v85, s53
	v_fma_f32 v90, |v87|, v90, s53
	v_fma_f32 v95, |v92|, v95, s53
	v_fma_f32 v100, |v97|, v100, s53
	v_fma_f32 v85, |v82|, v85, s54
	v_fma_f32 v90, |v87|, v90, s54
	v_fma_f32 v95, |v92|, v95, s54
	v_fma_f32 v100, |v97|, v100, s54
	v_fma_f32 v85, |v82|, v85, s55
	v_fma_f32 v90, |v87|, v90, s55
	v_fma_f32 v95, |v92|, v95, s55
	v_fma_f32 v100, |v97|, v100, s55
	v_fma_f32 v85, |v82|, v85, |v82|
	v_fma_f32 v90, |v87|, v90, |v87|
	v_fma_f32 v95, |v92|, v95, |v92|
	v_fma_f32 v100, |v97|, v100, |v97|
	v_mul_f32_e32 v85, 0xbfb8aa3b, v85
	v_mul_f32_e32 v90, 0xbfb8aa3b, v90
	v_mul_f32_e32 v95, 0xbfb8aa3b, v95
	v_mul_f32_e32 v100, 0xbfb8aa3b, v100
	v_exp_f32_e32 v85, v85
	v_exp_f32_e32 v90, v90
	v_exp_f32_e32 v95, v95
	v_exp_f32_e32 v100, v100
	s_nop 0
	v_sub_f32_e32 v85, 1.0, v85
	v_sub_f32_e32 v90, 1.0, v90
	v_sub_f32_e32 v95, 1.0, v95
	v_sub_f32_e32 v100, 1.0, v100
	v_cndmask_b32_e64 v86, v85, v86, s[64:65]
	v_cndmask_b32_e64 v91, v90, v91, s[66:67]
	v_cndmask_b32_e64 v96, v95, v96, s[68:69]
	v_cndmask_b32_e64 v101, v100, v101, s[70:71]
.Lgsk_g3_9:
	v_fma_f32 v83, |v83|, v86, v83
	v_fma_f32 v88, |v88|, v91, v88
	v_fma_f32 v93, |v93|, v96, v93
	v_fma_f32 v98, |v98|, v101, v98
	v_cvt_f16_f32_e32 v82, v83
	v_cvt_f16_f32_e32 v87, v88
	v_cvt_f16_f32_e32 v92, v93
	v_cvt_f16_f32_e32 v97, v98
	v_fma_mixlo_f16 v84, v83, 1.0, -v82 op_sel_hi:[0,0,1]
	v_fma_mixlo_f16 v89, v88, 1.0, -v87 op_sel_hi:[0,0,1]
	v_fma_mixlo_f16 v94, v93, 1.0, -v92 op_sel_hi:[0,0,1]
	v_fma_mixlo_f16 v99, v98, 1.0, -v97 op_sel_hi:[0,0,1]
	ds_write_b16 v71, v82 offset:32
	ds_write_b16 v71, v87 offset:176
	ds_write_b16 v71, v92 offset:320
	ds_write_b16 v71, v97 offset:464
	ds_write_b16 v71, v84 offset:4640
	ds_write_b16 v71, v89 offset:4784
	ds_write_b16 v71, v94 offset:4928
	ds_write_b16 v71, v99 offset:5072
	v_fma_f32 v82, v22, s61, v142
	v_fma_f32 v87, v23, s61, v142
	v_fma_f32 v92, v24, s61, v142
	v_fma_f32 v97, v25, s61, v142
	v_fma_f32 v83, v22, s62, v146
	v_fma_f32 v88, v23, s62, v146
	v_fma_f32 v93, v24, s62, v146
	v_fma_f32 v98, v25, s62, v146
	v_mul_f32_e32 v84, v82, v82
	v_mul_f32_e32 v89, v87, v87
	v_mul_f32_e32 v94, v92, v92
	v_mul_f32_e32 v99, v97, v97
	v_cmp_lt_f32_e64 s[64:65], |v82|, 1.0
	v_cmp_lt_f32_e64 s[66:67], |v87|, 1.0
	v_cmp_lt_f32_e64 s[68:69], |v92|, 1.0
	v_cmp_lt_f32_e64 s[70:71], |v97|, 1.0
	v_fma_f32 v86, v84, v103, s56
	v_fma_f32 v91, v89, v103, s56
	v_fma_f32 v96, v94, v103, s56
	v_fma_f32 v101, v99, v103, s56
	s_and_b64 s[72:73], s[64:65], s[66:67]
	s_and_b64 s[74:75], s[68:69], s[70:71]
	s_and_b64 s[72:73], s[72:73], s[74:75]
	v_fma_f32 v86, v84, v86, s57
	v_fma_f32 v91, v89, v91, s57
	v_fma_f32 v96, v94, v96, s57
	v_fma_f32 v101, v99, v101, s57
	v_fma_f32 v86, v84, v86, s58
	v_fma_f32 v91, v89, v91, s58
	v_fma_f32 v96, v94, v96, s58
	v_fma_f32 v101, v99, v101, s58
	v_fma_f32 v86, v84, v86, s59
	v_fma_f32 v91, v89, v91, s59
	v_fma_f32 v96, v94, v96, s59
	v_fma_f32 v101, v99, v101, s59
	v_fma_f32 v86, v84, v86, s60
	v_fma_f32 v91, v89, v91, s60
	v_fma_f32 v96, v94, v96, s60
	v_fma_f32 v101, v99, v101, s60
	v_fma_f32 v86, |v82|, v86, |v82|
	v_fma_f32 v91, |v87|, v91, |v87|
	v_fma_f32 v96, |v92|, v96, |v92|
	v_fma_f32 v101, |v97|, v101, |v97|
	s_cmp_eq_u64 s[72:73], exec
	s_cbranch_scc1 .Lgsk_g3_10
	v_fma_f32 v85, |v82|, v102, s50
	v_fma_f32 v90, |v87|, v102, s50
	v_fma_f32 v95, |v92|, v102, s50
	v_fma_f32 v100, |v97|, v102, s50
	v_fma_f32 v85, |v82|, v85, s51
	v_fma_f32 v90, |v87|, v90, s51
	v_fma_f32 v95, |v92|, v95, s51
	v_fma_f32 v100, |v97|, v100, s51
	v_fma_f32 v85, |v82|, v85, s52
	v_fma_f32 v90, |v87|, v90, s52
	v_fma_f32 v95, |v92|, v95, s52
	v_fma_f32 v100, |v97|, v100, s52
	v_fma_f32 v85, |v82|, v85, s53
	v_fma_f32 v90, |v87|, v90, s53
	v_fma_f32 v95, |v92|, v95, s53
	v_fma_f32 v100, |v97|, v100, s53
	v_fma_f32 v85, |v82|, v85, s54
	v_fma_f32 v90, |v87|, v90, s54
	v_fma_f32 v95, |v92|, v95, s54
	v_fma_f32 v100, |v97|, v100, s54
	v_fma_f32 v85, |v82|, v85, s55
	v_fma_f32 v90, |v87|, v90, s55
	v_fma_f32 v95, |v92|, v95, s55
	v_fma_f32 v100, |v97|, v100, s55
	v_fma_f32 v85, |v82|, v85, |v82|
	v_fma_f32 v90, |v87|, v90, |v87|
	v_fma_f32 v95, |v92|, v95, |v92|
	v_fma_f32 v100, |v97|, v100, |v97|
	v_mul_f32_e32 v85, 0xbfb8aa3b, v85
	v_mul_f32_e32 v90, 0xbfb8aa3b, v90
	v_mul_f32_e32 v95, 0xbfb8aa3b, v95
	v_mul_f32_e32 v100, 0xbfb8aa3b, v100
	v_exp_f32_e32 v85, v85
	v_exp_f32_e32 v90, v90
	v_exp_f32_e32 v95, v95
	v_exp_f32_e32 v100, v100
	s_nop 0
	v_sub_f32_e32 v85, 1.0, v85
	v_sub_f32_e32 v90, 1.0, v90
	v_sub_f32_e32 v95, 1.0, v95
	v_sub_f32_e32 v100, 1.0, v100
	v_cndmask_b32_e64 v86, v85, v86, s[64:65]
	v_cndmask_b32_e64 v91, v90, v91, s[66:67]
	v_cndmask_b32_e64 v96, v95, v96, s[68:69]
	v_cndmask_b32_e64 v101, v100, v101, s[70:71]
.Lgsk_g3_10:
	v_fma_f32 v83, |v83|, v86, v83
	v_fma_f32 v88, |v88|, v91, v88
	v_fma_f32 v93, |v93|, v96, v93
	v_fma_f32 v98, |v98|, v101, v98
	v_cvt_f16_f32_e32 v82, v83
	v_cvt_f16_f32_e32 v87, v88
	v_cvt_f16_f32_e32 v92, v93
	v_cvt_f16_f32_e32 v97, v98
	v_fma_mixlo_f16 v84, v83, 1.0, -v82 op_sel_hi:[0,0,1]
	v_fma_mixlo_f16 v89, v88, 1.0, -v87 op_sel_hi:[0,0,1]
	v_fma_mixlo_f16 v94, v93, 1.0, -v92 op_sel_hi:[0,0,1]
	v_fma_mixlo_f16 v99, v98, 1.0, -v97 op_sel_hi:[0,0,1]
	ds_write_b16 v71, v82 offset:64
	ds_write_b16 v71, v87 offset:208
	ds_write_b16 v71, v92 offset:352
	ds_write_b16 v71, v97 offset:496
	ds_write_b16 v71, v84 offset:4672
	ds_write_b16 v71, v89 offset:4816
	ds_write_b16 v71, v94 offset:4960
	ds_write_b16 v71, v99 offset:5104
	v_fma_f32 v82, v18, s61, v143
	v_fma_f32 v87, v19, s61, v143
	v_fma_f32 v92, v20, s61, v143
	v_fma_f32 v97, v21, s61, v143
	v_fma_f32 v83, v18, s62, v147
	v_fma_f32 v88, v19, s62, v147
	v_fma_f32 v93, v20, s62, v147
	v_fma_f32 v98, v21, s62, v147
	v_mul_f32_e32 v84, v82, v82
	v_mul_f32_e32 v89, v87, v87
	v_mul_f32_e32 v94, v92, v92
	v_mul_f32_e32 v99, v97, v97
	v_cmp_lt_f32_e64 s[64:65], |v82|, 1.0
	v_cmp_lt_f32_e64 s[66:67], |v87|, 1.0
	v_cmp_lt_f32_e64 s[68:69], |v92|, 1.0
	v_cmp_lt_f32_e64 s[70:71], |v97|, 1.0
	v_fma_f32 v86, v84, v103, s56
	v_fma_f32 v91, v89, v103, s56
	v_fma_f32 v96, v94, v103, s56
	v_fma_f32 v101, v99, v103, s56
	s_and_b64 s[72:73], s[64:65], s[66:67]
	s_and_b64 s[74:75], s[68:69], s[70:71]
	s_and_b64 s[72:73], s[72:73], s[74:75]
	v_fma_f32 v86, v84, v86, s57
	v_fma_f32 v91, v89, v91, s57
	v_fma_f32 v96, v94, v96, s57
	v_fma_f32 v101, v99, v101, s57
	v_fma_f32 v86, v84, v86, s58
	v_fma_f32 v91, v89, v91, s58
	v_fma_f32 v96, v94, v96, s58
	v_fma_f32 v101, v99, v101, s58
	v_fma_f32 v86, v84, v86, s59
	v_fma_f32 v91, v89, v91, s59
	v_fma_f32 v96, v94, v96, s59
	v_fma_f32 v101, v99, v101, s59
	v_fma_f32 v86, v84, v86, s60
	v_fma_f32 v91, v89, v91, s60
	v_fma_f32 v96, v94, v96, s60
	v_fma_f32 v101, v99, v101, s60
	v_fma_f32 v86, |v82|, v86, |v82|
	v_fma_f32 v91, |v87|, v91, |v87|
	v_fma_f32 v96, |v92|, v96, |v92|
	v_fma_f32 v101, |v97|, v101, |v97|
	s_cmp_eq_u64 s[72:73], exec
	s_cbranch_scc1 .Lgsk_g3_11
	v_fma_f32 v85, |v82|, v102, s50
	v_fma_f32 v90, |v87|, v102, s50
	v_fma_f32 v95, |v92|, v102, s50
	v_fma_f32 v100, |v97|, v102, s50
	v_fma_f32 v85, |v82|, v85, s51
	v_fma_f32 v90, |v87|, v90, s51
	v_fma_f32 v95, |v92|, v95, s51
	v_fma_f32 v100, |v97|, v100, s51
	v_fma_f32 v85, |v82|, v85, s52
	v_fma_f32 v90, |v87|, v90, s52
	v_fma_f32 v95, |v92|, v95, s52
	v_fma_f32 v100, |v97|, v100, s52
	v_fma_f32 v85, |v82|, v85, s53
	v_fma_f32 v90, |v87|, v90, s53
	v_fma_f32 v95, |v92|, v95, s53
	v_fma_f32 v100, |v97|, v100, s53
	v_fma_f32 v85, |v82|, v85, s54
	v_fma_f32 v90, |v87|, v90, s54
	v_fma_f32 v95, |v92|, v95, s54
	v_fma_f32 v100, |v97|, v100, s54
	v_fma_f32 v85, |v82|, v85, s55
	v_fma_f32 v90, |v87|, v90, s55
	v_fma_f32 v95, |v92|, v95, s55
	v_fma_f32 v100, |v97|, v100, s55
	v_fma_f32 v85, |v82|, v85, |v82|
	v_fma_f32 v90, |v87|, v90, |v87|
	v_fma_f32 v95, |v92|, v95, |v92|
	v_fma_f32 v100, |v97|, v100, |v97|
	v_mul_f32_e32 v85, 0xbfb8aa3b, v85
	v_mul_f32_e32 v90, 0xbfb8aa3b, v90
	v_mul_f32_e32 v95, 0xbfb8aa3b, v95
	v_mul_f32_e32 v100, 0xbfb8aa3b, v100
	v_exp_f32_e32 v85, v85
	v_exp_f32_e32 v90, v90
	v_exp_f32_e32 v95, v95
	v_exp_f32_e32 v100, v100
	s_nop 0
	v_sub_f32_e32 v85, 1.0, v85
	v_sub_f32_e32 v90, 1.0, v90
	v_sub_f32_e32 v95, 1.0, v95
	v_sub_f32_e32 v100, 1.0, v100
	v_cndmask_b32_e64 v86, v85, v86, s[64:65]
	v_cndmask_b32_e64 v91, v90, v91, s[66:67]
	v_cndmask_b32_e64 v96, v95, v96, s[68:69]
	v_cndmask_b32_e64 v101, v100, v101, s[70:71]
.Lgsk_g3_11:
	v_fma_f32 v83, |v83|, v86, v83
	v_fma_f32 v88, |v88|, v91, v88
	v_fma_f32 v93, |v93|, v96, v93
	v_fma_f32 v98, |v98|, v101, v98
	v_cvt_f16_f32_e32 v82, v83
	v_cvt_f16_f32_e32 v87, v88
	v_cvt_f16_f32_e32 v92, v93
	v_cvt_f16_f32_e32 v97, v98
	v_fma_mixlo_f16 v84, v83, 1.0, -v82 op_sel_hi:[0,0,1]
	v_fma_mixlo_f16 v89, v88, 1.0, -v87 op_sel_hi:[0,0,1]
	v_fma_mixlo_f16 v94, v93, 1.0, -v92 op_sel_hi:[0,0,1]
	v_fma_mixlo_f16 v99, v98, 1.0, -v97 op_sel_hi:[0,0,1]
	ds_write_b16 v71, v82 offset:96
	ds_write_b16 v71, v87 offset:240
	ds_write_b16 v71, v92 offset:384
	ds_write_b16 v71, v97 offset:528
	ds_write_b16 v71, v84 offset:4704
	ds_write_b16 v71, v89 offset:4848
	ds_write_b16 v71, v94 offset:4992
	ds_write_b16 v71, v99 offset:5136
	v_fma_f32 v82, v14, s61, v140
	v_fma_f32 v87, v15, s61, v140
	v_fma_f32 v92, v16, s61, v140
	v_fma_f32 v97, v17, s61, v140
	v_fma_f32 v83, v14, s62, v144
	v_fma_f32 v88, v15, s62, v144
	v_fma_f32 v93, v16, s62, v144
	v_fma_f32 v98, v17, s62, v144
	v_mul_f32_e32 v84, v82, v82
	v_mul_f32_e32 v89, v87, v87
	v_mul_f32_e32 v94, v92, v92
	v_mul_f32_e32 v99, v97, v97
	v_cmp_lt_f32_e64 s[64:65], |v82|, 1.0
	v_cmp_lt_f32_e64 s[66:67], |v87|, 1.0
	v_cmp_lt_f32_e64 s[68:69], |v92|, 1.0
	v_cmp_lt_f32_e64 s[70:71], |v97|, 1.0
	v_fma_f32 v86, v84, v103, s56
	v_fma_f32 v91, v89, v103, s56
	v_fma_f32 v96, v94, v103, s56
	v_fma_f32 v101, v99, v103, s56
	s_and_b64 s[72:73], s[64:65], s[66:67]
	s_and_b64 s[74:75], s[68:69], s[70:71]
	s_and_b64 s[72:73], s[72:73], s[74:75]
	v_fma_f32 v86, v84, v86, s57
	v_fma_f32 v91, v89, v91, s57
	v_fma_f32 v96, v94, v96, s57
	v_fma_f32 v101, v99, v101, s57
	v_fma_f32 v86, v84, v86, s58
	v_fma_f32 v91, v89, v91, s58
	v_fma_f32 v96, v94, v96, s58
	v_fma_f32 v101, v99, v101, s58
	v_fma_f32 v86, v84, v86, s59
	v_fma_f32 v91, v89, v91, s59
	v_fma_f32 v96, v94, v96, s59
	v_fma_f32 v101, v99, v101, s59
	v_fma_f32 v86, v84, v86, s60
	v_fma_f32 v91, v89, v91, s60
	v_fma_f32 v96, v94, v96, s60
	v_fma_f32 v101, v99, v101, s60
	v_fma_f32 v86, |v82|, v86, |v82|
	v_fma_f32 v91, |v87|, v91, |v87|
	v_fma_f32 v96, |v92|, v96, |v92|
	v_fma_f32 v101, |v97|, v101, |v97|
	s_cmp_eq_u64 s[72:73], exec
	s_cbranch_scc1 .Lgsk_g3_12
	v_fma_f32 v85, |v82|, v102, s50
	v_fma_f32 v90, |v87|, v102, s50
	v_fma_f32 v95, |v92|, v102, s50
	v_fma_f32 v100, |v97|, v102, s50
	v_fma_f32 v85, |v82|, v85, s51
	v_fma_f32 v90, |v87|, v90, s51
	v_fma_f32 v95, |v92|, v95, s51
	v_fma_f32 v100, |v97|, v100, s51
	v_fma_f32 v85, |v82|, v85, s52
	v_fma_f32 v90, |v87|, v90, s52
	v_fma_f32 v95, |v92|, v95, s52
	v_fma_f32 v100, |v97|, v100, s52
	v_fma_f32 v85, |v82|, v85, s53
	v_fma_f32 v90, |v87|, v90, s53
	v_fma_f32 v95, |v92|, v95, s53
	v_fma_f32 v100, |v97|, v100, s53
	v_fma_f32 v85, |v82|, v85, s54
	v_fma_f32 v90, |v87|, v90, s54
	v_fma_f32 v95, |v92|, v95, s54
	v_fma_f32 v100, |v97|, v100, s54
	v_fma_f32 v85, |v82|, v85, s55
	v_fma_f32 v90, |v87|, v90, s55
	v_fma_f32 v95, |v92|, v95, s55
	v_fma_f32 v100, |v97|, v100, s55
	v_fma_f32 v85, |v82|, v85, |v82|
	v_fma_f32 v90, |v87|, v90, |v87|
	v_fma_f32 v95, |v92|, v95, |v92|
	v_fma_f32 v100, |v97|, v100, |v97|
	v_mul_f32_e32 v85, 0xbfb8aa3b, v85
	v_mul_f32_e32 v90, 0xbfb8aa3b, v90
	v_mul_f32_e32 v95, 0xbfb8aa3b, v95
	v_mul_f32_e32 v100, 0xbfb8aa3b, v100
	v_exp_f32_e32 v85, v85
	v_exp_f32_e32 v90, v90
	v_exp_f32_e32 v95, v95
	v_exp_f32_e32 v100, v100
	s_nop 0
	v_sub_f32_e32 v85, 1.0, v85
	v_sub_f32_e32 v90, 1.0, v90
	v_sub_f32_e32 v95, 1.0, v95
	v_sub_f32_e32 v100, 1.0, v100
	v_cndmask_b32_e64 v86, v85, v86, s[64:65]
	v_cndmask_b32_e64 v91, v90, v91, s[66:67]
	v_cndmask_b32_e64 v96, v95, v96, s[68:69]
	v_cndmask_b32_e64 v101, v100, v101, s[70:71]
.Lgsk_g3_12:
	v_fma_f32 v83, |v83|, v86, v83
	v_fma_f32 v88, |v88|, v91, v88
	v_fma_f32 v93, |v93|, v96, v93
	v_fma_f32 v98, |v98|, v101, v98
	v_cvt_f16_f32_e32 v82, v83
	v_cvt_f16_f32_e32 v87, v88
	v_cvt_f16_f32_e32 v92, v93
	v_cvt_f16_f32_e32 v97, v98
	v_fma_mixlo_f16 v84, v83, 1.0, -v82 op_sel_hi:[0,0,1]
	v_fma_mixlo_f16 v89, v88, 1.0, -v87 op_sel_hi:[0,0,1]
	v_fma_mixlo_f16 v94, v93, 1.0, -v92 op_sel_hi:[0,0,1]
	v_fma_mixlo_f16 v99, v98, 1.0, -v97 op_sel_hi:[0,0,1]
	ds_write_b16 v71, v82 offset:2304
	ds_write_b16 v71, v87 offset:2448
	ds_write_b16 v71, v92 offset:2592
	ds_write_b16 v71, v97 offset:2736
	ds_write_b16 v71, v84 offset:6912
	ds_write_b16 v71, v89 offset:7056
	ds_write_b16 v71, v94 offset:7200
	ds_write_b16 v71, v99 offset:7344
	v_fma_f32 v82, v10, s61, v141
	v_fma_f32 v87, v11, s61, v141
	v_fma_f32 v92, v12, s61, v141
	v_fma_f32 v97, v13, s61, v141
	v_fma_f32 v83, v10, s62, v145
	v_fma_f32 v88, v11, s62, v145
	v_fma_f32 v93, v12, s62, v145
	v_fma_f32 v98, v13, s62, v145
	v_mul_f32_e32 v84, v82, v82
	v_mul_f32_e32 v89, v87, v87
	v_mul_f32_e32 v94, v92, v92
	v_mul_f32_e32 v99, v97, v97
	v_cmp_lt_f32_e64 s[64:65], |v82|, 1.0
	v_cmp_lt_f32_e64 s[66:67], |v87|, 1.0
	v_cmp_lt_f32_e64 s[68:69], |v92|, 1.0
	v_cmp_lt_f32_e64 s[70:71], |v97|, 1.0
	v_fma_f32 v86, v84, v103, s56
	v_fma_f32 v91, v89, v103, s56
	v_fma_f32 v96, v94, v103, s56
	v_fma_f32 v101, v99, v103, s56
	s_and_b64 s[72:73], s[64:65], s[66:67]
	s_and_b64 s[74:75], s[68:69], s[70:71]
	s_and_b64 s[72:73], s[72:73], s[74:75]
	v_fma_f32 v86, v84, v86, s57
	v_fma_f32 v91, v89, v91, s57
	v_fma_f32 v96, v94, v96, s57
	v_fma_f32 v101, v99, v101, s57
	v_fma_f32 v86, v84, v86, s58
	v_fma_f32 v91, v89, v91, s58
	v_fma_f32 v96, v94, v96, s58
	v_fma_f32 v101, v99, v101, s58
	v_fma_f32 v86, v84, v86, s59
	v_fma_f32 v91, v89, v91, s59
	v_fma_f32 v96, v94, v96, s59
	v_fma_f32 v101, v99, v101, s59
	v_fma_f32 v86, v84, v86, s60
	v_fma_f32 v91, v89, v91, s60
	v_fma_f32 v96, v94, v96, s60
	v_fma_f32 v101, v99, v101, s60
	v_fma_f32 v86, |v82|, v86, |v82|
	v_fma_f32 v91, |v87|, v91, |v87|
	v_fma_f32 v96, |v92|, v96, |v92|
	v_fma_f32 v101, |v97|, v101, |v97|
	s_cmp_eq_u64 s[72:73], exec
	s_cbranch_scc1 .Lgsk_g3_13
	v_fma_f32 v85, |v82|, v102, s50
	v_fma_f32 v90, |v87|, v102, s50
	v_fma_f32 v95, |v92|, v102, s50
	v_fma_f32 v100, |v97|, v102, s50
	v_fma_f32 v85, |v82|, v85, s51
	v_fma_f32 v90, |v87|, v90, s51
	v_fma_f32 v95, |v92|, v95, s51
	v_fma_f32 v100, |v97|, v100, s51
	v_fma_f32 v85, |v82|, v85, s52
	v_fma_f32 v90, |v87|, v90, s52
	v_fma_f32 v95, |v92|, v95, s52
	v_fma_f32 v100, |v97|, v100, s52
	v_fma_f32 v85, |v82|, v85, s53
	v_fma_f32 v90, |v87|, v90, s53
	v_fma_f32 v95, |v92|, v95, s53
	v_fma_f32 v100, |v97|, v100, s53
	v_fma_f32 v85, |v82|, v85, s54
	v_fma_f32 v90, |v87|, v90, s54
	v_fma_f32 v95, |v92|, v95, s54
	v_fma_f32 v100, |v97|, v100, s54
	v_fma_f32 v85, |v82|, v85, s55
	v_fma_f32 v90, |v87|, v90, s55
	v_fma_f32 v95, |v92|, v95, s55
	v_fma_f32 v100, |v97|, v100, s55
	v_fma_f32 v85, |v82|, v85, |v82|
	v_fma_f32 v90, |v87|, v90, |v87|
	v_fma_f32 v95, |v92|, v95, |v92|
	v_fma_f32 v100, |v97|, v100, |v97|
	v_mul_f32_e32 v85, 0xbfb8aa3b, v85
	v_mul_f32_e32 v90, 0xbfb8aa3b, v90
	v_mul_f32_e32 v95, 0xbfb8aa3b, v95
	v_mul_f32_e32 v100, 0xbfb8aa3b, v100
	v_exp_f32_e32 v85, v85
	v_exp_f32_e32 v90, v90
	v_exp_f32_e32 v95, v95
	v_exp_f32_e32 v100, v100
	s_nop 0
	v_sub_f32_e32 v85, 1.0, v85
	v_sub_f32_e32 v90, 1.0, v90
	v_sub_f32_e32 v95, 1.0, v95
	v_sub_f32_e32 v100, 1.0, v100
	v_cndmask_b32_e64 v86, v85, v86, s[64:65]
	v_cndmask_b32_e64 v91, v90, v91, s[66:67]
	v_cndmask_b32_e64 v96, v95, v96, s[68:69]
	v_cndmask_b32_e64 v101, v100, v101, s[70:71]
.Lgsk_g3_13:
	v_fma_f32 v83, |v83|, v86, v83
	v_fma_f32 v88, |v88|, v91, v88
	v_fma_f32 v93, |v93|, v96, v93
	v_fma_f32 v98, |v98|, v101, v98
	v_cvt_f16_f32_e32 v82, v83
	v_cvt_f16_f32_e32 v87, v88
	v_cvt_f16_f32_e32 v92, v93
	v_cvt_f16_f32_e32 v97, v98
	v_fma_mixlo_f16 v84, v83, 1.0, -v82 op_sel_hi:[0,0,1]
	v_fma_mixlo_f16 v89, v88, 1.0, -v87 op_sel_hi:[0,0,1]
	v_fma_mixlo_f16 v94, v93, 1.0, -v92 op_sel_hi:[0,0,1]
	v_fma_mixlo_f16 v99, v98, 1.0, -v97 op_sel_hi:[0,0,1]
	ds_write_b16 v71, v82 offset:2336
	ds_write_b16 v71, v87 offset:2480
	ds_write_b16 v71, v92 offset:2624
	ds_write_b16 v71, v97 offset:2768
	ds_write_b16 v71, v84 offset:6944
	ds_write_b16 v71, v89 offset:7088
	ds_write_b16 v71, v94 offset:7232
	ds_write_b16 v71, v99 offset:7376
	v_fma_f32 v82, v6, s61, v142
	v_fma_f32 v87, v7, s61, v142
	v_fma_f32 v92, v8, s61, v142
	v_fma_f32 v97, v9, s61, v142
	v_fma_f32 v83, v6, s62, v146
	v_fma_f32 v88, v7, s62, v146
	v_fma_f32 v93, v8, s62, v146
	v_fma_f32 v98, v9, s62, v146
	v_mul_f32_e32 v84, v82, v82
	v_mul_f32_e32 v89, v87, v87
	v_mul_f32_e32 v94, v92, v92
	v_mul_f32_e32 v99, v97, v97
	v_cmp_lt_f32_e64 s[64:65], |v82|, 1.0
	v_cmp_lt_f32_e64 s[66:67], |v87|, 1.0
	v_cmp_lt_f32_e64 s[68:69], |v92|, 1.0
	v_cmp_lt_f32_e64 s[70:71], |v97|, 1.0
	v_fma_f32 v86, v84, v103, s56
	v_fma_f32 v91, v89, v103, s56
	v_fma_f32 v96, v94, v103, s56
	v_fma_f32 v101, v99, v103, s56
	s_and_b64 s[72:73], s[64:65], s[66:67]
	s_and_b64 s[74:75], s[68:69], s[70:71]
	s_and_b64 s[72:73], s[72:73], s[74:75]
	v_fma_f32 v86, v84, v86, s57
	v_fma_f32 v91, v89, v91, s57
	v_fma_f32 v96, v94, v96, s57
	v_fma_f32 v101, v99, v101, s57
	v_fma_f32 v86, v84, v86, s58
	v_fma_f32 v91, v89, v91, s58
	v_fma_f32 v96, v94, v96, s58
	v_fma_f32 v101, v99, v101, s58
	v_fma_f32 v86, v84, v86, s59
	v_fma_f32 v91, v89, v91, s59
	v_fma_f32 v96, v94, v96, s59
	v_fma_f32 v101, v99, v101, s59
	v_fma_f32 v86, v84, v86, s60
	v_fma_f32 v91, v89, v91, s60
	v_fma_f32 v96, v94, v96, s60
	v_fma_f32 v101, v99, v101, s60
	v_fma_f32 v86, |v82|, v86, |v82|
	v_fma_f32 v91, |v87|, v91, |v87|
	v_fma_f32 v96, |v92|, v96, |v92|
	v_fma_f32 v101, |v97|, v101, |v97|
	s_cmp_eq_u64 s[72:73], exec
	s_cbranch_scc1 .Lgsk_g3_14
	v_fma_f32 v85, |v82|, v102, s50
	v_fma_f32 v90, |v87|, v102, s50
	v_fma_f32 v95, |v92|, v102, s50
	v_fma_f32 v100, |v97|, v102, s50
	v_fma_f32 v85, |v82|, v85, s51
	v_fma_f32 v90, |v87|, v90, s51
	v_fma_f32 v95, |v92|, v95, s51
	v_fma_f32 v100, |v97|, v100, s51
	v_fma_f32 v85, |v82|, v85, s52
	v_fma_f32 v90, |v87|, v90, s52
	v_fma_f32 v95, |v92|, v95, s52
	v_fma_f32 v100, |v97|, v100, s52
	v_fma_f32 v85, |v82|, v85, s53
	v_fma_f32 v90, |v87|, v90, s53
	v_fma_f32 v95, |v92|, v95, s53
	v_fma_f32 v100, |v97|, v100, s53
	v_fma_f32 v85, |v82|, v85, s54
	v_fma_f32 v90, |v87|, v90, s54
	v_fma_f32 v95, |v92|, v95, s54
	v_fma_f32 v100, |v97|, v100, s54
	v_fma_f32 v85, |v82|, v85, s55
	v_fma_f32 v90, |v87|, v90, s55
	v_fma_f32 v95, |v92|, v95, s55
	v_fma_f32 v100, |v97|, v100, s55
	v_fma_f32 v85, |v82|, v85, |v82|
	v_fma_f32 v90, |v87|, v90, |v87|
	v_fma_f32 v95, |v92|, v95, |v92|
	v_fma_f32 v100, |v97|, v100, |v97|
	v_mul_f32_e32 v85, 0xbfb8aa3b, v85
	v_mul_f32_e32 v90, 0xbfb8aa3b, v90
	v_mul_f32_e32 v95, 0xbfb8aa3b, v95
	v_mul_f32_e32 v100, 0xbfb8aa3b, v100
	v_exp_f32_e32 v85, v85
	v_exp_f32_e32 v90, v90
	v_exp_f32_e32 v95, v95
	v_exp_f32_e32 v100, v100
	s_nop 0
	v_sub_f32_e32 v85, 1.0, v85
	v_sub_f32_e32 v90, 1.0, v90
	v_sub_f32_e32 v95, 1.0, v95
	v_sub_f32_e32 v100, 1.0, v100
	v_cndmask_b32_e64 v86, v85, v86, s[64:65]
	v_cndmask_b32_e64 v91, v90, v91, s[66:67]
	v_cndmask_b32_e64 v96, v95, v96, s[68:69]
	v_cndmask_b32_e64 v101, v100, v101, s[70:71]
.Lgsk_g3_14:
	v_fma_f32 v83, |v83|, v86, v83
	v_fma_f32 v88, |v88|, v91, v88
	v_fma_f32 v93, |v93|, v96, v93
	v_fma_f32 v98, |v98|, v101, v98
	v_cvt_f16_f32_e32 v82, v83
	v_cvt_f16_f32_e32 v87, v88
	v_cvt_f16_f32_e32 v92, v93
	v_cvt_f16_f32_e32 v97, v98
	v_fma_mixlo_f16 v84, v83, 1.0, -v82 op_sel_hi:[0,0,1]
	v_fma_mixlo_f16 v89, v88, 1.0, -v87 op_sel_hi:[0,0,1]
	v_fma_mixlo_f16 v94, v93, 1.0, -v92 op_sel_hi:[0,0,1]
	v_fma_mixlo_f16 v99, v98, 1.0, -v97 op_sel_hi:[0,0,1]
	ds_write_b16 v71, v82 offset:2368
	ds_write_b16 v71, v87 offset:2512
	ds_write_b16 v71, v92 offset:2656
	ds_write_b16 v71, v97 offset:2800
	ds_write_b16 v71, v84 offset:6976
	ds_write_b16 v71, v89 offset:7120
	ds_write_b16 v71, v94 offset:7264
	ds_write_b16 v71, v99 offset:7408
	v_fma_f32 v82, v2, s61, v143
	v_fma_f32 v87, v3, s61, v143
	v_fma_f32 v92, v4, s61, v143
	v_fma_f32 v97, v5, s61, v143
	v_fma_f32 v83, v2, s62, v147
	v_fma_f32 v88, v3, s62, v147
	v_fma_f32 v93, v4, s62, v147
	v_fma_f32 v98, v5, s62, v147
	v_mul_f32_e32 v84, v82, v82
	v_mul_f32_e32 v89, v87, v87
	v_mul_f32_e32 v94, v92, v92
	v_mul_f32_e32 v99, v97, v97
	v_cmp_lt_f32_e64 s[64:65], |v82|, 1.0
	v_cmp_lt_f32_e64 s[66:67], |v87|, 1.0
	v_cmp_lt_f32_e64 s[68:69], |v92|, 1.0
	v_cmp_lt_f32_e64 s[70:71], |v97|, 1.0
	v_fma_f32 v86, v84, v103, s56
	v_fma_f32 v91, v89, v103, s56
	v_fma_f32 v96, v94, v103, s56
	v_fma_f32 v101, v99, v103, s56
	s_and_b64 s[72:73], s[64:65], s[66:67]
	s_and_b64 s[74:75], s[68:69], s[70:71]
	s_and_b64 s[72:73], s[72:73], s[74:75]
	v_fma_f32 v86, v84, v86, s57
	v_fma_f32 v91, v89, v91, s57
	v_fma_f32 v96, v94, v96, s57
	v_fma_f32 v101, v99, v101, s57
	v_fma_f32 v86, v84, v86, s58
	v_fma_f32 v91, v89, v91, s58
	v_fma_f32 v96, v94, v96, s58
	v_fma_f32 v101, v99, v101, s58
	v_fma_f32 v86, v84, v86, s59
	v_fma_f32 v91, v89, v91, s59
	v_fma_f32 v96, v94, v96, s59
	v_fma_f32 v101, v99, v101, s59
	v_fma_f32 v86, v84, v86, s60
	v_fma_f32 v91, v89, v91, s60
	v_fma_f32 v96, v94, v96, s60
	v_fma_f32 v101, v99, v101, s60
	v_fma_f32 v86, |v82|, v86, |v82|
	v_fma_f32 v91, |v87|, v91, |v87|
	v_fma_f32 v96, |v92|, v96, |v92|
	v_fma_f32 v101, |v97|, v101, |v97|
	s_cmp_eq_u64 s[72:73], exec
	s_cbranch_scc1 .Lgsk_g3_15
	v_fma_f32 v85, |v82|, v102, s50
	v_fma_f32 v90, |v87|, v102, s50
	v_fma_f32 v95, |v92|, v102, s50
	v_fma_f32 v100, |v97|, v102, s50
	v_fma_f32 v85, |v82|, v85, s51
	v_fma_f32 v90, |v87|, v90, s51
	v_fma_f32 v95, |v92|, v95, s51
	v_fma_f32 v100, |v97|, v100, s51
	v_fma_f32 v85, |v82|, v85, s52
	v_fma_f32 v90, |v87|, v90, s52
	v_fma_f32 v95, |v92|, v95, s52
	v_fma_f32 v100, |v97|, v100, s52
	v_fma_f32 v85, |v82|, v85, s53
	v_fma_f32 v90, |v87|, v90, s53
	v_fma_f32 v95, |v92|, v95, s53
	v_fma_f32 v100, |v97|, v100, s53
	v_fma_f32 v85, |v82|, v85, s54
	v_fma_f32 v90, |v87|, v90, s54
	v_fma_f32 v95, |v92|, v95, s54
	v_fma_f32 v100, |v97|, v100, s54
	v_fma_f32 v85, |v82|, v85, s55
	v_fma_f32 v90, |v87|, v90, s55
	v_fma_f32 v95, |v92|, v95, s55
	v_fma_f32 v100, |v97|, v100, s55
	v_fma_f32 v85, |v82|, v85, |v82|
	v_fma_f32 v90, |v87|, v90, |v87|
	v_fma_f32 v95, |v92|, v95, |v92|
	v_fma_f32 v100, |v97|, v100, |v97|
	v_mul_f32_e32 v85, 0xbfb8aa3b, v85
	v_mul_f32_e32 v90, 0xbfb8aa3b, v90
	v_mul_f32_e32 v95, 0xbfb8aa3b, v95
	v_mul_f32_e32 v100, 0xbfb8aa3b, v100
	v_exp_f32_e32 v85, v85
	v_exp_f32_e32 v90, v90
	v_exp_f32_e32 v95, v95
	v_exp_f32_e32 v100, v100
	s_nop 0
	v_sub_f32_e32 v85, 1.0, v85
	v_sub_f32_e32 v90, 1.0, v90
	v_sub_f32_e32 v95, 1.0, v95
	v_sub_f32_e32 v100, 1.0, v100
	v_cndmask_b32_e64 v86, v85, v86, s[64:65]
	v_cndmask_b32_e64 v91, v90, v91, s[66:67]
	v_cndmask_b32_e64 v96, v95, v96, s[68:69]
	v_cndmask_b32_e64 v101, v100, v101, s[70:71]
.Lgsk_g3_15:
	v_fma_f32 v83, |v83|, v86, v83
	v_fma_f32 v88, |v88|, v91, v88
	v_fma_f32 v93, |v93|, v96, v93
	v_fma_f32 v98, |v98|, v101, v98
	v_cvt_f16_f32_e32 v82, v83
	v_cvt_f16_f32_e32 v87, v88
	v_cvt_f16_f32_e32 v92, v93
	v_cvt_f16_f32_e32 v97, v98
	v_fma_mixlo_f16 v84, v83, 1.0, -v82 op_sel_hi:[0,0,1]
	v_fma_mixlo_f16 v89, v88, 1.0, -v87 op_sel_hi:[0,0,1]
	v_fma_mixlo_f16 v94, v93, 1.0, -v92 op_sel_hi:[0,0,1]
	v_fma_mixlo_f16 v99, v98, 1.0, -v97 op_sel_hi:[0,0,1]
	ds_write_b16 v71, v82 offset:2400
	ds_write_b16 v71, v87 offset:2544
	ds_write_b16 v71, v92 offset:2688
	ds_write_b16 v71, v97 offset:2832
	ds_write_b16 v71, v84 offset:7008
	ds_write_b16 v71, v89 offset:7152
	ds_write_b16 v71, v94 offset:7296
	ds_write_b16 v71, v99 offset:7440
	ds_read_b128 v[104:107], v74
	ds_read_b128 v[108:111], v74 offset:1152
	ds_read_b128 v[112:115], v74 offset:2304
	ds_read_b128 v[116:119], v74 offset:3456
	ds_read_b128 v[120:123], v74 offset:4608
	ds_read_b128 v[124:127], v74 offset:5760
	ds_read_b128 v[128:131], v74 offset:6912
	ds_read_b128 v[132:135], v74 offset:8064
	s_waitcnt lgkmcnt(0)
	s_sub_i32 s2, s42, 32
	v_cmp_gt_i32_e32 vcc, s2, v75
	s_and_saveexec_b64 s[44:45], vcc
	s_add_u32 s2, s38, 0x20000
	s_addc_u32 s3, s39, 0
	global_store_dwordx4 v76, v[104:107], s[2:3]
	s_add_u32 s2, s40, 0x20000
	s_addc_u32 s3, s41, 0
	global_store_dwordx4 v76, v[120:123], s[2:3]
	s_mov_b64 exec, s[44:45]
	s_sub_i32 s2, s42, 40
	v_cmp_gt_i32_e32 vcc, s2, v75
	s_and_saveexec_b64 s[44:45], vcc
	s_add_u32 s2, s38, 0x28000
	s_addc_u32 s3, s39, 0
	global_store_dwordx4 v76, v[108:111], s[2:3]
	s_add_u32 s2, s40, 0x28000
	s_addc_u32 s3, s41, 0
	global_store_dwordx4 v76, v[124:127], s[2:3]
	s_mov_b64 exec, s[44:45]
	s_sub_i32 s2, s42, 48
	v_cmp_gt_i32_e32 vcc, s2, v75
	s_and_saveexec_b64 s[44:45], vcc
	s_add_u32 s2, s38, 0x30000
	s_addc_u32 s3, s39, 0
	global_store_dwordx4 v76, v[112:115], s[2:3]
	s_add_u32 s2, s40, 0x30000
	s_addc_u32 s3, s41, 0
	global_store_dwordx4 v76, v[128:131], s[2:3]
	s_mov_b64 exec, s[44:45]
	s_sub_i32 s2, s42, 56
	v_cmp_gt_i32_e32 vcc, s2, v75
	s_and_saveexec_b64 s[44:45], vcc
	s_add_u32 s2, s38, 0x38000
	s_addc_u32 s3, s39, 0
	global_store_dwordx4 v76, v[116:119], s[2:3]
	s_add_u32 s2, s40, 0x38000
	s_addc_u32 s3, s41, 0
	global_store_dwordx4 v76, v[132:135], s[2:3]
	s_mov_b64 exec, s[44:45]
	s_endpgm

.LBB10_47:
.Lepi_again_g1:
	s_mov_b32 s24, s17
	s_mov_b32 s25, s14
	s_mov_b32 s26, s16
	s_mov_b32 s27, s18
	s_load_dwordx2 s[28:29], s[0:1], 0x58
	s_load_dwordx2 s[30:31], s[0:1], 0x60
	s_load_dwordx4 s[32:35], s[0:1], 0x88
	v_and_b32_e32 v66, 63, v0
	v_lshrrev_b32_e32 v67, 6, v0
	v_and_b32_e32 v68, 15, v0
	v_bfe_u32 v69, v0, 4, 2
	v_mul_u32_u24_e32 v70, 0x2000, v67
	s_movk_i32 s2, 0x240
	v_mad_u32_u24 v71, v69, s2, v70
	v_lshl_add_u32 v71, v68, 1, v71
	v_lshrrev_b32_e32 v72, 3, v66
	v_and_b32_e32 v73, 7, v66
	s_movk_i32 s3, 0x90
	v_mad_u32_u24 v74, v72, s3, v70
	v_lshl_add_u32 v74, v73, 4, v74
	v_lshrrev_b32_e32 v75, 1, v67
	v_lshl_add_u32 v75, v75, 6, v72
	v_and_b32_e32 v76, 1, v67
	v_lshlrev_b32_e32 v76, 7, v76
	v_lshl_add_u32 v76, v75, 12, v76
	v_lshl_add_u32 v76, v73, 4, v76
	v_and_b32_e32 v77, 0x4f, v0
	v_lshlrev_b32_e32 v77, 2, v77
	s_waitcnt lgkmcnt(0)
	s_mul_i32 s2, s24, s30
	s_add_i32 s2, s2, s27
	s_lshl_b32 s2, s2, 2
	s_add_u32 s36, s28, s2
	s_addc_u32 s37, s29, 0
	global_load_dword v78, v77, s[36:37]
	global_load_dword v79, v77, s[36:37] offset:64
	global_load_dword v80, v77, s[36:37] offset:128
	global_load_dword v81, v77, s[36:37] offset:192
	s_lshl_b32 s2, s25, 12
	s_lshl_b32 s3, s27, 1
	s_add_u32 s2, s2, s3
	s_add_u32 s38, s32, s2
	s_addc_u32 s39, s33, 0
	s_add_u32 s40, s34, s2
	s_addc_u32 s41, s35, 0
	s_sub_i32 s42, s26, s25
	s_mov_b32 s50, 0xb9c68948
	s_mov_b32 s51, 0x3b7cd369
	s_mov_b32 s52, 0xbcc618b2
	s_mov_b32 s53, 0x3dda74e4
	s_mov_b32 s54, 0x3f228afd
	s_mov_b32 s55, 0x3e03c728
	s_mov_b32 s56, 0x3ba10414
	s_mov_b32 s57, 0xbcdac9b8
	s_mov_b32 s58, 0x3de703be
	s_mov_b32 s59, 0xbec09330
	s_mov_b32 s60, 0x3e0375d0
	s_mov_b32 s61, 0x353504f3
	s_mov_b32 s62, 0x39000000
	v_mov_b32_e32 v102, 0x378e98ab
	v_mov_b32_e32 v103, 0xba1345e1
	s_waitcnt vmcnt(0)
	v_mul_f32_e32 v136, 0x3f3504f3, v78
	v_mul_f32_e32 v140, 0x43000000, v78
	v_mul_f32_e32 v137, 0x3f3504f3, v79
	v_mul_f32_e32 v141, 0x43000000, v79
	v_mul_f32_e32 v138, 0x3f3504f3, v80
	v_mul_f32_e32 v142, 0x43000000, v80
	v_mul_f32_e32 v139, 0x3f3504f3, v81
	v_mul_f32_e32 v143, 0x43000000, v81
	v_fma_f32 v82, v62, s61, v136
	v_fma_f32 v87, v63, s61, v136
	v_fma_f32 v92, v64, s61, v136
	v_fma_f32 v97, v65, s61, v136
	v_fma_f32 v83, v62, s62, v140
	v_fma_f32 v88, v63, s62, v140
	v_fma_f32 v93, v64, s62, v140
	v_fma_f32 v98, v65, s62, v140
	v_mul_f32_e32 v84, v82, v82
	v_mul_f32_e32 v89, v87, v87
	v_mul_f32_e32 v94, v92, v92
	v_mul_f32_e32 v99, v97, v97
	v_cmp_lt_f32_e64 s[64:65], |v82|, 1.0
	v_cmp_lt_f32_e64 s[66:67], |v87|, 1.0
	v_cmp_lt_f32_e64 s[68:69], |v92|, 1.0
	v_cmp_lt_f32_e64 s[70:71], |v97|, 1.0
	v_fma_f32 v86, v84, v103, s56
	v_fma_f32 v91, v89, v103, s56
	v_fma_f32 v96, v94, v103, s56
	v_fma_f32 v101, v99, v103, s56
	s_and_b64 s[72:73], s[64:65], s[66:67]
	s_and_b64 s[74:75], s[68:69], s[70:71]
	s_and_b64 s[72:73], s[72:73], s[74:75]
	v_fma_f32 v86, v84, v86, s57
	v_fma_f32 v91, v89, v91, s57
	v_fma_f32 v96, v94, v96, s57
	v_fma_f32 v101, v99, v101, s57
	v_fma_f32 v86, v84, v86, s58
	v_fma_f32 v91, v89, v91, s58
	v_fma_f32 v96, v94, v96, s58
	v_fma_f32 v101, v99, v101, s58
	v_fma_f32 v86, v84, v86, s59
	v_fma_f32 v91, v89, v91, s59
	v_fma_f32 v96, v94, v96, s59
	v_fma_f32 v101, v99, v101, s59
	v_fma_f32 v86, v84, v86, s60
	v_fma_f32 v91, v89, v91, s60
	v_fma_f32 v96, v94, v96, s60
	v_fma_f32 v101, v99, v101, s60
	v_fma_f32 v86, |v82|, v86, |v82|
	v_fma_f32 v91, |v87|, v91, |v87|
	v_fma_f32 v96, |v92|, v96, |v92|
	v_fma_f32 v101, |v97|, v101, |v97|
	s_cmp_eq_u64 s[72:73], exec
	s_cbranch_scc1 .Lgsk_g1_0
	v_fma_f32 v85, |v82|, v102, s50
	v_fma_f32 v90, |v87|, v102, s50
	v_fma_f32 v95, |v92|, v102, s50
	v_fma_f32 v100, |v97|, v102, s50
	v_fma_f32 v85, |v82|, v85, s51
	v_fma_f32 v90, |v87|, v90, s51
	v_fma_f32 v95, |v92|, v95, s51
	v_fma_f32 v100, |v97|, v100, s51
	v_fma_f32 v85, |v82|, v85, s52
	v_fma_f32 v90, |v87|, v90, s52
	v_fma_f32 v95, |v92|, v95, s52
	v_fma_f32 v100, |v97|, v100, s52
	v_fma_f32 v85, |v82|, v85, s53
	v_fma_f32 v90, |v87|, v90, s53
	v_fma_f32 v95, |v92|, v95, s53
	v_fma_f32 v100, |v97|, v100, s53
	v_fma_f32 v85, |v82|, v85, s54
	v_fma_f32 v90, |v87|, v90, s54
	v_fma_f32 v95, |v92|, v95, s54
	v_fma_f32 v100, |v97|, v100, s54
	v_fma_f32 v85, |v82|, v85, s55
	v_fma_f32 v90, |v87|, v90, s55
	v_fma_f32 v95, |v92|, v95, s55
	v_fma_f32 v100, |v97|, v100, s55
	v_fma_f32 v85, |v82|, v85, |v82|
	v_fma_f32 v90, |v87|, v90, |v87|
	v_fma_f32 v95, |v92|, v95, |v92|
	v_fma_f32 v100, |v97|, v100, |v97|
	v_mul_f32_e32 v85, 0xbfb8aa3b, v85
	v_mul_f32_e32 v90, 0xbfb8aa3b, v90
	v_mul_f32_e32 v95, 0xbfb8aa3b, v95
	v_mul_f32_e32 v100, 0xbfb8aa3b, v100
	v_exp_f32_e32 v85, v85
	v_exp_f32_e32 v90, v90
	v_exp_f32_e32 v95, v95
	v_exp_f32_e32 v100, v100
	s_nop 0
	v_sub_f32_e32 v85, 1.0, v85
	v_sub_f32_e32 v90, 1.0, v90
	v_sub_f32_e32 v95, 1.0, v95
	v_sub_f32_e32 v100, 1.0, v100
	v_cndmask_b32_e64 v86, v85, v86, s[64:65]
	v_cndmask_b32_e64 v91, v90, v91, s[66:67]
	v_cndmask_b32_e64 v96, v95, v96, s[68:69]
	v_cndmask_b32_e64 v101, v100, v101, s[70:71]
.Lgsk_g1_0:
	v_fma_f32 v83, |v83|, v86, v83
	v_fma_f32 v88, |v88|, v91, v88
	v_fma_f32 v93, |v93|, v96, v93
	v_fma_f32 v98, |v98|, v101, v98
	v_cvt_f16_f32_e32 v82, v83
	v_cvt_f16_f32_e32 v87, v88
	v_cvt_f16_f32_e32 v92, v93
	v_cvt_f16_f32_e32 v97, v98
	ds_write_b16 v71, v82
	ds_write_b16 v71, v87 offset:144
	ds_write_b16 v71, v92 offset:288
	ds_write_b16 v71, v97 offset:432
	v_fma_f32 v82, v58, s61, v137
	v_fma_f32 v87, v59, s61, v137
	v_fma_f32 v92, v60, s61, v137
	v_fma_f32 v97, v61, s61, v137
	v_fma_f32 v83, v58, s62, v141
	v_fma_f32 v88, v59, s62, v141
	v_fma_f32 v93, v60, s62, v141
	v_fma_f32 v98, v61, s62, v141
	v_mul_f32_e32 v84, v82, v82
	v_mul_f32_e32 v89, v87, v87
	v_mul_f32_e32 v94, v92, v92
	v_mul_f32_e32 v99, v97, v97
	v_cmp_lt_f32_e64 s[64:65], |v82|, 1.0
	v_cmp_lt_f32_e64 s[66:67], |v87|, 1.0
	v_cmp_lt_f32_e64 s[68:69], |v92|, 1.0
	v_cmp_lt_f32_e64 s[70:71], |v97|, 1.0
	v_fma_f32 v86, v84, v103, s56
	v_fma_f32 v91, v89, v103, s56
	v_fma_f32 v96, v94, v103, s56
	v_fma_f32 v101, v99, v103, s56
	s_and_b64 s[72:73], s[64:65], s[66:67]
	s_and_b64 s[74:75], s[68:69], s[70:71]
	s_and_b64 s[72:73], s[72:73], s[74:75]
	v_fma_f32 v86, v84, v86, s57
	v_fma_f32 v91, v89, v91, s57
	v_fma_f32 v96, v94, v96, s57
	v_fma_f32 v101, v99, v101, s57
	v_fma_f32 v86, v84, v86, s58
	v_fma_f32 v91, v89, v91, s58
	v_fma_f32 v96, v94, v96, s58
	v_fma_f32 v101, v99, v101, s58
	v_fma_f32 v86, v84, v86, s59
	v_fma_f32 v91, v89, v91, s59
	v_fma_f32 v96, v94, v96, s59
	v_fma_f32 v101, v99, v101, s59
	v_fma_f32 v86, v84, v86, s60
	v_fma_f32 v91, v89, v91, s60
	v_fma_f32 v96, v94, v96, s60
	v_fma_f32 v101, v99, v101, s60
	v_fma_f32 v86, |v82|, v86, |v82|
	v_fma_f32 v91, |v87|, v91, |v87|
	v_fma_f32 v96, |v92|, v96, |v92|
	v_fma_f32 v101, |v97|, v101, |v97|
	s_cmp_eq_u64 s[72:73], exec
	s_cbranch_scc1 .Lgsk_g1_1
	v_fma_f32 v85, |v82|, v102, s50
	v_fma_f32 v90, |v87|, v102, s50
	v_fma_f32 v95, |v92|, v102, s50
	v_fma_f32 v100, |v97|, v102, s50
	v_fma_f32 v85, |v82|, v85, s51
	v_fma_f32 v90, |v87|, v90, s51
	v_fma_f32 v95, |v92|, v95, s51
	v_fma_f32 v100, |v97|, v100, s51
	v_fma_f32 v85, |v82|, v85, s52
	v_fma_f32 v90, |v87|, v90, s52
	v_fma_f32 v95, |v92|, v95, s52
	v_fma_f32 v100, |v97|, v100, s52
	v_fma_f32 v85, |v82|, v85, s53
	v_fma_f32 v90, |v87|, v90, s53
	v_fma_f32 v95, |v92|, v95, s53
	v_fma_f32 v100, |v97|, v100, s53
	v_fma_f32 v85, |v82|, v85, s54
	v_fma_f32 v90, |v87|, v90, s54
	v_fma_f32 v95, |v92|, v95, s54
	v_fma_f32 v100, |v97|, v100, s54
	v_fma_f32 v85, |v82|, v85, s55
	v_fma_f32 v90, |v87|, v90, s55
	v_fma_f32 v95, |v92|, v95, s55
	v_fma_f32 v100, |v97|, v100, s55
	v_fma_f32 v85, |v82|, v85, |v82|
	v_fma_f32 v90, |v87|, v90, |v87|
	v_fma_f32 v95, |v92|, v95, |v92|
	v_fma_f32 v100, |v97|, v100, |v97|
	v_mul_f32_e32 v85, 0xbfb8aa3b, v85
	v_mul_f32_e32 v90, 0xbfb8aa3b, v90
	v_mul_f32_e32 v95, 0xbfb8aa3b, v95
	v_mul_f32_e32 v100, 0xbfb8aa3b, v100
	v_exp_f32_e32 v85, v85
	v_exp_f32_e32 v90, v90
	v_exp_f32_e32 v95, v95
	v_exp_f32_e32 v100, v100
	s_nop 0
	v_sub_f32_e32 v85, 1.0, v85
	v_sub_f32_e32 v90, 1.0, v90
	v_sub_f32_e32 v95, 1.0, v95
	v_sub_f32_e32 v100, 1.0, v100
	v_cndmask_b32_e64 v86, v85, v86, s[64:65]
	v_cndmask_b32_e64 v91, v90, v91, s[66:67]
	v_cndmask_b32_e64 v96, v95, v96, s[68:69]
	v_cndmask_b32_e64 v101, v100, v101, s[70:71]
.Lgsk_g1_1:
	v_fma_f32 v83, |v83|, v86, v83
	v_fma_f32 v88, |v88|, v91, v88
	v_fma_f32 v93, |v93|, v96, v93
	v_fma_f32 v98, |v98|, v101, v98
	v_cvt_f16_f32_e32 v82, v83
	v_cvt_f16_f32_e32 v87, v88
	v_cvt_f16_f32_e32 v92, v93
	v_cvt_f16_f32_e32 v97, v98
	ds_write_b16 v71, v82 offset:32
	ds_write_b16 v71, v87 offset:176
	ds_write_b16 v71, v92 offset:320
	ds_write_b16 v71, v97 offset:464
	v_fma_f32 v82, v54, s61, v138
	v_fma_f32 v87, v55, s61, v138
	v_fma_f32 v92, v56, s61, v138
	v_fma_f32 v97, v57, s61, v138
	v_fma_f32 v83, v54, s62, v142
	v_fma_f32 v88, v55, s62, v142
	v_fma_f32 v93, v56, s62, v142
	v_fma_f32 v98, v57, s62, v142
	v_mul_f32_e32 v84, v82, v82
	v_mul_f32_e32 v89, v87, v87
	v_mul_f32_e32 v94, v92, v92
	v_mul_f32_e32 v99, v97, v97
	v_cmp_lt_f32_e64 s[64:65], |v82|, 1.0
	v_cmp_lt_f32_e64 s[66:67], |v87|, 1.0
	v_cmp_lt_f32_e64 s[68:69], |v92|, 1.0
	v_cmp_lt_f32_e64 s[70:71], |v97|, 1.0
	v_fma_f32 v86, v84, v103, s56
	v_fma_f32 v91, v89, v103, s56
	v_fma_f32 v96, v94, v103, s56
	v_fma_f32 v101, v99, v103, s56
	s_and_b64 s[72:73], s[64:65], s[66:67]
	s_and_b64 s[74:75], s[68:69], s[70:71]
	s_and_b64 s[72:73], s[72:73], s[74:75]
	v_fma_f32 v86, v84, v86, s57
	v_fma_f32 v91, v89, v91, s57
	v_fma_f32 v96, v94, v96, s57
	v_fma_f32 v101, v99, v101, s57
	v_fma_f32 v86, v84, v86, s58
	v_fma_f32 v91, v89, v91, s58
	v_fma_f32 v96, v94, v96, s58
	v_fma_f32 v101, v99, v101, s58
	v_fma_f32 v86, v84, v86, s59
	v_fma_f32 v91, v89, v91, s59
	v_fma_f32 v96, v94, v96, s59
	v_fma_f32 v101, v99, v101, s59
	v_fma_f32 v86, v84, v86, s60
	v_fma_f32 v91, v89, v91, s60
	v_fma_f32 v96, v94, v96, s60
	v_fma_f32 v101, v99, v101, s60
	v_fma_f32 v86, |v82|, v86, |v82|
	v_fma_f32 v91, |v87|, v91, |v87|
	v_fma_f32 v96, |v92|, v96, |v92|
	v_fma_f32 v101, |v97|, v101, |v97|
	s_cmp_eq_u64 s[72:73], exec
	s_cbranch_scc1 .Lgsk_g1_2
	v_fma_f32 v85, |v82|, v102, s50
	v_fma_f32 v90, |v87|, v102, s50
	v_fma_f32 v95, |v92|, v102, s50
	v_fma_f32 v100, |v97|, v102, s50
	v_fma_f32 v85, |v82|, v85, s51
	v_fma_f32 v90, |v87|, v90, s51
	v_fma_f32 v95, |v92|, v95, s51
	v_fma_f32 v100, |v97|, v100, s51
	v_fma_f32 v85, |v82|, v85, s52
	v_fma_f32 v90, |v87|, v90, s52
	v_fma_f32 v95, |v92|, v95, s52
	v_fma_f32 v100, |v97|, v100, s52
	v_fma_f32 v85, |v82|, v85, s53
	v_fma_f32 v90, |v87|, v90, s53
	v_fma_f32 v95, |v92|, v95, s53
	v_fma_f32 v100, |v97|, v100, s53
	v_fma_f32 v85, |v82|, v85, s54
	v_fma_f32 v90, |v87|, v90, s54
	v_fma_f32 v95, |v92|, v95, s54
	v_fma_f32 v100, |v97|, v100, s54
	v_fma_f32 v85, |v82|, v85, s55
	v_fma_f32 v90, |v87|, v90, s55
	v_fma_f32 v95, |v92|, v95, s55
	v_fma_f32 v100, |v97|, v100, s55
	v_fma_f32 v85, |v82|, v85, |v82|
	v_fma_f32 v90, |v87|, v90, |v87|
	v_fma_f32 v95, |v92|, v95, |v92|
	v_fma_f32 v100, |v97|, v100, |v97|
	v_mul_f32_e32 v85, 0xbfb8aa3b, v85
	v_mul_f32_e32 v90, 0xbfb8aa3b, v90
	v_mul_f32_e32 v95, 0xbfb8aa3b, v95
	v_mul_f32_e32 v100, 0xbfb8aa3b, v100
	v_exp_f32_e32 v85, v85
	v_exp_f32_e32 v90, v90
	v_exp_f32_e32 v95, v95
	v_exp_f32_e32 v100, v100
	s_nop 0
	v_sub_f32_e32 v85, 1.0, v85
	v_sub_f32_e32 v90, 1.0, v90
	v_sub_f32_e32 v95, 1.0, v95
	v_sub_f32_e32 v100, 1.0, v100
	v_cndmask_b32_e64 v86, v85, v86, s[64:65]
	v_cndmask_b32_e64 v91, v90, v91, s[66:67]
	v_cndmask_b32_e64 v96, v95, v96, s[68:69]
	v_cndmask_b32_e64 v101, v100, v101, s[70:71]
.Lgsk_g1_2:
	v_fma_f32 v83, |v83|, v86, v83
	v_fma_f32 v88, |v88|, v91, v88
	v_fma_f32 v93, |v93|, v96, v93
	v_fma_f32 v98, |v98|, v101, v98
	v_cvt_f16_f32_e32 v82, v83
	v_cvt_f16_f32_e32 v87, v88
	v_cvt_f16_f32_e32 v92, v93
	v_cvt_f16_f32_e32 v97, v98
	ds_write_b16 v71, v82 offset:64
	ds_write_b16 v71, v87 offset:208
	ds_write_b16 v71, v92 offset:352
	ds_write_b16 v71, v97 offset:496
	v_fma_f32 v82, v50, s61, v139
	v_fma_f32 v87, v51, s61, v139
	v_fma_f32 v92, v52, s61, v139
	v_fma_f32 v97, v53, s61, v139
	v_fma_f32 v83, v50, s62, v143
	v_fma_f32 v88, v51, s62, v143
	v_fma_f32 v93, v52, s62, v143
	v_fma_f32 v98, v53, s62, v143
	v_mul_f32_e32 v84, v82, v82
	v_mul_f32_e32 v89, v87, v87
	v_mul_f32_e32 v94, v92, v92
	v_mul_f32_e32 v99, v97, v97
	v_cmp_lt_f32_e64 s[64:65], |v82|, 1.0
	v_cmp_lt_f32_e64 s[66:67], |v87|, 1.0
	v_cmp_lt_f32_e64 s[68:69], |v92|, 1.0
	v_cmp_lt_f32_e64 s[70:71], |v97|, 1.0
	v_fma_f32 v86, v84, v103, s56
	v_fma_f32 v91, v89, v103, s56
	v_fma_f32 v96, v94, v103, s56
	v_fma_f32 v101, v99, v103, s56
	s_and_b64 s[72:73], s[64:65], s[66:67]
	s_and_b64 s[74:75], s[68:69], s[70:71]
	s_and_b64 s[72:73], s[72:73], s[74:75]
	v_fma_f32 v86, v84, v86, s57
	v_fma_f32 v91, v89, v91, s57
	v_fma_f32 v96, v94, v96, s57
	v_fma_f32 v101, v99, v101, s57
	v_fma_f32 v86, v84, v86, s58
	v_fma_f32 v91, v89, v91, s58
	v_fma_f32 v96, v94, v96, s58
	v_fma_f32 v101, v99, v101, s58
	v_fma_f32 v86, v84, v86, s59
	v_fma_f32 v91, v89, v91, s59
	v_fma_f32 v96, v94, v96, s59
	v_fma_f32 v101, v99, v101, s59
	v_fma_f32 v86, v84, v86, s60
	v_fma_f32 v91, v89, v91, s60
	v_fma_f32 v96, v94, v96, s60
	v_fma_f32 v101, v99, v101, s60
	v_fma_f32 v86, |v82|, v86, |v82|
	v_fma_f32 v91, |v87|, v91, |v87|
	v_fma_f32 v96, |v92|, v96, |v92|
	v_fma_f32 v101, |v97|, v101, |v97|
	s_cmp_eq_u64 s[72:73], exec
	s_cbranch_scc1 .Lgsk_g1_3
	v_fma_f32 v85, |v82|, v102, s50
	v_fma_f32 v90, |v87|, v102, s50
	v_fma_f32 v95, |v92|, v102, s50
	v_fma_f32 v100, |v97|, v102, s50
	v_fma_f32 v85, |v82|, v85, s51
	v_fma_f32 v90, |v87|, v90, s51
	v_fma_f32 v95, |v92|, v95, s51
	v_fma_f32 v100, |v97|, v100, s51
	v_fma_f32 v85, |v82|, v85, s52
	v_fma_f32 v90, |v87|, v90, s52
	v_fma_f32 v95, |v92|, v95, s52
	v_fma_f32 v100, |v97|, v100, s52
	v_fma_f32 v85, |v82|, v85, s53
	v_fma_f32 v90, |v87|, v90, s53
	v_fma_f32 v95, |v92|, v95, s53
	v_fma_f32 v100, |v97|, v100, s53
	v_fma_f32 v85, |v82|, v85, s54
	v_fma_f32 v90, |v87|, v90, s54
	v_fma_f32 v95, |v92|, v95, s54
	v_fma_f32 v100, |v97|, v100, s54
	v_fma_f32 v85, |v82|, v85, s55
	v_fma_f32 v90, |v87|, v90, s55
	v_fma_f32 v95, |v92|, v95, s55
	v_fma_f32 v100, |v97|, v100, s55
	v_fma_f32 v85, |v82|, v85, |v82|
	v_fma_f32 v90, |v87|, v90, |v87|
	v_fma_f32 v95, |v92|, v95, |v92|
	v_fma_f32 v100, |v97|, v100, |v97|
	v_mul_f32_e32 v85, 0xbfb8aa3b, v85
	v_mul_f32_e32 v90, 0xbfb8aa3b, v90
	v_mul_f32_e32 v95, 0xbfb8aa3b, v95
	v_mul_f32_e32 v100, 0xbfb8aa3b, v100
	v_exp_f32_e32 v85, v85
	v_exp_f32_e32 v90, v90
	v_exp_f32_e32 v95, v95
	v_exp_f32_e32 v100, v100
	s_nop 0
	v_sub_f32_e32 v85, 1.0, v85
	v_sub_f32_e32 v90, 1.0, v90
	v_sub_f32_e32 v95, 1.0, v95
	v_sub_f32_e32 v100, 1.0, v100
	v_cndmask_b32_e64 v86, v85, v86, s[64:65]
	v_cndmask_b32_e64 v91, v90, v91, s[66:67]
	v_cndmask_b32_e64 v96, v95, v96, s[68:69]
	v_cndmask_b32_e64 v101, v100, v101, s[70:71]
.Lgsk_g1_3:
	v_fma_f32 v83, |v83|, v86, v83
	v_fma_f32 v88, |v88|, v91, v88
	v_fma_f32 v93, |v93|, v96, v93
	v_fma_f32 v98, |v98|, v101, v98
	v_cvt_f16_f32_e32 v82, v83
	v_cvt_f16_f32_e32 v87, v88
	v_cvt_f16_f32_e32 v92, v93
	v_cvt_f16_f32_e32 v97, v98
	ds_write_b16 v71, v82 offset:96
	ds_write_b16 v71, v87 offset:240
	ds_write_b16 v71, v92 offset:384
	ds_write_b16 v71, v97 offset:528
	v_fma_f32 v82, v46, s61, v136
	v_fma_f32 v87, v47, s61, v136
	v_fma_f32 v92, v48, s61, v136
	v_fma_f32 v97, v49, s61, v136
	v_fma_f32 v83, v46, s62, v140
	v_fma_f32 v88, v47, s62, v140
	v_fma_f32 v93, v48, s62, v140
	v_fma_f32 v98, v49, s62, v140
	v_mul_f32_e32 v84, v82, v82
	v_mul_f32_e32 v89, v87, v87
	v_mul_f32_e32 v94, v92, v92
	v_mul_f32_e32 v99, v97, v97
	v_cmp_lt_f32_e64 s[64:65], |v82|, 1.0
	v_cmp_lt_f32_e64 s[66:67], |v87|, 1.0
	v_cmp_lt_f32_e64 s[68:69], |v92|, 1.0
	v_cmp_lt_f32_e64 s[70:71], |v97|, 1.0
	v_fma_f32 v86, v84, v103, s56
	v_fma_f32 v91, v89, v103, s56
	v_fma_f32 v96, v94, v103, s56
	v_fma_f32 v101, v99, v103, s56
	s_and_b64 s[72:73], s[64:65], s[66:67]
	s_and_b64 s[74:75], s[68:69], s[70:71]
	s_and_b64 s[72:73], s[72:73], s[74:75]
	v_fma_f32 v86, v84, v86, s57
	v_fma_f32 v91, v89, v91, s57
	v_fma_f32 v96, v94, v96, s57
	v_fma_f32 v101, v99, v101, s57
	v_fma_f32 v86, v84, v86, s58
	v_fma_f32 v91, v89, v91, s58
	v_fma_f32 v96, v94, v96, s58
	v_fma_f32 v101, v99, v101, s58
	v_fma_f32 v86, v84, v86, s59
	v_fma_f32 v91, v89, v91, s59
	v_fma_f32 v96, v94, v96, s59
	v_fma_f32 v101, v99, v101, s59
	v_fma_f32 v86, v84, v86, s60
	v_fma_f32 v91, v89, v91, s60
	v_fma_f32 v96, v94, v96, s60
	v_fma_f32 v101, v99, v101, s60
	v_fma_f32 v86, |v82|, v86, |v82|
	v_fma_f32 v91, |v87|, v91, |v87|
	v_fma_f32 v96, |v92|, v96, |v92|
	v_fma_f32 v101, |v97|, v101, |v97|
	s_cmp_eq_u64 s[72:73], exec
	s_cbranch_scc1 .Lgsk_g1_4
	v_fma_f32 v85, |v82|, v102, s50
	v_fma_f32 v90, |v87|, v102, s50
	v_fma_f32 v95, |v92|, v102, s50
	v_fma_f32 v100, |v97|, v102, s50
	v_fma_f32 v85, |v82|, v85, s51
	v_fma_f32 v90, |v87|, v90, s51
	v_fma_f32 v95, |v92|, v95, s51
	v_fma_f32 v100, |v97|, v100, s51
	v_fma_f32 v85, |v82|, v85, s52
	v_fma_f32 v90, |v87|, v90, s52
	v_fma_f32 v95, |v92|, v95, s52
	v_fma_f32 v100, |v97|, v100, s52
	v_fma_f32 v85, |v82|, v85, s53
	v_fma_f32 v90, |v87|, v90, s53
	v_fma_f32 v95, |v92|, v95, s53
	v_fma_f32 v100, |v97|, v100, s53
	v_fma_f32 v85, |v82|, v85, s54
	v_fma_f32 v90, |v87|, v90, s54
	v_fma_f32 v95, |v92|, v95, s54
	v_fma_f32 v100, |v97|, v100, s54
	v_fma_f32 v85, |v82|, v85, s55
	v_fma_f32 v90, |v87|, v90, s55
	v_fma_f32 v95, |v92|, v95, s55
	v_fma_f32 v100, |v97|, v100, s55
	v_fma_f32 v85, |v82|, v85, |v82|
	v_fma_f32 v90, |v87|, v90, |v87|
	v_fma_f32 v95, |v92|, v95, |v92|
	v_fma_f32 v100, |v97|, v100, |v97|
	v_mul_f32_e32 v85, 0xbfb8aa3b, v85
	v_mul_f32_e32 v90, 0xbfb8aa3b, v90
	v_mul_f32_e32 v95, 0xbfb8aa3b, v95
	v_mul_f32_e32 v100, 0xbfb8aa3b, v100
	v_exp_f32_e32 v85, v85
	v_exp_f32_e32 v90, v90
	v_exp_f32_e32 v95, v95
	v_exp_f32_e32 v100, v100
	s_nop 0
	v_sub_f32_e32 v85, 1.0, v85
	v_sub_f32_e32 v90, 1.0, v90
	v_sub_f32_e32 v95, 1.0, v95
	v_sub_f32_e32 v100, 1.0, v100
	v_cndmask_b32_e64 v86, v85, v86, s[64:65]
	v_cndmask_b32_e64 v91, v90, v91, s[66:67]
	v_cndmask_b32_e64 v96, v95, v96, s[68:69]
	v_cndmask_b32_e64 v101, v100, v101, s[70:71]
.Lgsk_g1_4:
	v_fma_f32 v83, |v83|, v86, v83
	v_fma_f32 v88, |v88|, v91, v88
	v_fma_f32 v93, |v93|, v96, v93
	v_fma_f32 v98, |v98|, v101, v98
	v_cvt_f16_f32_e32 v82, v83
	v_cvt_f16_f32_e32 v87, v88
	v_cvt_f16_f32_e32 v92, v93
	v_cvt_f16_f32_e32 v97, v98
	ds_write_b16 v71, v82 offset:2304
	ds_write_b16 v71, v87 offset:2448
	ds_write_b16 v71, v92 offset:2592
	ds_write_b16 v71, v97 offset:2736
	v_fma_f32 v82, v42, s61, v137
	v_fma_f32 v87, v43, s61, v137
	v_fma_f32 v92, v44, s61, v137
	v_fma_f32 v97, v45, s61, v137
	v_fma_f32 v83, v42, s62, v141
	v_fma_f32 v88, v43, s62, v141
	v_fma_f32 v93, v44, s62, v141
	v_fma_f32 v98, v45, s62, v141
	v_mul_f32_e32 v84, v82, v82
	v_mul_f32_e32 v89, v87, v87
	v_mul_f32_e32 v94, v92, v92
	v_mul_f32_e32 v99, v97, v97
	v_cmp_lt_f32_e64 s[64:65], |v82|, 1.0
	v_cmp_lt_f32_e64 s[66:67], |v87|, 1.0
	v_cmp_lt_f32_e64 s[68:69], |v92|, 1.0
	v_cmp_lt_f32_e64 s[70:71], |v97|, 1.0
	v_fma_f32 v86, v84, v103, s56
	v_fma_f32 v91, v89, v103, s56
	v_fma_f32 v96, v94, v103, s56
	v_fma_f32 v101, v99, v103, s56
	s_and_b64 s[72:73], s[64:65], s[66:67]
	s_and_b64 s[74:75], s[68:69], s[70:71]
	s_and_b64 s[72:73], s[72:73], s[74:75]
	v_fma_f32 v86, v84, v86, s57
	v_fma_f32 v91, v89, v91, s57
	v_fma_f32 v96, v94, v96, s57
	v_fma_f32 v101, v99, v101, s57
	v_fma_f32 v86, v84, v86, s58
	v_fma_f32 v91, v89, v91, s58
	v_fma_f32 v96, v94, v96, s58
	v_fma_f32 v101, v99, v101, s58
	v_fma_f32 v86, v84, v86, s59
	v_fma_f32 v91, v89, v91, s59
	v_fma_f32 v96, v94, v96, s59
	v_fma_f32 v101, v99, v101, s59
	v_fma_f32 v86, v84, v86, s60
	v_fma_f32 v91, v89, v91, s60
	v_fma_f32 v96, v94, v96, s60
	v_fma_f32 v101, v99, v101, s60
	v_fma_f32 v86, |v82|, v86, |v82|
	v_fma_f32 v91, |v87|, v91, |v87|
	v_fma_f32 v96, |v92|, v96, |v92|
	v_fma_f32 v101, |v97|, v101, |v97|
	s_cmp_eq_u64 s[72:73], exec
	s_cbranch_scc1 .Lgsk_g1_5
	v_fma_f32 v85, |v82|, v102, s50
	v_fma_f32 v90, |v87|, v102, s50
	v_fma_f32 v95, |v92|, v102, s50
	v_fma_f32 v100, |v97|, v102, s50
	v_fma_f32 v85, |v82|, v85, s51
	v_fma_f32 v90, |v87|, v90, s51
	v_fma_f32 v95, |v92|, v95, s51
	v_fma_f32 v100, |v97|, v100, s51
	v_fma_f32 v85, |v82|, v85, s52
	v_fma_f32 v90, |v87|, v90, s52
	v_fma_f32 v95, |v92|, v95, s52
	v_fma_f32 v100, |v97|, v100, s52
	v_fma_f32 v85, |v82|, v85, s53
	v_fma_f32 v90, |v87|, v90, s53
	v_fma_f32 v95, |v92|, v95, s53
	v_fma_f32 v100, |v97|, v100, s53
	v_fma_f32 v85, |v82|, v85, s54
	v_fma_f32 v90, |v87|, v90, s54
	v_fma_f32 v95, |v92|, v95, s54
	v_fma_f32 v100, |v97|, v100, s54
	v_fma_f32 v85, |v82|, v85, s55
	v_fma_f32 v90, |v87|, v90, s55
	v_fma_f32 v95, |v92|, v95, s55
	v_fma_f32 v100, |v97|, v100, s55
	v_fma_f32 v85, |v82|, v85, |v82|
	v_fma_f32 v90, |v87|, v90, |v87|
	v_fma_f32 v95, |v92|, v95, |v92|
	v_fma_f32 v100, |v97|, v100, |v97|
	v_mul_f32_e32 v85, 0xbfb8aa3b, v85
	v_mul_f32_e32 v90, 0xbfb8aa3b, v90
	v_mul_f32_e32 v95, 0xbfb8aa3b, v95
	v_mul_f32_e32 v100, 0xbfb8aa3b, v100
	v_exp_f32_e32 v85, v85
	v_exp_f32_e32 v90, v90
	v_exp_f32_e32 v95, v95
	v_exp_f32_e32 v100, v100
	s_nop 0
	v_sub_f32_e32 v85, 1.0, v85
	v_sub_f32_e32 v90, 1.0, v90
	v_sub_f32_e32 v95, 1.0, v95
	v_sub_f32_e32 v100, 1.0, v100
	v_cndmask_b32_e64 v86, v85, v86, s[64:65]
	v_cndmask_b32_e64 v91, v90, v91, s[66:67]
	v_cndmask_b32_e64 v96, v95, v96, s[68:69]
	v_cndmask_b32_e64 v101, v100, v101, s[70:71]
.Lgsk_g1_5:
	v_fma_f32 v83, |v83|, v86, v83
	v_fma_f32 v88, |v88|, v91, v88
	v_fma_f32 v93, |v93|, v96, v93
	v_fma_f32 v98, |v98|, v101, v98
	v_cvt_f16_f32_e32 v82, v83
	v_cvt_f16_f32_e32 v87, v88
	v_cvt_f16_f32_e32 v92, v93
	v_cvt_f16_f32_e32 v97, v98
	ds_write_b16 v71, v82 offset:2336
	ds_write_b16 v71, v87 offset:2480
	ds_write_b16 v71, v92 offset:2624
	ds_write_b16 v71, v97 offset:2768
	v_fma_f32 v82, v38, s61, v138
	v_fma_f32 v87, v39, s61, v138
	v_fma_f32 v92, v40, s61, v138
	v_fma_f32 v97, v41, s61, v138
	v_fma_f32 v83, v38, s62, v142
	v_fma_f32 v88, v39, s62, v142
	v_fma_f32 v93, v40, s62, v142
	v_fma_f32 v98, v41, s62, v142
	v_mul_f32_e32 v84, v82, v82
	v_mul_f32_e32 v89, v87, v87
	v_mul_f32_e32 v94, v92, v92
	v_mul_f32_e32 v99, v97, v97
	v_cmp_lt_f32_e64 s[64:65], |v82|, 1.0
	v_cmp_lt_f32_e64 s[66:67], |v87|, 1.0
	v_cmp_lt_f32_e64 s[68:69], |v92|, 1.0
	v_cmp_lt_f32_e64 s[70:71], |v97|, 1.0
	v_fma_f32 v86, v84, v103, s56
	v_fma_f32 v91, v89, v103, s56
	v_fma_f32 v96, v94, v103, s56
	v_fma_f32 v101, v99, v103, s56
	s_and_b64 s[72:73], s[64:65], s[66:67]
	s_and_b64 s[74:75], s[68:69], s[70:71]
	s_and_b64 s[72:73], s[72:73], s[74:75]
	v_fma_f32 v86, v84, v86, s57
	v_fma_f32 v91, v89, v91, s57
	v_fma_f32 v96, v94, v96, s57
	v_fma_f32 v101, v99, v101, s57
	v_fma_f32 v86, v84, v86, s58
	v_fma_f32 v91, v89, v91, s58
	v_fma_f32 v96, v94, v96, s58
	v_fma_f32 v101, v99, v101, s58
	v_fma_f32 v86, v84, v86, s59
	v_fma_f32 v91, v89, v91, s59
	v_fma_f32 v96, v94, v96, s59
	v_fma_f32 v101, v99, v101, s59
	v_fma_f32 v86, v84, v86, s60
	v_fma_f32 v91, v89, v91, s60
	v_fma_f32 v96, v94, v96, s60
	v_fma_f32 v101, v99, v101, s60
	v_fma_f32 v86, |v82|, v86, |v82|
	v_fma_f32 v91, |v87|, v91, |v87|
	v_fma_f32 v96, |v92|, v96, |v92|
	v_fma_f32 v101, |v97|, v101, |v97|
	s_cmp_eq_u64 s[72:73], exec
	s_cbranch_scc1 .Lgsk_g1_6
	v_fma_f32 v85, |v82|, v102, s50
	v_fma_f32 v90, |v87|, v102, s50
	v_fma_f32 v95, |v92|, v102, s50
	v_fma_f32 v100, |v97|, v102, s50
	v_fma_f32 v85, |v82|, v85, s51
	v_fma_f32 v90, |v87|, v90, s51
	v_fma_f32 v95, |v92|, v95, s51
	v_fma_f32 v100, |v97|, v100, s51
	v_fma_f32 v85, |v82|, v85, s52
	v_fma_f32 v90, |v87|, v90, s52
	v_fma_f32 v95, |v92|, v95, s52
	v_fma_f32 v100, |v97|, v100, s52
	v_fma_f32 v85, |v82|, v85, s53
	v_fma_f32 v90, |v87|, v90, s53
	v_fma_f32 v95, |v92|, v95, s53
	v_fma_f32 v100, |v97|, v100, s53
	v_fma_f32 v85, |v82|, v85, s54
	v_fma_f32 v90, |v87|, v90, s54
	v_fma_f32 v95, |v92|, v95, s54
	v_fma_f32 v100, |v97|, v100, s54
	v_fma_f32 v85, |v82|, v85, s55
	v_fma_f32 v90, |v87|, v90, s55
	v_fma_f32 v95, |v92|, v95, s55
	v_fma_f32 v100, |v97|, v100, s55
	v_fma_f32 v85, |v82|, v85, |v82|
	v_fma_f32 v90, |v87|, v90, |v87|
	v_fma_f32 v95, |v92|, v95, |v92|
	v_fma_f32 v100, |v97|, v100, |v97|
	v_mul_f32_e32 v85, 0xbfb8aa3b, v85
	v_mul_f32_e32 v90, 0xbfb8aa3b, v90
	v_mul_f32_e32 v95, 0xbfb8aa3b, v95
	v_mul_f32_e32 v100, 0xbfb8aa3b, v100
	v_exp_f32_e32 v85, v85
	v_exp_f32_e32 v90, v90
	v_exp_f32_e32 v95, v95
	v_exp_f32_e32 v100, v100
	s_nop 0
	v_sub_f32_e32 v85, 1.0, v85
	v_sub_f32_e32 v90, 1.0, v90
	v_sub_f32_e32 v95, 1.0, v95
	v_sub_f32_e32 v100, 1.0, v100
	v_cndmask_b32_e64 v86, v85, v86, s[64:65]
	v_cndmask_b32_e64 v91, v90, v91, s[66:67]
	v_cndmask_b32_e64 v96, v95, v96, s[68:69]
	v_cndmask_b32_e64 v101, v100, v101, s[70:71]
.Lgsk_g1_6:
	v_fma_f32 v83, |v83|, v86, v83
	v_fma_f32 v88, |v88|, v91, v88
	v_fma_f32 v93, |v93|, v96, v93
	v_fma_f32 v98, |v98|, v101, v98
	v_cvt_f16_f32_e32 v82, v83
	v_cvt_f16_f32_e32 v87, v88
	v_cvt_f16_f32_e32 v92, v93
	v_cvt_f16_f32_e32 v97, v98
	ds_write_b16 v71, v82 offset:2368
	ds_write_b16 v71, v87 offset:2512
	ds_write_b16 v71, v92 offset:2656
	ds_write_b16 v71, v97 offset:2800
	v_fma_f32 v82, v34, s61, v139
	v_fma_f32 v87, v35, s61, v139
	v_fma_f32 v92, v36, s61, v139
	v_fma_f32 v97, v37, s61, v139
	v_fma_f32 v83, v34, s62, v143
	v_fma_f32 v88, v35, s62, v143
	v_fma_f32 v93, v36, s62, v143
	v_fma_f32 v98, v37, s62, v143
	v_mul_f32_e32 v84, v82, v82
	v_mul_f32_e32 v89, v87, v87
	v_mul_f32_e32 v94, v92, v92
	v_mul_f32_e32 v99, v97, v97
	v_cmp_lt_f32_e64 s[64:65], |v82|, 1.0
	v_cmp_lt_f32_e64 s[66:67], |v87|, 1.0
	v_cmp_lt_f32_e64 s[68:69], |v92|, 1.0
	v_cmp_lt_f32_e64 s[70:71], |v97|, 1.0
	v_fma_f32 v86, v84, v103, s56
	v_fma_f32 v91, v89, v103, s56
	v_fma_f32 v96, v94, v103, s56
	v_fma_f32 v101, v99, v103, s56
	s_and_b64 s[72:73], s[64:65], s[66:67]
	s_and_b64 s[74:75], s[68:69], s[70:71]
	s_and_b64 s[72:73], s[72:73], s[74:75]
	v_fma_f32 v86, v84, v86, s57
	v_fma_f32 v91, v89, v91, s57
	v_fma_f32 v96, v94, v96, s57
	v_fma_f32 v101, v99, v101, s57
	v_fma_f32 v86, v84, v86, s58
	v_fma_f32 v91, v89, v91, s58
	v_fma_f32 v96, v94, v96, s58
	v_fma_f32 v101, v99, v101, s58
	v_fma_f32 v86, v84, v86, s59
	v_fma_f32 v91, v89, v91, s59
	v_fma_f32 v96, v94, v96, s59
	v_fma_f32 v101, v99, v101, s59
	v_fma_f32 v86, v84, v86, s60
	v_fma_f32 v91, v89, v91, s60
	v_fma_f32 v96, v94, v96, s60
	v_fma_f32 v101, v99, v101, s60
	v_fma_f32 v86, |v82|, v86, |v82|
	v_fma_f32 v91, |v87|, v91, |v87|
	v_fma_f32 v96, |v92|, v96, |v92|
	v_fma_f32 v101, |v97|, v101, |v97|
	s_cmp_eq_u64 s[72:73], exec
	s_cbranch_scc1 .Lgsk_g1_7
	v_fma_f32 v85, |v82|, v102, s50
	v_fma_f32 v90, |v87|, v102, s50
	v_fma_f32 v95, |v92|, v102, s50
	v_fma_f32 v100, |v97|, v102, s50
	v_fma_f32 v85, |v82|, v85, s51
	v_fma_f32 v90, |v87|, v90, s51
	v_fma_f32 v95, |v92|, v95, s51
	v_fma_f32 v100, |v97|, v100, s51
	v_fma_f32 v85, |v82|, v85, s52
	v_fma_f32 v90, |v87|, v90, s52
	v_fma_f32 v95, |v92|, v95, s52
	v_fma_f32 v100, |v97|, v100, s52
	v_fma_f32 v85, |v82|, v85, s53
	v_fma_f32 v90, |v87|, v90, s53
	v_fma_f32 v95, |v92|, v95, s53
	v_fma_f32 v100, |v97|, v100, s53
	v_fma_f32 v85, |v82|, v85, s54
	v_fma_f32 v90, |v87|, v90, s54
	v_fma_f32 v95, |v92|, v95, s54
	v_fma_f32 v100, |v97|, v100, s54
	v_fma_f32 v85, |v82|, v85, s55
	v_fma_f32 v90, |v87|, v90, s55
	v_fma_f32 v95, |v92|, v95, s55
	v_fma_f32 v100, |v97|, v100, s55
	v_fma_f32 v85, |v82|, v85, |v82|
	v_fma_f32 v90, |v87|, v90, |v87|
	v_fma_f32 v95, |v92|, v95, |v92|
	v_fma_f32 v100, |v97|, v100, |v97|
	v_mul_f32_e32 v85, 0xbfb8aa3b, v85
	v_mul_f32_e32 v90, 0xbfb8aa3b, v90
	v_mul_f32_e32 v95, 0xbfb8aa3b, v95
	v_mul_f32_e32 v100, 0xbfb8aa3b, v100
	v_exp_f32_e32 v85, v85
	v_exp_f32_e32 v90, v90
	v_exp_f32_e32 v95, v95
	v_exp_f32_e32 v100, v100
	s_nop 0
	v_sub_f32_e32 v85, 1.0, v85
	v_sub_f32_e32 v90, 1.0, v90
	v_sub_f32_e32 v95, 1.0, v95
	v_sub_f32_e32 v100, 1.0, v100
	v_cndmask_b32_e64 v86, v85, v86, s[64:65]
	v_cndmask_b32_e64 v91, v90, v91, s[66:67]
	v_cndmask_b32_e64 v96, v95, v96, s[68:69]
	v_cndmask_b32_e64 v101, v100, v101, s[70:71]
.Lgsk_g1_7:
	v_fma_f32 v83, |v83|, v86, v83
	v_fma_f32 v88, |v88|, v91, v88
	v_fma_f32 v93, |v93|, v96, v93
	v_fma_f32 v98, |v98|, v101, v98
	v_cvt_f16_f32_e32 v82, v83
	v_cvt_f16_f32_e32 v87, v88
	v_cvt_f16_f32_e32 v92, v93
	v_cvt_f16_f32_e32 v97, v98
	ds_write_b16 v71, v82 offset:2400
	ds_write_b16 v71, v87 offset:2544
	ds_write_b16 v71, v92 offset:2688
	ds_write_b16 v71, v97 offset:2832
	ds_read_b128 v[104:107], v74
	ds_read_b128 v[108:111], v74 offset:1152
	ds_read_b128 v[112:115], v74 offset:2304
	ds_read_b128 v[116:119], v74 offset:3456
	v_fma_f32 v82, v30, s61, v136
	v_fma_f32 v87, v31, s61, v136
	v_fma_f32 v92, v32, s61, v136
	v_fma_f32 v97, v33, s61, v136
	v_fma_f32 v83, v30, s62, v140
	v_fma_f32 v88, v31, s62, v140
	v_fma_f32 v93, v32, s62, v140
	v_fma_f32 v98, v33, s62, v140
	v_mul_f32_e32 v84, v82, v82
	v_mul_f32_e32 v89, v87, v87
	v_mul_f32_e32 v94, v92, v92
	v_mul_f32_e32 v99, v97, v97
	v_cmp_lt_f32_e64 s[64:65], |v82|, 1.0
	v_cmp_lt_f32_e64 s[66:67], |v87|, 1.0
	v_cmp_lt_f32_e64 s[68:69], |v92|, 1.0
	v_cmp_lt_f32_e64 s[70:71], |v97|, 1.0
	v_fma_f32 v86, v84, v103, s56
	v_fma_f32 v91, v89, v103, s56
	v_fma_f32 v96, v94, v103, s56
	v_fma_f32 v101, v99, v103, s56
	s_and_b64 s[72:73], s[64:65], s[66:67]
	s_and_b64 s[74:75], s[68:69], s[70:71]
	s_and_b64 s[72:73], s[72:73], s[74:75]
	v_fma_f32 v86, v84, v86, s57
	v_fma_f32 v91, v89, v91, s57
	v_fma_f32 v96, v94, v96, s57
	v_fma_f32 v101, v99, v101, s57
	v_fma_f32 v86, v84, v86, s58
	v_fma_f32 v91, v89, v91, s58
	v_fma_f32 v96, v94, v96, s58
	v_fma_f32 v101, v99, v101, s58
	v_fma_f32 v86, v84, v86, s59
	v_fma_f32 v91, v89, v91, s59
	v_fma_f32 v96, v94, v96, s59
	v_fma_f32 v101, v99, v101, s59
	v_fma_f32 v86, v84, v86, s60
	v_fma_f32 v91, v89, v91, s60
	v_fma_f32 v96, v94, v96, s60
	v_fma_f32 v101, v99, v101, s60
	v_fma_f32 v86, |v82|, v86, |v82|
	v_fma_f32 v91, |v87|, v91, |v87|
	v_fma_f32 v96, |v92|, v96, |v92|
	v_fma_f32 v101, |v97|, v101, |v97|
	s_cmp_eq_u64 s[72:73], exec
	s_cbranch_scc1 .Lgsk_g1_8
	v_fma_f32 v85, |v82|, v102, s50
	v_fma_f32 v90, |v87|, v102, s50
	v_fma_f32 v95, |v92|, v102, s50
	v_fma_f32 v100, |v97|, v102, s50
	v_fma_f32 v85, |v82|, v85, s51
	v_fma_f32 v90, |v87|, v90, s51
	v_fma_f32 v95, |v92|, v95, s51
	v_fma_f32 v100, |v97|, v100, s51
	v_fma_f32 v85, |v82|, v85, s52
	v_fma_f32 v90, |v87|, v90, s52
	v_fma_f32 v95, |v92|, v95, s52
	v_fma_f32 v100, |v97|, v100, s52
	v_fma_f32 v85, |v82|, v85, s53
	v_fma_f32 v90, |v87|, v90, s53
	v_fma_f32 v95, |v92|, v95, s53
	v_fma_f32 v100, |v97|, v100, s53
	v_fma_f32 v85, |v82|, v85, s54
	v_fma_f32 v90, |v87|, v90, s54
	v_fma_f32 v95, |v92|, v95, s54
	v_fma_f32 v100, |v97|, v100, s54
	v_fma_f32 v85, |v82|, v85, s55
	v_fma_f32 v90, |v87|, v90, s55
	v_fma_f32 v95, |v92|, v95, s55
	v_fma_f32 v100, |v97|, v100, s55
	v_fma_f32 v85, |v82|, v85, |v82|
	v_fma_f32 v90, |v87|, v90, |v87|
	v_fma_f32 v95, |v92|, v95, |v92|
	v_fma_f32 v100, |v97|, v100, |v97|
	v_mul_f32_e32 v85, 0xbfb8aa3b, v85
	v_mul_f32_e32 v90, 0xbfb8aa3b, v90
	v_mul_f32_e32 v95, 0xbfb8aa3b, v95
	v_mul_f32_e32 v100, 0xbfb8aa3b, v100
	v_exp_f32_e32 v85, v85
	v_exp_f32_e32 v90, v90
	v_exp_f32_e32 v95, v95
	v_exp_f32_e32 v100, v100
	s_nop 0
	v_sub_f32_e32 v85, 1.0, v85
	v_sub_f32_e32 v90, 1.0, v90
	v_sub_f32_e32 v95, 1.0, v95
	v_sub_f32_e32 v100, 1.0, v100
	v_cndmask_b32_e64 v86, v85, v86, s[64:65]
	v_cndmask_b32_e64 v91, v90, v91, s[66:67]
	v_cndmask_b32_e64 v96, v95, v96, s[68:69]
	v_cndmask_b32_e64 v101, v100, v101, s[70:71]
.Lgsk_g1_8:
	v_fma_f32 v83, |v83|, v86, v83
	v_fma_f32 v88, |v88|, v91, v88
	v_fma_f32 v93, |v93|, v96, v93
	v_fma_f32 v98, |v98|, v101, v98
	v_cvt_f16_f32_e32 v82, v83
	v_cvt_f16_f32_e32 v87, v88
	v_cvt_f16_f32_e32 v92, v93
	v_cvt_f16_f32_e32 v97, v98
	s_waitcnt lgkmcnt(0)
	s_sub_i32 s2, s42, 0
	v_cmp_gt_i32_e32 vcc, s2, v75
	s_and_saveexec_b64 s[44:45], vcc
	s_add_u32 s2, s38, 0x0
	s_addc_u32 s3, s39, 0
	global_store_dwordx4 v76, v[104:107], s[2:3]
	s_mov_b64 exec, s[44:45]
	s_sub_i32 s2, s42, 8
	v_cmp_gt_i32_e32 vcc, s2, v75
	s_and_saveexec_b64 s[44:45], vcc
	s_add_u32 s2, s38, 0x8000
	s_addc_u32 s3, s39, 0
	global_store_dwordx4 v76, v[108:111], s[2:3]
	s_mov_b64 exec, s[44:45]
	s_sub_i32 s2, s42, 16
	v_cmp_gt_i32_e32 vcc, s2, v75
	s_and_saveexec_b64 s[44:45], vcc
	s_add_u32 s2, s38, 0x10000
	s_addc_u32 s3, s39, 0
	global_store_dwordx4 v76, v[112:115], s[2:3]
	s_mov_b64 exec, s[44:45]
	s_sub_i32 s2, s42, 24
	v_cmp_gt_i32_e32 vcc, s2, v75
	s_and_saveexec_b64 s[44:45], vcc
	s_add_u32 s2, s38, 0x18000
	s_addc_u32 s3, s39, 0
	global_store_dwordx4 v76, v[116:119], s[2:3]
	s_mov_b64 exec, s[44:45]
	ds_write_b16 v71, v82
	ds_write_b16 v71, v87 offset:144
	ds_write_b16 v71, v92 offset:288
	ds_write_b16 v71, v97 offset:432
	v_fma_f32 v82, v26, s61, v137
	v_fma_f32 v87, v27, s61, v137
	v_fma_f32 v92, v28, s61, v137
	v_fma_f32 v97, v29, s61, v137
	v_fma_f32 v83, v26, s62, v141
	v_fma_f32 v88, v27, s62, v141
	v_fma_f32 v93, v28, s62, v141
	v_fma_f32 v98, v29, s62, v141
	v_mul_f32_e32 v84, v82, v82
	v_mul_f32_e32 v89, v87, v87
	v_mul_f32_e32 v94, v92, v92
	v_mul_f32_e32 v99, v97, v97
	v_cmp_lt_f32_e64 s[64:65], |v82|, 1.0
	v_cmp_lt_f32_e64 s[66:67], |v87|, 1.0
	v_cmp_lt_f32_e64 s[68:69], |v92|, 1.0
	v_cmp_lt_f32_e64 s[70:71], |v97|, 1.0
	v_fma_f32 v86, v84, v103, s56
	v_fma_f32 v91, v89, v103, s56
	v_fma_f32 v96, v94, v103, s56
	v_fma_f32 v101, v99, v103, s56
	s_and_b64 s[72:73], s[64:65], s[66:67]
	s_and_b64 s[74:75], s[68:69], s[70:71]
	s_and_b64 s[72:73], s[72:73], s[74:75]
	v_fma_f32 v86, v84, v86, s57
	v_fma_f32 v91, v89, v91, s57
	v_fma_f32 v96, v94, v96, s57
	v_fma_f32 v101, v99, v101, s57
	v_fma_f32 v86, v84, v86, s58
	v_fma_f32 v91, v89, v91, s58
	v_fma_f32 v96, v94, v96, s58
	v_fma_f32 v101, v99, v101, s58
	v_fma_f32 v86, v84, v86, s59
	v_fma_f32 v91, v89, v91, s59
	v_fma_f32 v96, v94, v96, s59
	v_fma_f32 v101, v99, v101, s59
	v_fma_f32 v86, v84, v86, s60
	v_fma_f32 v91, v89, v91, s60
	v_fma_f32 v96, v94, v96, s60
	v_fma_f32 v101, v99, v101, s60
	v_fma_f32 v86, |v82|, v86, |v82|
	v_fma_f32 v91, |v87|, v91, |v87|
	v_fma_f32 v96, |v92|, v96, |v92|
	v_fma_f32 v101, |v97|, v101, |v97|
	s_cmp_eq_u64 s[72:73], exec
	s_cbranch_scc1 .Lgsk_g1_9
	v_fma_f32 v85, |v82|, v102, s50
	v_fma_f32 v90, |v87|, v102, s50
	v_fma_f32 v95, |v92|, v102, s50
	v_fma_f32 v100, |v97|, v102, s50
	v_fma_f32 v85, |v82|, v85, s51
	v_fma_f32 v90, |v87|, v90, s51
	v_fma_f32 v95, |v92|, v95, s51
	v_fma_f32 v100, |v97|, v100, s51
	v_fma_f32 v85, |v82|, v85, s52
	v_fma_f32 v90, |v87|, v90, s52
	v_fma_f32 v95, |v92|, v95, s52
	v_fma_f32 v100, |v97|, v100, s52
	v_fma_f32 v85, |v82|, v85, s53
	v_fma_f32 v90, |v87|, v90, s53
	v_fma_f32 v95, |v92|, v95, s53
	v_fma_f32 v100, |v97|, v100, s53
	v_fma_f32 v85, |v82|, v85, s54
	v_fma_f32 v90, |v87|, v90, s54
	v_fma_f32 v95, |v92|, v95, s54
	v_fma_f32 v100, |v97|, v100, s54
	v_fma_f32 v85, |v82|, v85, s55
	v_fma_f32 v90, |v87|, v90, s55
	v_fma_f32 v95, |v92|, v95, s55
	v_fma_f32 v100, |v97|, v100, s55
	v_fma_f32 v85, |v82|, v85, |v82|
	v_fma_f32 v90, |v87|, v90, |v87|
	v_fma_f32 v95, |v92|, v95, |v92|
	v_fma_f32 v100, |v97|, v100, |v97|
	v_mul_f32_e32 v85, 0xbfb8aa3b, v85
	v_mul_f32_e32 v90, 0xbfb8aa3b, v90
	v_mul_f32_e32 v95, 0xbfb8aa3b, v95
	v_mul_f32_e32 v100, 0xbfb8aa3b, v100
	v_exp_f32_e32 v85, v85
	v_exp_f32_e32 v90, v90
	v_exp_f32_e32 v95, v95
	v_exp_f32_e32 v100, v100
	s_nop 0
	v_sub_f32_e32 v85, 1.0, v85
	v_sub_f32_e32 v90, 1.0, v90
	v_sub_f32_e32 v95, 1.0, v95
	v_sub_f32_e32 v100, 1.0, v100
	v_cndmask_b32_e64 v86, v85, v86, s[64:65]
	v_cndmask_b32_e64 v91, v90, v91, s[66:67]
	v_cndmask_b32_e64 v96, v95, v96, s[68:69]
	v_cndmask_b32_e64 v101, v100, v101, s[70:71]
.Lgsk_g1_9:
	v_fma_f32 v83, |v83|, v86, v83
	v_fma_f32 v88, |v88|, v91, v88
	v_fma_f32 v93, |v93|, v96, v93
	v_fma_f32 v98, |v98|, v101, v98
	v_cvt_f16_f32_e32 v82, v83
	v_cvt_f16_f32_e32 v87, v88
	v_cvt_f16_f32_e32 v92, v93
	v_cvt_f16_f32_e32 v97, v98
	ds_write_b16 v71, v82 offset:32
	ds_write_b16 v71, v87 offset:176
	ds_write_b16 v71, v92 offset:320
	ds_write_b16 v71, v97 offset:464
	v_fma_f32 v82, v22, s61, v138
	v_fma_f32 v87, v23, s61, v138
	v_fma_f32 v92, v24, s61, v138
	v_fma_f32 v97, v25, s61, v138
	v_fma_f32 v83, v22, s62, v142
	v_fma_f32 v88, v23, s62, v142
	v_fma_f32 v93, v24, s62, v142
	v_fma_f32 v98, v25, s62, v142
	v_mul_f32_e32 v84, v82, v82
	v_mul_f32_e32 v89, v87, v87
	v_mul_f32_e32 v94, v92, v92
	v_mul_f32_e32 v99, v97, v97
	v_cmp_lt_f32_e64 s[64:65], |v82|, 1.0
	v_cmp_lt_f32_e64 s[66:67], |v87|, 1.0
	v_cmp_lt_f32_e64 s[68:69], |v92|, 1.0
	v_cmp_lt_f32_e64 s[70:71], |v97|, 1.0
	v_fma_f32 v86, v84, v103, s56
	v_fma_f32 v91, v89, v103, s56
	v_fma_f32 v96, v94, v103, s56
	v_fma_f32 v101, v99, v103, s56
	s_and_b64 s[72:73], s[64:65], s[66:67]
	s_and_b64 s[74:75], s[68:69], s[70:71]
	s_and_b64 s[72:73], s[72:73], s[74:75]
	v_fma_f32 v86, v84, v86, s57
	v_fma_f32 v91, v89, v91, s57
	v_fma_f32 v96, v94, v96, s57
	v_fma_f32 v101, v99, v101, s57
	v_fma_f32 v86, v84, v86, s58
	v_fma_f32 v91, v89, v91, s58
	v_fma_f32 v96, v94, v96, s58
	v_fma_f32 v101, v99, v101, s58
	v_fma_f32 v86, v84, v86, s59
	v_fma_f32 v91, v89, v91, s59
	v_fma_f32 v96, v94, v96, s59
	v_fma_f32 v101, v99, v101, s59
	v_fma_f32 v86, v84, v86, s60
	v_fma_f32 v91, v89, v91, s60
	v_fma_f32 v96, v94, v96, s60
	v_fma_f32 v101, v99, v101, s60
	v_fma_f32 v86, |v82|, v86, |v82|
	v_fma_f32 v91, |v87|, v91, |v87|
	v_fma_f32 v96, |v92|, v96, |v92|
	v_fma_f32 v101, |v97|, v101, |v97|
	s_cmp_eq_u64 s[72:73], exec
	s_cbranch_scc1 .Lgsk_g1_10
	v_fma_f32 v85, |v82|, v102, s50
	v_fma_f32 v90, |v87|, v102, s50
	v_fma_f32 v95, |v92|, v102, s50
	v_fma_f32 v100, |v97|, v102, s50
	v_fma_f32 v85, |v82|, v85, s51
	v_fma_f32 v90, |v87|, v90, s51
	v_fma_f32 v95, |v92|, v95, s51
	v_fma_f32 v100, |v97|, v100, s51
	v_fma_f32 v85, |v82|, v85, s52
	v_fma_f32 v90, |v87|, v90, s52
	v_fma_f32 v95, |v92|, v95, s52
	v_fma_f32 v100, |v97|, v100, s52
	v_fma_f32 v85, |v82|, v85, s53
	v_fma_f32 v90, |v87|, v90, s53
	v_fma_f32 v95, |v92|, v95, s53
	v_fma_f32 v100, |v97|, v100, s53
	v_fma_f32 v85, |v82|, v85, s54
	v_fma_f32 v90, |v87|, v90, s54
	v_fma_f32 v95, |v92|, v95, s54
	v_fma_f32 v100, |v97|, v100, s54
	v_fma_f32 v85, |v82|, v85, s55
	v_fma_f32 v90, |v87|, v90, s55
	v_fma_f32 v95, |v92|, v95, s55
	v_fma_f32 v100, |v97|, v100, s55
	v_fma_f32 v85, |v82|, v85, |v82|
	v_fma_f32 v90, |v87|, v90, |v87|
	v_fma_f32 v95, |v92|, v95, |v92|
	v_fma_f32 v100, |v97|, v100, |v97|
	v_mul_f32_e32 v85, 0xbfb8aa3b, v85
	v_mul_f32_e32 v90, 0xbfb8aa3b, v90
	v_mul_f32_e32 v95, 0xbfb8aa3b, v95
	v_mul_f32_e32 v100, 0xbfb8aa3b, v100
	v_exp_f32_e32 v85, v85
	v_exp_f32_e32 v90, v90
	v_exp_f32_e32 v95, v95
	v_exp_f32_e32 v100, v100
	s_nop 0
	v_sub_f32_e32 v85, 1.0, v85
	v_sub_f32_e32 v90, 1.0, v90
	v_sub_f32_e32 v95, 1.0, v95
	v_sub_f32_e32 v100, 1.0, v100
	v_cndmask_b32_e64 v86, v85, v86, s[64:65]
	v_cndmask_b32_e64 v91, v90, v91, s[66:67]
	v_cndmask_b32_e64 v96, v95, v96, s[68:69]
	v_cndmask_b32_e64 v101, v100, v101, s[70:71]
.Lgsk_g1_10:
	v_fma_f32 v83, |v83|, v86, v83
	v_fma_f32 v88, |v88|, v91, v88
	v_fma_f32 v93, |v93|, v96, v93
	v_fma_f32 v98, |v98|, v101, v98
	v_cvt_f16_f32_e32 v82, v83
	v_cvt_f16_f32_e32 v87, v88
	v_cvt_f16_f32_e32 v92, v93
	v_cvt_f16_f32_e32 v97, v98
	ds_write_b16 v71, v82 offset:64
	ds_write_b16 v71, v87 offset:208
	ds_write_b16 v71, v92 offset:352
	ds_write_b16 v71, v97 offset:496
	v_fma_f32 v82, v18, s61, v139
	v_fma_f32 v87, v19, s61, v139
	v_fma_f32 v92, v20, s61, v139
	v_fma_f32 v97, v21, s61, v139
	v_fma_f32 v83, v18, s62, v143
	v_fma_f32 v88, v19, s62, v143
	v_fma_f32 v93, v20, s62, v143
	v_fma_f32 v98, v21, s62, v143
	v_mul_f32_e32 v84, v82, v82
	v_mul_f32_e32 v89, v87, v87
	v_mul_f32_e32 v94, v92, v92
	v_mul_f32_e32 v99, v97, v97
	v_cmp_lt_f32_e64 s[64:65], |v82|, 1.0
	v_cmp_lt_f32_e64 s[66:67], |v87|, 1.0
	v_cmp_lt_f32_e64 s[68:69], |v92|, 1.0
	v_cmp_lt_f32_e64 s[70:71], |v97|, 1.0
	v_fma_f32 v86, v84, v103, s56
	v_fma_f32 v91, v89, v103, s56
	v_fma_f32 v96, v94, v103, s56
	v_fma_f32 v101, v99, v103, s56
	s_and_b64 s[72:73], s[64:65], s[66:67]
	s_and_b64 s[74:75], s[68:69], s[70:71]
	s_and_b64 s[72:73], s[72:73], s[74:75]
	v_fma_f32 v86, v84, v86, s57
	v_fma_f32 v91, v89, v91, s57
	v_fma_f32 v96, v94, v96, s57
	v_fma_f32 v101, v99, v101, s57
	v_fma_f32 v86, v84, v86, s58
	v_fma_f32 v91, v89, v91, s58
	v_fma_f32 v96, v94, v96, s58
	v_fma_f32 v101, v99, v101, s58
	v_fma_f32 v86, v84, v86, s59
	v_fma_f32 v91, v89, v91, s59
	v_fma_f32 v96, v94, v96, s59
	v_fma_f32 v101, v99, v101, s59
	v_fma_f32 v86, v84, v86, s60
	v_fma_f32 v91, v89, v91, s60
	v_fma_f32 v96, v94, v96, s60
	v_fma_f32 v101, v99, v101, s60
	v_fma_f32 v86, |v82|, v86, |v82|
	v_fma_f32 v91, |v87|, v91, |v87|
	v_fma_f32 v96, |v92|, v96, |v92|
	v_fma_f32 v101, |v97|, v101, |v97|
	s_cmp_eq_u64 s[72:73], exec
	s_cbranch_scc1 .Lgsk_g1_11
	v_fma_f32 v85, |v82|, v102, s50
	v_fma_f32 v90, |v87|, v102, s50
	v_fma_f32 v95, |v92|, v102, s50
	v_fma_f32 v100, |v97|, v102, s50
	v_fma_f32 v85, |v82|, v85, s51
	v_fma_f32 v90, |v87|, v90, s51
	v_fma_f32 v95, |v92|, v95, s51
	v_fma_f32 v100, |v97|, v100, s51
	v_fma_f32 v85, |v82|, v85, s52
	v_fma_f32 v90, |v87|, v90, s52
	v_fma_f32 v95, |v92|, v95, s52
	v_fma_f32 v100, |v97|, v100, s52
	v_fma_f32 v85, |v82|, v85, s53
	v_fma_f32 v90, |v87|, v90, s53
	v_fma_f32 v95, |v92|, v95, s53
	v_fma_f32 v100, |v97|, v100, s53
	v_fma_f32 v85, |v82|, v85, s54
	v_fma_f32 v90, |v87|, v90, s54
	v_fma_f32 v95, |v92|, v95, s54
	v_fma_f32 v100, |v97|, v100, s54
	v_fma_f32 v85, |v82|, v85, s55
	v_fma_f32 v90, |v87|, v90, s55
	v_fma_f32 v95, |v92|, v95, s55
	v_fma_f32 v100, |v97|, v100, s55
	v_fma_f32 v85, |v82|, v85, |v82|
	v_fma_f32 v90, |v87|, v90, |v87|
	v_fma_f32 v95, |v92|, v95, |v92|
	v_fma_f32 v100, |v97|, v100, |v97|
	v_mul_f32_e32 v85, 0xbfb8aa3b, v85
	v_mul_f32_e32 v90, 0xbfb8aa3b, v90
	v_mul_f32_e32 v95, 0xbfb8aa3b, v95
	v_mul_f32_e32 v100, 0xbfb8aa3b, v100
	v_exp_f32_e32 v85, v85
	v_exp_f32_e32 v90, v90
	v_exp_f32_e32 v95, v95
	v_exp_f32_e32 v100, v100
	s_nop 0
	v_sub_f32_e32 v85, 1.0, v85
	v_sub_f32_e32 v90, 1.0, v90
	v_sub_f32_e32 v95, 1.0, v95
	v_sub_f32_e32 v100, 1.0, v100
	v_cndmask_b32_e64 v86, v85, v86, s[64:65]
	v_cndmask_b32_e64 v91, v90, v91, s[66:67]
	v_cndmask_b32_e64 v96, v95, v96, s[68:69]
	v_cndmask_b32_e64 v101, v100, v101, s[70:71]
.Lgsk_g1_11:
	v_fma_f32 v83, |v83|, v86, v83
	v_fma_f32 v88, |v88|, v91, v88
	v_fma_f32 v93, |v93|, v96, v93
	v_fma_f32 v98, |v98|, v101, v98
	v_cvt_f16_f32_e32 v82, v83
	v_cvt_f16_f32_e32 v87, v88
	v_cvt_f16_f32_e32 v92, v93
	v_cvt_f16_f32_e32 v97, v98
	ds_write_b16 v71, v82 offset:96
	ds_write_b16 v71, v87 offset:240
	ds_write_b16 v71, v92 offset:384
	ds_write_b16 v71, v97 offset:528
	v_fma_f32 v82, v14, s61, v136
	v_fma_f32 v87, v15, s61, v136
	v_fma_f32 v92, v16, s61, v136
	v_fma_f32 v97, v17, s61, v136
	v_fma_f32 v83, v14, s62, v140
	v_fma_f32 v88, v15, s62, v140
	v_fma_f32 v93, v16, s62, v140
	v_fma_f32 v98, v17, s62, v140
	v_mul_f32_e32 v84, v82, v82
	v_mul_f32_e32 v89, v87, v87
	v_mul_f32_e32 v94, v92, v92
	v_mul_f32_e32 v99, v97, v97
	v_cmp_lt_f32_e64 s[64:65], |v82|, 1.0
	v_cmp_lt_f32_e64 s[66:67], |v87|, 1.0
	v_cmp_lt_f32_e64 s[68:69], |v92|, 1.0
	v_cmp_lt_f32_e64 s[70:71], |v97|, 1.0
	v_fma_f32 v86, v84, v103, s56
	v_fma_f32 v91, v89, v103, s56
	v_fma_f32 v96, v94, v103, s56
	v_fma_f32 v101, v99, v103, s56
	s_and_b64 s[72:73], s[64:65], s[66:67]
	s_and_b64 s[74:75], s[68:69], s[70:71]
	s_and_b64 s[72:73], s[72:73], s[74:75]
	v_fma_f32 v86, v84, v86, s57
	v_fma_f32 v91, v89, v91, s57
	v_fma_f32 v96, v94, v96, s57
	v_fma_f32 v101, v99, v101, s57
	v_fma_f32 v86, v84, v86, s58
	v_fma_f32 v91, v89, v91, s58
	v_fma_f32 v96, v94, v96, s58
	v_fma_f32 v101, v99, v101, s58
	v_fma_f32 v86, v84, v86, s59
	v_fma_f32 v91, v89, v91, s59
	v_fma_f32 v96, v94, v96, s59
	v_fma_f32 v101, v99, v101, s59
	v_fma_f32 v86, v84, v86, s60
	v_fma_f32 v91, v89, v91, s60
	v_fma_f32 v96, v94, v96, s60
	v_fma_f32 v101, v99, v101, s60
	v_fma_f32 v86, |v82|, v86, |v82|
	v_fma_f32 v91, |v87|, v91, |v87|
	v_fma_f32 v96, |v92|, v96, |v92|
	v_fma_f32 v101, |v97|, v101, |v97|
	s_cmp_eq_u64 s[72:73], exec
	s_cbranch_scc1 .Lgsk_g1_12
	v_fma_f32 v85, |v82|, v102, s50
	v_fma_f32 v90, |v87|, v102, s50
	v_fma_f32 v95, |v92|, v102, s50
	v_fma_f32 v100, |v97|, v102, s50
	v_fma_f32 v85, |v82|, v85, s51
	v_fma_f32 v90, |v87|, v90, s51
	v_fma_f32 v95, |v92|, v95, s51
	v_fma_f32 v100, |v97|, v100, s51
	v_fma_f32 v85, |v82|, v85, s52
	v_fma_f32 v90, |v87|, v90, s52
	v_fma_f32 v95, |v92|, v95, s52
	v_fma_f32 v100, |v97|, v100, s52
	v_fma_f32 v85, |v82|, v85, s53
	v_fma_f32 v90, |v87|, v90, s53
	v_fma_f32 v95, |v92|, v95, s53
	v_fma_f32 v100, |v97|, v100, s53
	v_fma_f32 v85, |v82|, v85, s54
	v_fma_f32 v90, |v87|, v90, s54
	v_fma_f32 v95, |v92|, v95, s54
	v_fma_f32 v100, |v97|, v100, s54
	v_fma_f32 v85, |v82|, v85, s55
	v_fma_f32 v90, |v87|, v90, s55
	v_fma_f32 v95, |v92|, v95, s55
	v_fma_f32 v100, |v97|, v100, s55
	v_fma_f32 v85, |v82|, v85, |v82|
	v_fma_f32 v90, |v87|, v90, |v87|
	v_fma_f32 v95, |v92|, v95, |v92|
	v_fma_f32 v100, |v97|, v100, |v97|
	v_mul_f32_e32 v85, 0xbfb8aa3b, v85
	v_mul_f32_e32 v90, 0xbfb8aa3b, v90
	v_mul_f32_e32 v95, 0xbfb8aa3b, v95
	v_mul_f32_e32 v100, 0xbfb8aa3b, v100
	v_exp_f32_e32 v85, v85
	v_exp_f32_e32 v90, v90
	v_exp_f32_e32 v95, v95
	v_exp_f32_e32 v100, v100
	s_nop 0
	v_sub_f32_e32 v85, 1.0, v85
	v_sub_f32_e32 v90, 1.0, v90
	v_sub_f32_e32 v95, 1.0, v95
	v_sub_f32_e32 v100, 1.0, v100
	v_cndmask_b32_e64 v86, v85, v86, s[64:65]
	v_cndmask_b32_e64 v91, v90, v91, s[66:67]
	v_cndmask_b32_e64 v96, v95, v96, s[68:69]
	v_cndmask_b32_e64 v101, v100, v101, s[70:71]
.Lgsk_g1_12:
	v_fma_f32 v83, |v83|, v86, v83
	v_fma_f32 v88, |v88|, v91, v88
	v_fma_f32 v93, |v93|, v96, v93
	v_fma_f32 v98, |v98|, v101, v98
	v_cvt_f16_f32_e32 v82, v83
	v_cvt_f16_f32_e32 v87, v88
	v_cvt_f16_f32_e32 v92, v93
	v_cvt_f16_f32_e32 v97, v98
	ds_write_b16 v71, v82 offset:2304
	ds_write_b16 v71, v87 offset:2448
	ds_write_b16 v71, v92 offset:2592
	ds_write_b16 v71, v97 offset:2736
	v_fma_f32 v82, v10, s61, v137
	v_fma_f32 v87, v11, s61, v137
	v_fma_f32 v92, v12, s61, v137
	v_fma_f32 v97, v13, s61, v137
	v_fma_f32 v83, v10, s62, v141
	v_fma_f32 v88, v11, s62, v141
	v_fma_f32 v93, v12, s62, v141
	v_fma_f32 v98, v13, s62, v141
	v_mul_f32_e32 v84, v82, v82
	v_mul_f32_e32 v89, v87, v87
	v_mul_f32_e32 v94, v92, v92
	v_mul_f32_e32 v99, v97, v97
	v_cmp_lt_f32_e64 s[64:65], |v82|, 1.0
	v_cmp_lt_f32_e64 s[66:67], |v87|, 1.0
	v_cmp_lt_f32_e64 s[68:69], |v92|, 1.0
	v_cmp_lt_f32_e64 s[70:71], |v97|, 1.0
	v_fma_f32 v86, v84, v103, s56
	v_fma_f32 v91, v89, v103, s56
	v_fma_f32 v96, v94, v103, s56
	v_fma_f32 v101, v99, v103, s56
	s_and_b64 s[72:73], s[64:65], s[66:67]
	s_and_b64 s[74:75], s[68:69], s[70:71]
	s_and_b64 s[72:73], s[72:73], s[74:75]
	v_fma_f32 v86, v84, v86, s57
	v_fma_f32 v91, v89, v91, s57
	v_fma_f32 v96, v94, v96, s57
	v_fma_f32 v101, v99, v101, s57
	v_fma_f32 v86, v84, v86, s58
	v_fma_f32 v91, v89, v91, s58
	v_fma_f32 v96, v94, v96, s58
	v_fma_f32 v101, v99, v101, s58
	v_fma_f32 v86, v84, v86, s59
	v_fma_f32 v91, v89, v91, s59
	v_fma_f32 v96, v94, v96, s59
	v_fma_f32 v101, v99, v101, s59
	v_fma_f32 v86, v84, v86, s60
	v_fma_f32 v91, v89, v91, s60
	v_fma_f32 v96, v94, v96, s60
	v_fma_f32 v101, v99, v101, s60
	v_fma_f32 v86, |v82|, v86, |v82|
	v_fma_f32 v91, |v87|, v91, |v87|
	v_fma_f32 v96, |v92|, v96, |v92|
	v_fma_f32 v101, |v97|, v101, |v97|
	s_cmp_eq_u64 s[72:73], exec
	s_cbranch_scc1 .Lgsk_g1_13
	v_fma_f32 v85, |v82|, v102, s50
	v_fma_f32 v90, |v87|, v102, s50
	v_fma_f32 v95, |v92|, v102, s50
	v_fma_f32 v100, |v97|, v102, s50
	v_fma_f32 v85, |v82|, v85, s51
	v_fma_f32 v90, |v87|, v90, s51
	v_fma_f32 v95, |v92|, v95, s51
	v_fma_f32 v100, |v97|, v100, s51
	v_fma_f32 v85, |v82|, v85, s52
	v_fma_f32 v90, |v87|, v90, s52
	v_fma_f32 v95, |v92|, v95, s52
	v_fma_f32 v100, |v97|, v100, s52
	v_fma_f32 v85, |v82|, v85, s53
	v_fma_f32 v90, |v87|, v90, s53
	v_fma_f32 v95, |v92|, v95, s53
	v_fma_f32 v100, |v97|, v100, s53
	v_fma_f32 v85, |v82|, v85, s54
	v_fma_f32 v90, |v87|, v90, s54
	v_fma_f32 v95, |v92|, v95, s54
	v_fma_f32 v100, |v97|, v100, s54
	v_fma_f32 v85, |v82|, v85, s55
	v_fma_f32 v90, |v87|, v90, s55
	v_fma_f32 v95, |v92|, v95, s55
	v_fma_f32 v100, |v97|, v100, s55
	v_fma_f32 v85, |v82|, v85, |v82|
	v_fma_f32 v90, |v87|, v90, |v87|
	v_fma_f32 v95, |v92|, v95, |v92|
	v_fma_f32 v100, |v97|, v100, |v97|
	v_mul_f32_e32 v85, 0xbfb8aa3b, v85
	v_mul_f32_e32 v90, 0xbfb8aa3b, v90
	v_mul_f32_e32 v95, 0xbfb8aa3b, v95
	v_mul_f32_e32 v100, 0xbfb8aa3b, v100
	v_exp_f32_e32 v85, v85
	v_exp_f32_e32 v90, v90
	v_exp_f32_e32 v95, v95
	v_exp_f32_e32 v100, v100
	s_nop 0
	v_sub_f32_e32 v85, 1.0, v85
	v_sub_f32_e32 v90, 1.0, v90
	v_sub_f32_e32 v95, 1.0, v95
	v_sub_f32_e32 v100, 1.0, v100
	v_cndmask_b32_e64 v86, v85, v86, s[64:65]
	v_cndmask_b32_e64 v91, v90, v91, s[66:67]
	v_cndmask_b32_e64 v96, v95, v96, s[68:69]
	v_cndmask_b32_e64 v101, v100, v101, s[70:71]
.Lgsk_g1_13:
	v_fma_f32 v83, |v83|, v86, v83
	v_fma_f32 v88, |v88|, v91, v88
	v_fma_f32 v93, |v93|, v96, v93
	v_fma_f32 v98, |v98|, v101, v98
	v_cvt_f16_f32_e32 v82, v83
	v_cvt_f16_f32_e32 v87, v88
	v_cvt_f16_f32_e32 v92, v93
	v_cvt_f16_f32_e32 v97, v98
	ds_write_b16 v71, v82 offset:2336
	ds_write_b16 v71, v87 offset:2480
	ds_write_b16 v71, v92 offset:2624
	ds_write_b16 v71, v97 offset:2768
	v_fma_f32 v82, v6, s61, v138
	v_fma_f32 v87, v7, s61, v138
	v_fma_f32 v92, v8, s61, v138
	v_fma_f32 v97, v9, s61, v138
	v_fma_f32 v83, v6, s62, v142
	v_fma_f32 v88, v7, s62, v142
	v_fma_f32 v93, v8, s62, v142
	v_fma_f32 v98, v9, s62, v142
	v_mul_f32_e32 v84, v82, v82
	v_mul_f32_e32 v89, v87, v87
	v_mul_f32_e32 v94, v92, v92
	v_mul_f32_e32 v99, v97, v97
	v_cmp_lt_f32_e64 s[64:65], |v82|, 1.0
	v_cmp_lt_f32_e64 s[66:67], |v87|, 1.0
	v_cmp_lt_f32_e64 s[68:69], |v92|, 1.0
	v_cmp_lt_f32_e64 s[70:71], |v97|, 1.0
	v_fma_f32 v86, v84, v103, s56
	v_fma_f32 v91, v89, v103, s56
	v_fma_f32 v96, v94, v103, s56
	v_fma_f32 v101, v99, v103, s56
	s_and_b64 s[72:73], s[64:65], s[66:67]
	s_and_b64 s[74:75], s[68:69], s[70:71]
	s_and_b64 s[72:73], s[72:73], s[74:75]
	v_fma_f32 v86, v84, v86, s57
	v_fma_f32 v91, v89, v91, s57
	v_fma_f32 v96, v94, v96, s57
	v_fma_f32 v101, v99, v101, s57
	v_fma_f32 v86, v84, v86, s58
	v_fma_f32 v91, v89, v91, s58
	v_fma_f32 v96, v94, v96, s58
	v_fma_f32 v101, v99, v101, s58
	v_fma_f32 v86, v84, v86, s59
	v_fma_f32 v91, v89, v91, s59
	v_fma_f32 v96, v94, v96, s59
	v_fma_f32 v101, v99, v101, s59
	v_fma_f32 v86, v84, v86, s60
	v_fma_f32 v91, v89, v91, s60
	v_fma_f32 v96, v94, v96, s60
	v_fma_f32 v101, v99, v101, s60
	v_fma_f32 v86, |v82|, v86, |v82|
	v_fma_f32 v91, |v87|, v91, |v87|
	v_fma_f32 v96, |v92|, v96, |v92|
	v_fma_f32 v101, |v97|, v101, |v97|
	s_cmp_eq_u64 s[72:73], exec
	s_cbranch_scc1 .Lgsk_g1_14
	v_fma_f32 v85, |v82|, v102, s50
	v_fma_f32 v90, |v87|, v102, s50
	v_fma_f32 v95, |v92|, v102, s50
	v_fma_f32 v100, |v97|, v102, s50
	v_fma_f32 v85, |v82|, v85, s51
	v_fma_f32 v90, |v87|, v90, s51
	v_fma_f32 v95, |v92|, v95, s51
	v_fma_f32 v100, |v97|, v100, s51
	v_fma_f32 v85, |v82|, v85, s52
	v_fma_f32 v90, |v87|, v90, s52
	v_fma_f32 v95, |v92|, v95, s52
	v_fma_f32 v100, |v97|, v100, s52
	v_fma_f32 v85, |v82|, v85, s53
	v_fma_f32 v90, |v87|, v90, s53
	v_fma_f32 v95, |v92|, v95, s53
	v_fma_f32 v100, |v97|, v100, s53
	v_fma_f32 v85, |v82|, v85, s54
	v_fma_f32 v90, |v87|, v90, s54
	v_fma_f32 v95, |v92|, v95, s54
	v_fma_f32 v100, |v97|, v100, s54
	v_fma_f32 v85, |v82|, v85, s55
	v_fma_f32 v90, |v87|, v90, s55
	v_fma_f32 v95, |v92|, v95, s55
	v_fma_f32 v100, |v97|, v100, s55
	v_fma_f32 v85, |v82|, v85, |v82|
	v_fma_f32 v90, |v87|, v90, |v87|
	v_fma_f32 v95, |v92|, v95, |v92|
	v_fma_f32 v100, |v97|, v100, |v97|
	v_mul_f32_e32 v85, 0xbfb8aa3b, v85
	v_mul_f32_e32 v90, 0xbfb8aa3b, v90
	v_mul_f32_e32 v95, 0xbfb8aa3b, v95
	v_mul_f32_e32 v100, 0xbfb8aa3b, v100
	v_exp_f32_e32 v85, v85
	v_exp_f32_e32 v90, v90
	v_exp_f32_e32 v95, v95
	v_exp_f32_e32 v100, v100
	s_nop 0
	v_sub_f32_e32 v85, 1.0, v85
	v_sub_f32_e32 v90, 1.0, v90
	v_sub_f32_e32 v95, 1.0, v95
	v_sub_f32_e32 v100, 1.0, v100
	v_cndmask_b32_e64 v86, v85, v86, s[64:65]
	v_cndmask_b32_e64 v91, v90, v91, s[66:67]
	v_cndmask_b32_e64 v96, v95, v96, s[68:69]
	v_cndmask_b32_e64 v101, v100, v101, s[70:71]
.Lgsk_g1_14:
	v_fma_f32 v83, |v83|, v86, v83
	v_fma_f32 v88, |v88|, v91, v88
	v_fma_f32 v93, |v93|, v96, v93
	v_fma_f32 v98, |v98|, v101, v98
	v_cvt_f16_f32_e32 v82, v83
	v_cvt_f16_f32_e32 v87, v88
	v_cvt_f16_f32_e32 v92, v93
	v_cvt_f16_f32_e32 v97, v98
	ds_write_b16 v71, v82 offset:2368
	ds_write_b16 v71, v87 offset:2512
	ds_write_b16 v71, v92 offset:2656
	ds_write_b16 v71, v97 offset:2800
	v_fma_f32 v82, v2, s61, v139
	v_fma_f32 v87, v3, s61, v139
	v_fma_f32 v92, v4, s61, v139
	v_fma_f32 v97, v5, s61, v139
	v_fma_f32 v83, v2, s62, v143
	v_fma_f32 v88, v3, s62, v143
	v_fma_f32 v93, v4, s62, v143
	v_fma_f32 v98, v5, s62, v143
	v_mul_f32_e32 v84, v82, v82
	v_mul_f32_e32 v89, v87, v87
	v_mul_f32_e32 v94, v92, v92
	v_mul_f32_e32 v99, v97, v97
	v_cmp_lt_f32_e64 s[64:65], |v82|, 1.0
	v_cmp_lt_f32_e64 s[66:67], |v87|, 1.0
	v_cmp_lt_f32_e64 s[68:69], |v92|, 1.0
	v_cmp_lt_f32_e64 s[70:71], |v97|, 1.0
	v_fma_f32 v86, v84, v103, s56
	v_fma_f32 v91, v89, v103, s56
	v_fma_f32 v96, v94, v103, s56
	v_fma_f32 v101, v99, v103, s56
	s_and_b64 s[72:73], s[64:65], s[66:67]
	s_and_b64 s[74:75], s[68:69], s[70:71]
	s_and_b64 s[72:73], s[72:73], s[74:75]
	v_fma_f32 v86, v84, v86, s57
	v_fma_f32 v91, v89, v91, s57
	v_fma_f32 v96, v94, v96, s57
	v_fma_f32 v101, v99, v101, s57
	v_fma_f32 v86, v84, v86, s58
	v_fma_f32 v91, v89, v91, s58
	v_fma_f32 v96, v94, v96, s58
	v_fma_f32 v101, v99, v101, s58
	v_fma_f32 v86, v84, v86, s59
	v_fma_f32 v91, v89, v91, s59
	v_fma_f32 v96, v94, v96, s59
	v_fma_f32 v101, v99, v101, s59
	v_fma_f32 v86, v84, v86, s60
	v_fma_f32 v91, v89, v91, s60
	v_fma_f32 v96, v94, v96, s60
	v_fma_f32 v101, v99, v101, s60
	v_fma_f32 v86, |v82|, v86, |v82|
	v_fma_f32 v91, |v87|, v91, |v87|
	v_fma_f32 v96, |v92|, v96, |v92|
	v_fma_f32 v101, |v97|, v101, |v97|
	s_cmp_eq_u64 s[72:73], exec
	s_cbranch_scc1 .Lgsk_g1_15
	v_fma_f32 v85, |v82|, v102, s50
	v_fma_f32 v90, |v87|, v102, s50
	v_fma_f32 v95, |v92|, v102, s50
	v_fma_f32 v100, |v97|, v102, s50
	v_fma_f32 v85, |v82|, v85, s51
	v_fma_f32 v90, |v87|, v90, s51
	v_fma_f32 v95, |v92|, v95, s51
	v_fma_f32 v100, |v97|, v100, s51
	v_fma_f32 v85, |v82|, v85, s52
	v_fma_f32 v90, |v87|, v90, s52
	v_fma_f32 v95, |v92|, v95, s52
	v_fma_f32 v100, |v97|, v100, s52
	v_fma_f32 v85, |v82|, v85, s53
	v_fma_f32 v90, |v87|, v90, s53
	v_fma_f32 v95, |v92|, v95, s53
	v_fma_f32 v100, |v97|, v100, s53
	v_fma_f32 v85, |v82|, v85, s54
	v_fma_f32 v90, |v87|, v90, s54
	v_fma_f32 v95, |v92|, v95, s54
	v_fma_f32 v100, |v97|, v100, s54
	v_fma_f32 v85, |v82|, v85, s55
	v_fma_f32 v90, |v87|, v90, s55
	v_fma_f32 v95, |v92|, v95, s55
	v_fma_f32 v100, |v97|, v100, s55
	v_fma_f32 v85, |v82|, v85, |v82|
	v_fma_f32 v90, |v87|, v90, |v87|
	v_fma_f32 v95, |v92|, v95, |v92|
	v_fma_f32 v100, |v97|, v100, |v97|
	v_mul_f32_e32 v85, 0xbfb8aa3b, v85
	v_mul_f32_e32 v90, 0xbfb8aa3b, v90
	v_mul_f32_e32 v95, 0xbfb8aa3b, v95
	v_mul_f32_e32 v100, 0xbfb8aa3b, v100
	v_exp_f32_e32 v85, v85
	v_exp_f32_e32 v90, v90
	v_exp_f32_e32 v95, v95
	v_exp_f32_e32 v100, v100
	s_nop 0
	v_sub_f32_e32 v85, 1.0, v85
	v_sub_f32_e32 v90, 1.0, v90
	v_sub_f32_e32 v95, 1.0, v95
	v_sub_f32_e32 v100, 1.0, v100
	v_cndmask_b32_e64 v86, v85, v86, s[64:65]
	v_cndmask_b32_e64 v91, v90, v91, s[66:67]
	v_cndmask_b32_e64 v96, v95, v96, s[68:69]
	v_cndmask_b32_e64 v101, v100, v101, s[70:71]
.Lgsk_g1_15:
	v_fma_f32 v83, |v83|, v86, v83
	v_fma_f32 v88, |v88|, v91, v88
	v_fma_f32 v93, |v93|, v96, v93
	v_fma_f32 v98, |v98|, v101, v98
	v_cvt_f16_f32_e32 v82, v83
	v_cvt_f16_f32_e32 v87, v88
	v_cvt_f16_f32_e32 v92, v93
	v_cvt_f16_f32_e32 v97, v98
	ds_write_b16 v71, v82 offset:2400
	ds_write_b16 v71, v87 offset:2544
	ds_write_b16 v71, v92 offset:2688
	ds_write_b16 v71, v97 offset:2832
	ds_read_b128 v[104:107], v74
	ds_read_b128 v[108:111], v74 offset:1152
	ds_read_b128 v[112:115], v74 offset:2304
	ds_read_b128 v[116:119], v74 offset:3456
	s_waitcnt lgkmcnt(0)
	s_sub_i32 s2, s42, 32
	v_cmp_gt_i32_e32 vcc, s2, v75
	s_and_saveexec_b64 s[44:45], vcc
	s_add_u32 s2, s38, 0x20000
	s_addc_u32 s3, s39, 0
	global_store_dwordx4 v76, v[104:107], s[2:3]
	s_mov_b64 exec, s[44:45]
	s_sub_i32 s2, s42, 40
	v_cmp_gt_i32_e32 vcc, s2, v75
	s_and_saveexec_b64 s[44:45], vcc
	s_add_u32 s2, s38, 0x28000
	s_addc_u32 s3, s39, 0
	global_store_dwordx4 v76, v[108:111], s[2:3]
	s_mov_b64 exec, s[44:45]
	s_sub_i32 s2, s42, 48
	v_cmp_gt_i32_e32 vcc, s2, v75
	s_and_saveexec_b64 s[44:45], vcc
	s_add_u32 s2, s38, 0x30000
	s_addc_u32 s3, s39, 0
	global_store_dwordx4 v76, v[112:115], s[2:3]
	s_mov_b64 exec, s[44:45]
	s_sub_i32 s2, s42, 56
	v_cmp_gt_i32_e32 vcc, s2, v75
	s_and_saveexec_b64 s[44:45], vcc
	s_add_u32 s2, s38, 0x38000
	s_addc_u32 s3, s39, 0
	global_store_dwordx4 v76, v[116:119], s[2:3]
	s_mov_b64 exec, s[44:45]
	s_endpgm
